# v30 + G1 full-drain wait moved to first consumer + scan and_or fusion + static setprio 1 for waves 0-3
# speedup vs baseline: 1.0155x; 1.0121x over previous
.LBB1_6:
	s_or_b64 exec, exec, s[4:5]
	v_mov_b32_e32 v6, 0x18010
	v_mov_b32_e32 v2, 0x18000
	s_waitcnt lgkmcnt(0)
	s_barrier
	s_waitcnt vmcnt(8)
	ds_read_b128 v[2:5], v2
	ds_read_b128 v[6:9], v6
	s_load_dwordx4 s[36:39], s[0:1], 0x20
	s_movk_i32 s0, 0x2000
	v_lshrrev_b32_e32 v125, 4, v131
	s_waitcnt lgkmcnt(0)
	v_mov_b32_e32 v14, v2
	v_mov_b32_e32 v15, v6
	v_mov_b32_e32 v6, v3
	v_pk_add_f32 v[2:3], v[14:15], v[6:7]
	v_mov_b32_e32 v6, v4
	v_mov_b32_e32 v7, v8
	v_mov_b32_e32 v8, v5
	v_pk_add_f32 v[4:5], v[6:7], v[8:9]
	v_mov_b32_e32 v14, 0x18060
	v_pk_add_f32 v[2:3], v[2:3], v[4:5]
	v_add_co_u32_e32 v42, vcc, s0, v82
	v_add_f32_e32 v2, v2, v3
	v_mul_f32_e32 v132, 0x3a800000, v2
	v_and_b32_e32 v107, 15, v0
	v_mov_b32_e32 v2, 0x18020
	v_mov_b32_e32 v3, 0x18030
	v_lshl_add_u32 v13, v13, 2, v14
	v_pk_add_f32 v[10:11], v[10:11], v[132:133] op_sel_hi:[1,0] neg_lo:[0,1] neg_hi:[0,1]
	v_lshlrev_b32_e32 v85, 13, v1
	v_xor_b32_e32 v114, v125, v0
	v_addc_co_u32_e32 v43, vcc, 0, v83, vcc
	s_movk_i32 s0, 0x3000
	ds_read_b128 v[6:9], v2
	ds_read_b128 v[2:5], v3
	ds_write_b64 v13, v[10:11]
	v_lshl_or_b32 v84, v107, 9, v85
	v_lshlrev_b32_e32 v10, 4, v114
	s_movk_i32 s41, 0xf0
	v_add_co_u32_e32 v44, vcc, s0, v82
	v_lshlrev_b32_e32 v130, 2, v12
	v_and_or_b32 v115, v10, s41, v84
	v_addc_co_u32_e32 v45, vcc, 0, v83, vcc
	global_load_dwordx4 v[34:37], v[42:43], off offset:1024 nt
	global_load_dwordx4 v[30:33], v[42:43], off offset:2048 nt
	global_load_dwordx4 v[26:29], v[42:43], off offset:3072 nt
	global_load_dwordx4 v[38:41], v[44:45], off offset:-4096 nt
	global_load_dwordx4 v[22:25], v[44:45], off nt
	global_load_dwordx4 v[18:21], v[44:45], off offset:1024 nt
	global_load_dwordx4 v[14:17], v[44:45], off offset:2048 nt
	global_load_dwordx4 v[10:13], v[44:45], off offset:3072 nt
	s_waitcnt vmcnt(15)
	v_add_f32_e32 v42, v78, v79
	v_add_f32_e32 v43, v80, v81
	v_add_f32_e32 v42, v42, v43
	s_waitcnt vmcnt(14)
	v_add_f32_e32 v43, v74, v75
	v_add_f32_e32 v44, v76, v77
	v_add_f32_e32 v43, v43, v44
	s_waitcnt vmcnt(13)
	v_add_f32_e32 v44, v70, v71
	v_add_f32_e32 v45, v72, v73
	v_add_f32_e32 v44, v44, v45
	s_waitcnt vmcnt(12)
	v_add_f32_e32 v45, v66, v67
	v_add_f32_e32 v49, v68, v69
	v_add_f32_e32 v45, v45, v49
	s_waitcnt vmcnt(11)
	v_add_f32_e32 v49, v62, v63
	v_add_f32_e32 v86, v64, v65
	v_and_b32_e32 v46, 1, v0
	v_add_f32_e32 v49, v49, v86
	s_waitcnt vmcnt(10)
	v_add_f32_e32 v86, v58, v59
	v_add_f32_e32 v88, v60, v61
	v_add_f32_e32 v86, v86, v88
	s_waitcnt vmcnt(9)
	v_add_f32_e32 v88, v54, v55
	v_add_f32_e32 v89, v56, v57
	v_cmp_eq_u32_e64 s[4:5], 1, v46
	v_add_f32_e32 v88, v88, v89
	s_waitcnt vmcnt(8)
	v_add_f32_e32 v89, v50, v51
	v_add_f32_e32 v90, v52, v53
	v_cndmask_b32_e64 v46, v43, v42, s[4:5]
	v_cndmask_b32_e64 v42, v42, v43, s[4:5]
	v_cndmask_b32_e64 v43, v45, v44, s[4:5]
	v_cndmask_b32_e64 v44, v44, v45, s[4:5]
	v_add_f32_e32 v89, v89, v90
	v_cndmask_b32_e64 v45, v49, v86, s[4:5]
	v_add_f32_dpp v43, v43, v44 quad_perm:[1,0,3,2] row_mask:0xf bank_mask:0xf bound_ctrl:1
	v_cndmask_b32_e64 v44, v86, v49, s[4:5]
	v_and_b32_e32 v47, 2, v0
	v_add_f32_dpp v42, v46, v42 quad_perm:[1,0,3,2] row_mask:0xf bank_mask:0xf bound_ctrl:1
	v_add_f32_dpp v44, v44, v45 quad_perm:[1,0,3,2] row_mask:0xf bank_mask:0xf bound_ctrl:1
	v_cndmask_b32_e64 v45, v89, v88, s[4:5]
	v_cndmask_b32_e64 v46, v88, v89, s[4:5]
	v_cmp_eq_u16_e64 s[6:7], 0, v47
	v_and_b32_e32 v48, 4, v0
	v_add_f32_dpp v45, v45, v46 quad_perm:[1,0,3,2] row_mask:0xf bank_mask:0xf bound_ctrl:1
	v_cndmask_b32_e64 v46, v42, v43, s[6:7]
	v_cndmask_b32_e64 v42, v43, v42, s[6:7]
	v_cndmask_b32_e64 v43, v44, v45, s[6:7]
	v_cndmask_b32_e64 v44, v45, v44, s[6:7]
	v_add_f32_dpp v42, v46, v42 quad_perm:[2,3,0,1] row_mask:0xf bank_mask:0xf bound_ctrl:1
	v_cmp_eq_u16_e64 s[8:9], 0, v48
	v_add_f32_dpp v43, v43, v44 quad_perm:[2,3,0,1] row_mask:0xf bank_mask:0xf bound_ctrl:1
	v_lshlrev_b32_e32 v86, 3, v131
	v_cndmask_b32_e64 v44, v42, v43, s[8:9]
	v_cndmask_b32_e64 v42, v43, v42, s[8:9]
	v_mov_b32_e32 v43, v44
	v_and_b32_e32 v87, 8, v87
	v_mov_b32_e32 v116, 0x3727c5ac
	v_mov_b32_dpp v43, v43 row_shl:4 row_mask:0xf bank_mask:0x5
	v_mov_b32_e32 v117, 0x260
	v_bitop3_b32 v141, v125, v0, 4 bitop3:0x36
	v_mov_b32_dpp v43, v44 row_shr:4 row_mask:0xf bank_mask:0xa
	v_add_f32_e32 v42, v42, v43
	v_bitop3_b32 v142, v125, v0, 8 bitop3:0x36
	v_bitop3_b32 v143, v125, v0, 12 bitop3:0x36
	v_add_f32_dpp v42, v42, v42 row_ror:8 row_mask:0xf bank_mask:0xf bound_ctrl:1
	v_mov_b32_e32 v43, v42
	s_nop 1
	v_permlane16_swap_b32_e32 v42, v43
	v_add_f32_e32 v42, v42, v43
	v_mov_b32_e32 v43, v42
	s_nop 1
	v_permlane32_swap_b32_e32 v42, v43
	v_add_f32_e32 v42, v42, v43
	v_mul_f32_e32 v42, 0x3b800000, v42
	s_mov_b32 s3, 0
	v_readlane_b32 s40, v42, 0
	v_readlane_b32 s42, v42, 1
	v_readlane_b32 s44, v42, 2
	v_readlane_b32 s46, v42, 3
	v_readlane_b32 s48, v42, 4
	v_readlane_b32 s50, v42, 5
	v_readlane_b32 s34, v42, 6
	v_readlane_b32 s0, v42, 7
	v_pk_add_f32 v[90:91], v[78:79], s[40:41] op_sel_hi:[1,0] neg_lo:[0,1] neg_hi:[0,1]
	v_pk_add_f32 v[80:81], v[80:81], s[40:41] op_sel_hi:[1,0] neg_lo:[0,1] neg_hi:[0,1]
	v_and_b32_e32 v78, 0x1f0, v86
	v_pk_add_f32 v[76:77], v[76:77], s[42:43] op_sel_hi:[1,0] neg_lo:[0,1] neg_hi:[0,1]
	v_mul_f32_e32 v88, v81, v81
	v_or3_b32 v140, v85, v78, v87
	v_pk_add_f32 v[78:79], v[74:75], s[42:43] op_sel_hi:[1,0] neg_lo:[0,1] neg_hi:[0,1]
	v_mul_f32_e32 v74, v77, v77
	v_fmac_f32_e32 v88, v80, v80
	v_fmac_f32_e32 v74, v76, v76
	v_fmac_f32_e32 v88, v91, v91
	v_fmac_f32_e32 v74, v79, v79
	v_fmac_f32_e32 v88, v90, v90
	v_fmac_f32_e32 v74, v78, v78
	v_cndmask_b32_e64 v75, v74, v88, s[4:5]
	v_cndmask_b32_e64 v74, v88, v74, s[4:5]
	v_mov_b32_e32 v88, 0x1f0
	v_pk_add_f32 v[72:73], v[72:73], s[44:45] op_sel_hi:[1,0] neg_lo:[0,1] neg_hi:[0,1]
	v_add_f32_dpp v89, v75, v74 quad_perm:[1,0,3,2] row_mask:0xf bank_mask:0xf bound_ctrl:1
	v_bitop3_b32 v74, v86, 16, v88 bitop3:0x6c
	v_or3_b32 v138, v85, v74, v87
	v_pk_add_f32 v[74:75], v[70:71], s[44:45] op_sel_hi:[1,0] neg_lo:[0,1] neg_hi:[0,1]
	v_bitop3_b32 v70, v86, 32, v88 bitop3:0x6c
	v_pk_add_f32 v[68:69], v[68:69], s[46:47] op_sel_hi:[1,0] neg_lo:[0,1] neg_hi:[0,1]
	v_mul_f32_e32 v92, v73, v73
	v_or3_b32 v135, v85, v70, v87
	v_pk_add_f32 v[70:71], v[66:67], s[46:47] op_sel_hi:[1,0] neg_lo:[0,1] neg_hi:[0,1]
	v_mul_f32_e32 v66, v69, v69
	v_fmac_f32_e32 v92, v72, v72
	v_fmac_f32_e32 v66, v68, v68
	v_fmac_f32_e32 v92, v75, v75
	v_fmac_f32_e32 v66, v71, v71
	v_fmac_f32_e32 v92, v74, v74
	v_fmac_f32_e32 v66, v70, v70
	v_cndmask_b32_e64 v67, v66, v92, s[4:5]
	v_cndmask_b32_e64 v66, v92, v66, s[4:5]
	v_pk_add_f32 v[64:65], v[64:65], s[48:49] op_sel_hi:[1,0] neg_lo:[0,1] neg_hi:[0,1]
	v_pk_add_f32 v[60:61], v[60:61], s[50:51] op_sel_hi:[1,0] neg_lo:[0,1] neg_hi:[0,1]
	v_add_f32_dpp v66, v67, v66 quad_perm:[1,0,3,2] row_mask:0xf bank_mask:0xf bound_ctrl:1
	v_cndmask_b32_e64 v67, v89, v66, s[6:7]
	v_cndmask_b32_e64 v66, v66, v89, s[6:7]
	v_mul_f32_e32 v92, v65, v65
	v_fmac_f32_e32 v92, v64, v64
	v_add_f32_dpp v89, v67, v66 quad_perm:[2,3,0,1] row_mask:0xf bank_mask:0xf bound_ctrl:1
	v_bitop3_b32 v66, v86, 48, v88 bitop3:0x6c
	v_or3_b32 v134, v85, v66, v87
	v_pk_add_f32 v[66:67], v[62:63], s[48:49] op_sel_hi:[1,0] neg_lo:[0,1] neg_hi:[0,1]
	v_bitop3_b32 v62, v86, 64, v88 bitop3:0x6c
	v_or3_b32 v120, v85, v62, v87
	v_pk_add_f32 v[62:63], v[58:59], s[50:51] op_sel_hi:[1,0] neg_lo:[0,1] neg_hi:[0,1]
	v_mul_f32_e32 v58, v61, v61
	v_fmac_f32_e32 v58, v60, v60
	v_fmac_f32_e32 v92, v67, v67
	v_fmac_f32_e32 v58, v63, v63
	v_fmac_f32_e32 v92, v66, v66
	v_fmac_f32_e32 v58, v62, v62
	v_cndmask_b32_e64 v59, v58, v92, s[4:5]
	v_cndmask_b32_e64 v58, v92, v58, s[4:5]
	v_pk_add_f32 v[56:57], v[56:57], s[34:35] op_sel_hi:[1,0] neg_lo:[0,1] neg_hi:[0,1]
	s_mov_b32 s25, 0x3e6d3387
	v_add_f32_dpp v92, v59, v58 quad_perm:[1,0,3,2] row_mask:0xf bank_mask:0xf bound_ctrl:1
	v_pk_add_f32 v[58:59], v[54:55], s[34:35] op_sel_hi:[1,0] neg_lo:[0,1] neg_hi:[0,1]
	v_pk_add_f32 v[54:55], v[50:51], s[0:1] op_sel_hi:[1,0] neg_lo:[0,1] neg_hi:[0,1]
	v_pk_add_f32 v[50:51], v[52:53], s[0:1] op_sel_hi:[1,0] neg_lo:[0,1] neg_hi:[0,1]
	v_mul_f32_e32 v93, v57, v57
	v_mul_f32_e32 v52, v51, v51
	v_fmac_f32_e32 v93, v56, v56
	v_fmac_f32_e32 v52, v50, v50
	v_fmac_f32_e32 v93, v59, v59
	v_fmac_f32_e32 v52, v55, v55
	v_fmac_f32_e32 v93, v58, v58
	v_fmac_f32_e32 v52, v54, v54
	v_cndmask_b32_e64 v53, v52, v93, s[4:5]
	v_cndmask_b32_e64 v52, v93, v52, s[4:5]
	s_mov_b32 s35, 0xf800000
	s_movk_i32 s0, 0x50
	v_add_f32_dpp v52, v53, v52 quad_perm:[1,0,3,2] row_mask:0xf bank_mask:0xf bound_ctrl:1
	v_cndmask_b32_e64 v53, v92, v52, s[6:7]
	v_cndmask_b32_e64 v52, v52, v92, s[6:7]
	s_mov_b32 s24, 0xbf3a00e3
	s_mov_b32 s22, 0x3f07dc22
	v_add_f32_dpp v52, v53, v52 quad_perm:[2,3,0,1] row_mask:0xf bank_mask:0xf bound_ctrl:1
	v_cndmask_b32_e64 v53, v89, v52, s[8:9]
	v_cndmask_b32_e64 v52, v52, v89, s[8:9]
	v_mov_b32_e32 v89, v53
	s_mov_b32 s34, 0xbe11a98e
	s_mov_b32 s40, 0x3e027906
	v_mov_b32_dpp v89, v89 row_shl:4 row_mask:0xf bank_mask:0x5
	s_mov_b32 s33, 5
	s_nop 0
	v_mov_b32_dpp v89, v53 row_shr:4 row_mask:0xf bank_mask:0xa
	v_add_f32_e32 v52, v52, v89
	v_bitop3_b32 v89, v86, s0, v88 bitop3:0x6c
	v_or3_b32 v121, v85, v89, v87
	v_add_f32_dpp v52, v52, v52 row_ror:8 row_mask:0xf bank_mask:0xf bound_ctrl:1
	v_mov_b32_e32 v53, v52
	s_nop 1
	v_permlane16_swap_b32_e32 v52, v53
	v_add_f32_e32 v52, v52, v53
	v_mov_b32_e32 v53, v52
	s_nop 1
	v_permlane32_swap_b32_e32 v52, v53
	v_add_f32_e32 v52, v52, v53
	v_fmamk_f32 v52, v52, 0x3b800000, v116
	v_mul_f32_e32 v53, 0x4f800000, v52
	v_cmp_gt_f32_e32 vcc, s35, v52
	s_nop 1
	v_cndmask_b32_e32 v52, v52, v53, vcc
	v_sqrt_f32_e32 v53, v52
	s_nop 0
	v_add_u32_e32 v89, -1, v53
	v_fma_f32 v92, -v89, v53, v52
	v_cmp_ge_f32_e64 s[0:1], 0, v92
	v_add_u32_e32 v92, 1, v53
	s_nop 0
	v_cndmask_b32_e64 v89, v53, v89, s[0:1]
	v_fma_f32 v53, -v92, v53, v52
	v_cmp_lt_f32_e64 s[0:1], 0, v53
	s_nop 1
	v_cndmask_b32_e64 v53, v89, v92, s[0:1]
	v_mul_f32_e32 v89, 0x37800000, v53
	v_cndmask_b32_e32 v53, v53, v89, vcc
	v_cmp_class_f32_e32 vcc, v52, v117
	s_nop 1
	v_cndmask_b32_e32 v52, v53, v52, vcc
	v_div_scale_f32 v53, s[0:1], v52, v52, 1.0
	v_rcp_f32_e32 v89, v53
	s_movk_i32 s0, 0x60
	v_bitop3_b32 v92, v86, s0, v88 bitop3:0x6c
	v_or3_b32 v118, v85, v92, v87
	v_fma_f32 v92, -v53, v89, 1.0
	v_fmac_f32_e32 v89, v92, v89
	v_div_scale_f32 v92, vcc, 1.0, v52, 1.0
	v_mul_f32_e32 v93, v92, v89
	v_fma_f32 v94, -v53, v93, v92
	v_fmac_f32_e32 v93, v94, v89
	v_fma_f32 v53, -v53, v93, v92
	v_div_fmas_f32 v53, v53, v89, v93
	v_div_fixup_f32 v52, v53, v52, 1.0
	s_waitcnt vmcnt(4)
	v_add_f32_e32 v89, v38, v39
	v_readlane_b32 s0, v52, 0
	s_nop 1
	v_pk_mul_f32 v[90:91], s[0:1], v[90:91] op_sel_hi:[0,1]
	v_pk_fma_f32 v[92:93], v[90:91], v[238:239], v[242:243]
	v_mov_b64_e32 v[90:91], s[24:25]
	v_fma_f32 v53, |v92|, s25, 1.0
	v_pk_mul_f32 v[98:99], v[92:93], v[92:93]
	v_rcp_f32_e32 v96, v53
	v_mul_f32_e32 v53, 0xbf38aa3b, v98
	v_exp_f32_e32 v98, v53
	v_fma_f32 v53, |v93|, s25, 1.0
	v_rcp_f32_e32 v97, v53
	s_mov_b32 s24, 0x3f35f0e3
	v_pk_mul_f32 v[80:81], s[0:1], v[80:81] op_sel_hi:[0,1]
	v_mul_f32_e32 v53, 0xbf38aa3b, v99
	v_pk_fma_f32 v[100:101], v[96:97], s[22:23], v[90:91] op_sel_hi:[1,0,0]
	v_pk_fma_f32 v[80:81], v[80:81], v[240:241], v[244:245]
	v_pk_fma_f32 v[100:101], v[96:97], v[100:101], s[24:25] op_sel_hi:[1,1,0]
	v_and_b32_e32 v95, 0x7fffffff, v93
	v_pk_fma_f32 v[100:101], v[96:97], v[100:101], s[34:35] op_sel_hi:[1,1,0]
	v_and_b32_e32 v94, 0x7fffffff, v92
	v_pk_fma_f32 v[100:101], v[96:97], v[100:101], s[40:41] op_sel_hi:[1,1,0]
	v_exp_f32_e32 v99, v53
	v_pk_mul_f32 v[96:97], v[96:97], v[100:101]
	v_fma_f32 v53, |v80|, s25, 1.0
	v_pk_mul_f32 v[94:95], v[94:95], v[96:97]
	v_rcp_f32_e32 v96, v53
	v_fma_f32 v53, |v81|, s25, 1.0
	v_rcp_f32_e32 v97, v53
	v_max_f32_e32 v92, 0, v92
	v_max_f32_e32 v93, 0, v93
	v_pk_fma_f32 v[92:93], v[98:99], v[94:95], v[92:93] neg_lo:[1,0,0] neg_hi:[1,0,0]
	v_pk_mul_f32 v[98:99], v[80:81], v[80:81]
	v_pk_fma_f32 v[100:101], v[96:97], s[22:23], v[90:91] op_sel_hi:[1,0,0]
	v_mul_f32_e32 v53, 0xbf38aa3b, v98
	v_exp_f32_e32 v98, v53
	v_pk_fma_f32 v[100:101], v[96:97], v[100:101], s[24:25] op_sel_hi:[1,1,0]
	v_mul_f32_e32 v53, 0xbf38aa3b, v99
	v_pk_fma_f32 v[100:101], v[96:97], v[100:101], s[34:35] op_sel_hi:[1,1,0]
	v_exp_f32_e32 v99, v53
	v_pk_fma_f32 v[100:101], v[96:97], v[100:101], s[40:41] op_sel_hi:[1,1,0]
	v_and_b32_e32 v95, 0x7fffffff, v81
	v_and_b32_e32 v94, 0x7fffffff, v80
	v_pk_mul_f32 v[96:97], v[96:97], v[100:101]
	v_readlane_b32 s0, v52, 1
	v_max_f32_e32 v80, 0, v80
	v_max_f32_e32 v81, 0, v81
	v_pk_mul_f32 v[94:95], v[94:95], v[96:97]
	v_pk_mul_f32 v[78:79], s[0:1], v[78:79] op_sel_hi:[0,1]
	v_pk_fma_f32 v[80:81], v[98:99], v[94:95], v[80:81] neg_lo:[1,0,0] neg_hi:[1,0,0]
	v_pk_fma_f32 v[78:79], v[78:79], v[238:239], v[242:243]
	v_cvt_pk_f16_f32 v92, v92, v93
	v_cvt_pk_f16_f32 v93, v80, v81
	v_fma_f32 v53, |v78|, s25, 1.0
	ds_write_b64 v140, v[92:93] offset:32768
	v_rcp_f32_e32 v92, v53
	v_fma_f32 v53, |v79|, s25, 1.0
	v_rcp_f32_e32 v93, v53
	v_pk_mul_f32 v[94:95], v[78:79], v[78:79]
	v_pk_mul_f32 v[76:77], s[0:1], v[76:77] op_sel_hi:[0,1]
	v_mul_f32_e32 v53, 0xbf38aa3b, v94
	v_pk_fma_f32 v[96:97], v[92:93], s[22:23], v[90:91] op_sel_hi:[1,0,0]
	v_exp_f32_e32 v94, v53
	v_pk_fma_f32 v[96:97], v[92:93], v[96:97], s[24:25] op_sel_hi:[1,1,0]
	v_mul_f32_e32 v53, 0xbf38aa3b, v95
	v_pk_fma_f32 v[96:97], v[92:93], v[96:97], s[34:35] op_sel_hi:[1,1,0]
	v_pk_fma_f32 v[76:77], v[76:77], v[240:241], v[244:245]
	v_pk_fma_f32 v[96:97], v[92:93], v[96:97], s[40:41] op_sel_hi:[1,1,0]
	v_and_b32_e32 v81, 0x7fffffff, v79
	v_and_b32_e32 v80, 0x7fffffff, v78
	v_exp_f32_e32 v95, v53
	v_pk_mul_f32 v[92:93], v[92:93], v[96:97]
	v_fma_f32 v53, |v76|, s25, 1.0
	v_pk_mul_f32 v[80:81], v[80:81], v[92:93]
	v_rcp_f32_e32 v92, v53
	v_fma_f32 v53, |v77|, s25, 1.0
	v_rcp_f32_e32 v93, v53
	v_max_f32_e32 v78, 0, v78
	v_max_f32_e32 v79, 0, v79
	v_pk_fma_f32 v[78:79], v[94:95], v[80:81], v[78:79] neg_lo:[1,0,0] neg_hi:[1,0,0]
	v_pk_mul_f32 v[94:95], v[76:77], v[76:77]
	v_pk_fma_f32 v[96:97], v[92:93], s[22:23], v[90:91] op_sel_hi:[1,0,0]
	v_mul_f32_e32 v53, 0xbf38aa3b, v94
	v_exp_f32_e32 v94, v53
	v_pk_fma_f32 v[96:97], v[92:93], v[96:97], s[24:25] op_sel_hi:[1,1,0]
	v_mul_f32_e32 v53, 0xbf38aa3b, v95
	v_pk_fma_f32 v[96:97], v[92:93], v[96:97], s[34:35] op_sel_hi:[1,1,0]
	v_exp_f32_e32 v95, v53
	v_pk_fma_f32 v[96:97], v[92:93], v[96:97], s[40:41] op_sel_hi:[1,1,0]
	v_and_b32_e32 v81, 0x7fffffff, v77
	v_and_b32_e32 v80, 0x7fffffff, v76
	v_pk_mul_f32 v[92:93], v[92:93], v[96:97]
	v_readlane_b32 s0, v52, 2
	v_max_f32_e32 v76, 0, v76
	v_max_f32_e32 v77, 0, v77
	v_pk_mul_f32 v[80:81], v[80:81], v[92:93]
	v_pk_mul_f32 v[74:75], s[0:1], v[74:75] op_sel_hi:[0,1]
	v_pk_fma_f32 v[76:77], v[94:95], v[80:81], v[76:77] neg_lo:[1,0,0] neg_hi:[1,0,0]
	v_pk_fma_f32 v[74:75], v[74:75], v[238:239], v[242:243]
	v_cvt_pk_f16_f32 v78, v78, v79
	v_cvt_pk_f16_f32 v79, v76, v77
	v_fma_f32 v53, |v74|, s25, 1.0
	ds_write_b64 v138, v[78:79] offset:33280
	v_rcp_f32_e32 v78, v53
	v_fma_f32 v53, |v75|, s25, 1.0
	v_rcp_f32_e32 v79, v53
	v_pk_mul_f32 v[80:81], v[74:75], v[74:75]
	v_pk_mul_f32 v[72:73], s[0:1], v[72:73] op_sel_hi:[0,1]
	v_mul_f32_e32 v53, 0xbf38aa3b, v80
	v_pk_fma_f32 v[92:93], v[78:79], s[22:23], v[90:91] op_sel_hi:[1,0,0]
	v_exp_f32_e32 v80, v53
	v_pk_fma_f32 v[92:93], v[78:79], v[92:93], s[24:25] op_sel_hi:[1,1,0]
	v_mul_f32_e32 v53, 0xbf38aa3b, v81
	v_pk_fma_f32 v[92:93], v[78:79], v[92:93], s[34:35] op_sel_hi:[1,1,0]
	v_pk_fma_f32 v[72:73], v[72:73], v[240:241], v[244:245]
	v_pk_fma_f32 v[92:93], v[78:79], v[92:93], s[40:41] op_sel_hi:[1,1,0]
	v_and_b32_e32 v77, 0x7fffffff, v75
	v_and_b32_e32 v76, 0x7fffffff, v74
	v_exp_f32_e32 v81, v53
	v_pk_mul_f32 v[78:79], v[78:79], v[92:93]
	v_fma_f32 v53, |v72|, s25, 1.0
	v_pk_mul_f32 v[76:77], v[76:77], v[78:79]
	v_rcp_f32_e32 v78, v53
	v_fma_f32 v53, |v73|, s25, 1.0
	v_rcp_f32_e32 v79, v53
	v_max_f32_e32 v74, 0, v74
	v_max_f32_e32 v75, 0, v75
	v_pk_fma_f32 v[74:75], v[80:81], v[76:77], v[74:75] neg_lo:[1,0,0] neg_hi:[1,0,0]
	v_pk_mul_f32 v[80:81], v[72:73], v[72:73]
	v_pk_fma_f32 v[92:93], v[78:79], s[22:23], v[90:91] op_sel_hi:[1,0,0]
	v_mul_f32_e32 v53, 0xbf38aa3b, v80
	v_exp_f32_e32 v80, v53
	v_pk_fma_f32 v[92:93], v[78:79], v[92:93], s[24:25] op_sel_hi:[1,1,0]
	v_mul_f32_e32 v53, 0xbf38aa3b, v81
	v_pk_fma_f32 v[92:93], v[78:79], v[92:93], s[34:35] op_sel_hi:[1,1,0]
	v_exp_f32_e32 v81, v53
	v_pk_fma_f32 v[92:93], v[78:79], v[92:93], s[40:41] op_sel_hi:[1,1,0]
	v_and_b32_e32 v77, 0x7fffffff, v73
	v_and_b32_e32 v76, 0x7fffffff, v72
	v_pk_mul_f32 v[78:79], v[78:79], v[92:93]
	v_readlane_b32 s0, v52, 3
	v_max_f32_e32 v72, 0, v72
	v_max_f32_e32 v73, 0, v73
	v_pk_mul_f32 v[76:77], v[76:77], v[78:79]
	v_pk_mul_f32 v[70:71], s[0:1], v[70:71] op_sel_hi:[0,1]
	v_pk_fma_f32 v[72:73], v[80:81], v[76:77], v[72:73] neg_lo:[1,0,0] neg_hi:[1,0,0]
	v_pk_fma_f32 v[70:71], v[70:71], v[238:239], v[242:243]
	v_cvt_pk_f16_f32 v74, v74, v75
	v_cvt_pk_f16_f32 v75, v72, v73
	v_fma_f32 v53, |v70|, s25, 1.0
	ds_write_b64 v135, v[74:75] offset:33792
	v_rcp_f32_e32 v74, v53
	v_fma_f32 v53, |v71|, s25, 1.0
	v_rcp_f32_e32 v75, v53
	v_pk_mul_f32 v[76:77], v[70:71], v[70:71]
	v_pk_mul_f32 v[68:69], s[0:1], v[68:69] op_sel_hi:[0,1]
	v_mul_f32_e32 v53, 0xbf38aa3b, v76
	v_pk_fma_f32 v[78:79], v[74:75], s[22:23], v[90:91] op_sel_hi:[1,0,0]
	v_exp_f32_e32 v76, v53
	v_pk_fma_f32 v[78:79], v[74:75], v[78:79], s[24:25] op_sel_hi:[1,1,0]
	v_mul_f32_e32 v53, 0xbf38aa3b, v77
	v_pk_fma_f32 v[78:79], v[74:75], v[78:79], s[34:35] op_sel_hi:[1,1,0]
	v_pk_fma_f32 v[68:69], v[68:69], v[240:241], v[244:245]
	v_pk_fma_f32 v[78:79], v[74:75], v[78:79], s[40:41] op_sel_hi:[1,1,0]
	v_and_b32_e32 v73, 0x7fffffff, v71
	v_and_b32_e32 v72, 0x7fffffff, v70
	v_exp_f32_e32 v77, v53
	v_pk_mul_f32 v[74:75], v[74:75], v[78:79]
	v_fma_f32 v53, |v68|, s25, 1.0
	v_pk_mul_f32 v[72:73], v[72:73], v[74:75]
	v_rcp_f32_e32 v74, v53
	v_fma_f32 v53, |v69|, s25, 1.0
	v_rcp_f32_e32 v75, v53
	v_max_f32_e32 v70, 0, v70
	v_max_f32_e32 v71, 0, v71
	v_pk_fma_f32 v[70:71], v[76:77], v[72:73], v[70:71] neg_lo:[1,0,0] neg_hi:[1,0,0]
	v_pk_mul_f32 v[76:77], v[68:69], v[68:69]
	v_pk_fma_f32 v[78:79], v[74:75], s[22:23], v[90:91] op_sel_hi:[1,0,0]
	v_mul_f32_e32 v53, 0xbf38aa3b, v76
	v_exp_f32_e32 v76, v53
	v_pk_fma_f32 v[78:79], v[74:75], v[78:79], s[24:25] op_sel_hi:[1,1,0]
	v_mul_f32_e32 v53, 0xbf38aa3b, v77
	v_pk_fma_f32 v[78:79], v[74:75], v[78:79], s[34:35] op_sel_hi:[1,1,0]
	v_exp_f32_e32 v77, v53
	v_pk_fma_f32 v[78:79], v[74:75], v[78:79], s[40:41] op_sel_hi:[1,1,0]
	v_and_b32_e32 v73, 0x7fffffff, v69
	v_and_b32_e32 v72, 0x7fffffff, v68
	v_pk_mul_f32 v[74:75], v[74:75], v[78:79]
	v_readlane_b32 s0, v52, 4
	v_max_f32_e32 v68, 0, v68
	v_max_f32_e32 v69, 0, v69
	v_pk_mul_f32 v[72:73], v[72:73], v[74:75]
	v_pk_mul_f32 v[66:67], s[0:1], v[66:67] op_sel_hi:[0,1]
	v_pk_fma_f32 v[68:69], v[76:77], v[72:73], v[68:69] neg_lo:[1,0,0] neg_hi:[1,0,0]
	v_pk_fma_f32 v[66:67], v[66:67], v[238:239], v[242:243]
	v_cvt_pk_f16_f32 v70, v70, v71
	v_cvt_pk_f16_f32 v71, v68, v69
	v_fma_f32 v53, |v66|, s25, 1.0
	ds_write_b64 v134, v[70:71] offset:34304
	v_rcp_f32_e32 v70, v53
	v_fma_f32 v53, |v67|, s25, 1.0
	v_rcp_f32_e32 v71, v53
	v_pk_mul_f32 v[72:73], v[66:67], v[66:67]
	v_pk_mul_f32 v[64:65], s[0:1], v[64:65] op_sel_hi:[0,1]
	v_mul_f32_e32 v53, 0xbf38aa3b, v72
	v_pk_fma_f32 v[74:75], v[70:71], s[22:23], v[90:91] op_sel_hi:[1,0,0]
	v_exp_f32_e32 v72, v53
	v_pk_fma_f32 v[74:75], v[70:71], v[74:75], s[24:25] op_sel_hi:[1,1,0]
	v_mul_f32_e32 v53, 0xbf38aa3b, v73
	v_pk_fma_f32 v[74:75], v[70:71], v[74:75], s[34:35] op_sel_hi:[1,1,0]
	v_pk_fma_f32 v[64:65], v[64:65], v[240:241], v[244:245]
	v_pk_fma_f32 v[74:75], v[70:71], v[74:75], s[40:41] op_sel_hi:[1,1,0]
	v_and_b32_e32 v69, 0x7fffffff, v67
	v_and_b32_e32 v68, 0x7fffffff, v66
	v_exp_f32_e32 v73, v53
	v_pk_mul_f32 v[70:71], v[70:71], v[74:75]
	v_fma_f32 v53, |v64|, s25, 1.0
	v_pk_mul_f32 v[68:69], v[68:69], v[70:71]
	v_rcp_f32_e32 v70, v53
	v_fma_f32 v53, |v65|, s25, 1.0
	v_rcp_f32_e32 v71, v53
	v_max_f32_e32 v66, 0, v66
	v_max_f32_e32 v67, 0, v67
	v_pk_fma_f32 v[66:67], v[72:73], v[68:69], v[66:67] neg_lo:[1,0,0] neg_hi:[1,0,0]
	v_pk_mul_f32 v[72:73], v[64:65], v[64:65]
	v_pk_fma_f32 v[74:75], v[70:71], s[22:23], v[90:91] op_sel_hi:[1,0,0]
	v_mul_f32_e32 v53, 0xbf38aa3b, v72
	v_exp_f32_e32 v72, v53
	v_pk_fma_f32 v[74:75], v[70:71], v[74:75], s[24:25] op_sel_hi:[1,1,0]
	v_mul_f32_e32 v53, 0xbf38aa3b, v73
	v_pk_fma_f32 v[74:75], v[70:71], v[74:75], s[34:35] op_sel_hi:[1,1,0]
	v_exp_f32_e32 v73, v53
	v_pk_fma_f32 v[74:75], v[70:71], v[74:75], s[40:41] op_sel_hi:[1,1,0]
	v_and_b32_e32 v69, 0x7fffffff, v65
	v_and_b32_e32 v68, 0x7fffffff, v64
	v_pk_mul_f32 v[70:71], v[70:71], v[74:75]
	v_readlane_b32 s0, v52, 5
	v_max_f32_e32 v64, 0, v64
	v_max_f32_e32 v65, 0, v65
	v_pk_mul_f32 v[68:69], v[68:69], v[70:71]
	v_pk_mul_f32 v[62:63], s[0:1], v[62:63] op_sel_hi:[0,1]
	v_pk_fma_f32 v[64:65], v[72:73], v[68:69], v[64:65] neg_lo:[1,0,0] neg_hi:[1,0,0]
	v_pk_fma_f32 v[62:63], v[62:63], v[238:239], v[242:243]
	v_cvt_pk_f16_f32 v66, v66, v67
	v_cvt_pk_f16_f32 v67, v64, v65
	v_fma_f32 v53, |v62|, s25, 1.0
	ds_write_b64 v120, v[66:67] offset:34816
	v_rcp_f32_e32 v66, v53
	v_fma_f32 v53, |v63|, s25, 1.0
	v_rcp_f32_e32 v67, v53
	v_pk_mul_f32 v[68:69], v[62:63], v[62:63]
	v_pk_mul_f32 v[60:61], s[0:1], v[60:61] op_sel_hi:[0,1]
	v_mul_f32_e32 v53, 0xbf38aa3b, v68
	v_pk_fma_f32 v[70:71], v[66:67], s[22:23], v[90:91] op_sel_hi:[1,0,0]
	v_exp_f32_e32 v68, v53
	v_pk_fma_f32 v[70:71], v[66:67], v[70:71], s[24:25] op_sel_hi:[1,1,0]
	v_mul_f32_e32 v53, 0xbf38aa3b, v69
	v_pk_fma_f32 v[70:71], v[66:67], v[70:71], s[34:35] op_sel_hi:[1,1,0]
	v_pk_fma_f32 v[60:61], v[60:61], v[240:241], v[244:245]
	v_pk_fma_f32 v[70:71], v[66:67], v[70:71], s[40:41] op_sel_hi:[1,1,0]
	v_and_b32_e32 v65, 0x7fffffff, v63
	v_and_b32_e32 v64, 0x7fffffff, v62
	v_exp_f32_e32 v69, v53
	v_pk_mul_f32 v[66:67], v[66:67], v[70:71]
	v_fma_f32 v53, |v60|, s25, 1.0
	v_pk_mul_f32 v[64:65], v[64:65], v[66:67]
	v_rcp_f32_e32 v66, v53
	v_fma_f32 v53, |v61|, s25, 1.0
	v_rcp_f32_e32 v67, v53
	v_max_f32_e32 v62, 0, v62
	v_max_f32_e32 v63, 0, v63
	v_pk_fma_f32 v[62:63], v[68:69], v[64:65], v[62:63] neg_lo:[1,0,0] neg_hi:[1,0,0]
	v_pk_mul_f32 v[68:69], v[60:61], v[60:61]
	v_pk_fma_f32 v[70:71], v[66:67], s[22:23], v[90:91] op_sel_hi:[1,0,0]
	v_mul_f32_e32 v53, 0xbf38aa3b, v68
	v_exp_f32_e32 v68, v53
	v_pk_fma_f32 v[70:71], v[66:67], v[70:71], s[24:25] op_sel_hi:[1,1,0]
	v_mul_f32_e32 v53, 0xbf38aa3b, v69
	v_pk_fma_f32 v[70:71], v[66:67], v[70:71], s[34:35] op_sel_hi:[1,1,0]
	v_exp_f32_e32 v69, v53
	v_pk_fma_f32 v[70:71], v[66:67], v[70:71], s[40:41] op_sel_hi:[1,1,0]
	v_and_b32_e32 v65, 0x7fffffff, v61
	v_and_b32_e32 v64, 0x7fffffff, v60
	v_pk_mul_f32 v[66:67], v[66:67], v[70:71]
	v_readlane_b32 s0, v52, 6
	v_max_f32_e32 v60, 0, v60
	v_max_f32_e32 v61, 0, v61
	v_pk_mul_f32 v[64:65], v[64:65], v[66:67]
	v_pk_mul_f32 v[58:59], s[0:1], v[58:59] op_sel_hi:[0,1]
	v_pk_fma_f32 v[60:61], v[68:69], v[64:65], v[60:61] neg_lo:[1,0,0] neg_hi:[1,0,0]
	v_pk_fma_f32 v[58:59], v[58:59], v[238:239], v[242:243]
	v_cvt_pk_f16_f32 v62, v62, v63
	v_cvt_pk_f16_f32 v63, v60, v61
	v_fma_f32 v53, |v58|, s25, 1.0
	ds_write_b64 v121, v[62:63] offset:35328
	v_rcp_f32_e32 v62, v53
	v_fma_f32 v53, |v59|, s25, 1.0
	v_rcp_f32_e32 v63, v53
	v_pk_mul_f32 v[64:65], v[58:59], v[58:59]
	v_pk_mul_f32 v[56:57], s[0:1], v[56:57] op_sel_hi:[0,1]
	v_mul_f32_e32 v53, 0xbf38aa3b, v64
	v_pk_fma_f32 v[66:67], v[62:63], s[22:23], v[90:91] op_sel_hi:[1,0,0]
	v_exp_f32_e32 v64, v53
	v_pk_fma_f32 v[66:67], v[62:63], v[66:67], s[24:25] op_sel_hi:[1,1,0]
	v_mul_f32_e32 v53, 0xbf38aa3b, v65
	v_pk_fma_f32 v[66:67], v[62:63], v[66:67], s[34:35] op_sel_hi:[1,1,0]
	v_pk_fma_f32 v[56:57], v[56:57], v[240:241], v[244:245]
	v_pk_fma_f32 v[66:67], v[62:63], v[66:67], s[40:41] op_sel_hi:[1,1,0]
	v_and_b32_e32 v61, 0x7fffffff, v59
	v_and_b32_e32 v60, 0x7fffffff, v58
	v_exp_f32_e32 v65, v53
	v_pk_mul_f32 v[62:63], v[62:63], v[66:67]
	v_fma_f32 v53, |v56|, s25, 1.0
	v_pk_mul_f32 v[60:61], v[60:61], v[62:63]
	v_rcp_f32_e32 v62, v53
	v_fma_f32 v53, |v57|, s25, 1.0
	v_rcp_f32_e32 v63, v53
	v_max_f32_e32 v58, 0, v58
	v_max_f32_e32 v59, 0, v59
	v_pk_fma_f32 v[58:59], v[64:65], v[60:61], v[58:59] neg_lo:[1,0,0] neg_hi:[1,0,0]
	v_pk_mul_f32 v[64:65], v[56:57], v[56:57]
	v_pk_fma_f32 v[66:67], v[62:63], s[22:23], v[90:91] op_sel_hi:[1,0,0]
	v_mul_f32_e32 v53, 0xbf38aa3b, v64
	v_exp_f32_e32 v64, v53
	v_pk_fma_f32 v[66:67], v[62:63], v[66:67], s[24:25] op_sel_hi:[1,1,0]
	v_mul_f32_e32 v53, 0xbf38aa3b, v65
	v_pk_fma_f32 v[66:67], v[62:63], v[66:67], s[34:35] op_sel_hi:[1,1,0]
	v_exp_f32_e32 v65, v53
	v_pk_fma_f32 v[66:67], v[62:63], v[66:67], s[40:41] op_sel_hi:[1,1,0]
	v_and_b32_e32 v61, 0x7fffffff, v57
	v_and_b32_e32 v60, 0x7fffffff, v56
	v_pk_mul_f32 v[62:63], v[62:63], v[66:67]
	v_readlane_b32 s0, v52, 7
	v_max_f32_e32 v56, 0, v56
	v_max_f32_e32 v57, 0, v57
	v_pk_mul_f32 v[60:61], v[60:61], v[62:63]
	v_pk_mul_f32 v[52:53], s[0:1], v[54:55] op_sel_hi:[0,1]
	v_pk_fma_f32 v[56:57], v[64:65], v[60:61], v[56:57] neg_lo:[1,0,0] neg_hi:[1,0,0]
	v_pk_fma_f32 v[52:53], v[52:53], v[238:239], v[242:243]
	v_cvt_pk_f16_f32 v58, v58, v59
	v_cvt_pk_f16_f32 v59, v56, v57
	v_fma_f32 v56, |v52|, s25, 1.0
	v_fma_f32 v57, |v53|, s25, 1.0
	v_rcp_f32_e32 v56, v56
	v_rcp_f32_e32 v57, v57
	ds_write_b64 v118, v[58:59] offset:35840
	v_pk_mul_f32 v[58:59], v[52:53], v[52:53]
	v_and_b32_e32 v55, 0x7fffffff, v53
	v_pk_fma_f32 v[60:61], v[56:57], s[22:23], v[90:91] op_sel_hi:[1,0,0]
	v_mul_f32_e32 v58, 0xbf38aa3b, v58
	v_pk_fma_f32 v[60:61], v[56:57], v[60:61], s[24:25] op_sel_hi:[1,1,0]
	v_mul_f32_e32 v59, 0xbf38aa3b, v59
	v_exp_f32_e32 v58, v58
	v_pk_fma_f32 v[60:61], v[56:57], v[60:61], s[34:35] op_sel_hi:[1,1,0]
	v_exp_f32_e32 v59, v59
	v_pk_fma_f32 v[60:61], v[56:57], v[60:61], s[40:41] op_sel_hi:[1,1,0]
	v_and_b32_e32 v54, 0x7fffffff, v52
	v_pk_mul_f32 v[56:57], v[56:57], v[60:61]
	v_max_f32_e32 v52, 0, v52
	v_max_f32_e32 v53, 0, v53
	v_pk_mul_f32 v[54:55], v[54:55], v[56:57]
	v_pk_mul_f32 v[50:51], s[0:1], v[50:51] op_sel_hi:[0,1]
	v_pk_fma_f32 v[52:53], v[58:59], v[54:55], v[52:53] neg_lo:[1,0,0] neg_hi:[1,0,0]
	v_pk_fma_f32 v[50:51], v[50:51], v[240:241], v[244:245]
	v_cvt_pk_f16_f32 v52, v52, v53
	v_fma_f32 v53, |v50|, s25, 1.0
	v_rcp_f32_e32 v56, v53
	v_fma_f32 v53, |v51|, s25, 1.0
	v_rcp_f32_e32 v57, v53
	v_pk_mul_f32 v[58:59], v[50:51], v[50:51]
	v_and_b32_e32 v55, 0x7fffffff, v51
	v_mul_f32_e32 v53, 0xbf38aa3b, v58
	v_pk_fma_f32 v[60:61], v[56:57], s[22:23], v[90:91] op_sel_hi:[1,0,0]
	v_exp_f32_e32 v58, v53
	v_pk_fma_f32 v[60:61], v[56:57], v[60:61], s[24:25] op_sel_hi:[1,1,0]
	v_mul_f32_e32 v53, 0xbf38aa3b, v59
	v_pk_fma_f32 v[60:61], v[56:57], v[60:61], s[34:35] op_sel_hi:[1,1,0]
	v_exp_f32_e32 v59, v53
	v_pk_fma_f32 v[60:61], v[56:57], v[60:61], s[40:41] op_sel_hi:[1,1,0]
	v_and_b32_e32 v54, 0x7fffffff, v50
	v_pk_mul_f32 v[56:57], v[56:57], v[60:61]
	v_max_f32_e32 v50, 0, v50
	v_max_f32_e32 v51, 0, v51
	v_pk_mul_f32 v[54:55], v[54:55], v[56:57]
	s_movk_i32 s0, 0x70
	v_pk_fma_f32 v[50:51], v[58:59], v[54:55], v[50:51] neg_lo:[1,0,0] neg_hi:[1,0,0]
	s_waitcnt vmcnt(0)
	v_add_f32_e32 v96, v24, v25
	v_cvt_pk_f16_f32 v53, v50, v51
	v_bitop3_b32 v50, v86, s0, v88 bitop3:0x6c
	s_movk_i32 s0, 0x4000
	v_add_co_u32_e32 v92, vcc, s0, v82
	s_movk_i32 s0, 0x5000
	s_nop 0
	v_addc_co_u32_e32 v93, vcc, 0, v83, vcc
	v_or3_b32 v144, v85, v50, v87
	v_add_co_u32_e32 v94, vcc, s0, v82
	ds_write_b64 v144, v[52:53] offset:36352
	s_nop 0
	v_addc_co_u32_e32 v95, vcc, 0, v83, vcc
	s_movk_i32 s56, 0x5000
	v_add_co_u32_e64 v234, s[58:59], s56, v82
	s_nop 1
	v_addc_co_u32_e64 v235, s[58:59], 0, v83, s[58:59]
	global_load_dwordx4 v[170:173], v[234:235], off offset:-4096 nt
	global_load_dwordx4 v[174:177], v[234:235], off offset:-3072 nt
	global_load_dwordx4 v[178:181], v[234:235], off offset:-2048 nt
	global_load_dwordx4 v[182:185], v[234:235], off offset:-1024 nt
	global_load_dwordx4 v[186:189], v[234:235], off nt
	global_load_dwordx4 v[190:193], v[234:235], off offset:1024 nt
	global_load_dwordx4 v[194:197], v[234:235], off offset:2048 nt
	global_load_dwordx4 v[198:201], v[234:235], off offset:3072 nt
	v_add_f32_e32 v92, v40, v41
	v_add_f32_e32 v89, v89, v92
	v_add_f32_e32 v92, v34, v35
	v_add_f32_e32 v93, v36, v37
	v_add_f32_e32 v92, v92, v93
	v_add_f32_e32 v93, v30, v31
	v_add_f32_e32 v94, v32, v33
	v_add_f32_e32 v93, v93, v94
	v_add_f32_e32 v94, v26, v27
	v_add_f32_e32 v95, v28, v29
	v_add_f32_e32 v94, v94, v95
	v_add_f32_e32 v95, v22, v23
	v_add_f32_e32 v95, v95, v96
	v_add_f32_e32 v96, v18, v19
	v_add_f32_e32 v97, v20, v21
	v_add_f32_e32 v96, v96, v97
	v_add_f32_e32 v97, v14, v15
	v_add_f32_e32 v98, v16, v17
	v_add_f32_e32 v97, v97, v98
	v_add_f32_e32 v98, v10, v11
	v_add_f32_e32 v99, v12, v13
	v_add_f32_e32 v98, v98, v99
	v_cndmask_b32_e64 v99, v92, v89, s[4:5]
	v_cndmask_b32_e64 v89, v89, v92, s[4:5]
	v_cndmask_b32_e64 v92, v94, v93, s[4:5]
	v_cndmask_b32_e64 v93, v93, v94, s[4:5]
	v_cndmask_b32_e64 v94, v95, v96, s[4:5]
	v_add_f32_dpp v89, v99, v89 quad_perm:[1,0,3,2] row_mask:0xf bank_mask:0xf bound_ctrl:1
	v_add_f32_dpp v92, v92, v93 quad_perm:[1,0,3,2] row_mask:0xf bank_mask:0xf bound_ctrl:1
	v_cndmask_b32_e64 v93, v96, v95, s[4:5]
	v_cndmask_b32_e64 v95, v97, v98, s[4:5]
	s_movk_i32 s1, 0x80
	v_add_f32_dpp v93, v93, v94 quad_perm:[1,0,3,2] row_mask:0xf bank_mask:0xf bound_ctrl:1
	v_cndmask_b32_e64 v94, v98, v97, s[4:5]
	s_movk_i32 s23, 0x90
	s_nop 0
	v_add_f32_dpp v94, v94, v95 quad_perm:[1,0,3,2] row_mask:0xf bank_mask:0xf bound_ctrl:1
	v_cndmask_b32_e64 v95, v89, v92, s[6:7]
	v_cndmask_b32_e64 v89, v92, v89, s[6:7]
	v_cndmask_b32_e64 v92, v93, v94, s[6:7]
	v_cndmask_b32_e64 v93, v94, v93, s[6:7]
	v_add_f32_dpp v89, v95, v89 quad_perm:[2,3,0,1] row_mask:0xf bank_mask:0xf bound_ctrl:1
	s_nop 0
	v_add_f32_dpp v92, v92, v93 quad_perm:[2,3,0,1] row_mask:0xf bank_mask:0xf bound_ctrl:1
	v_cndmask_b32_e64 v93, v89, v92, s[8:9]
	v_cndmask_b32_e64 v89, v92, v89, s[8:9]
	v_mov_b32_e32 v92, v93
	s_nop 1
	v_mov_b32_dpp v92, v92 row_shl:4 row_mask:0xf bank_mask:0x5
	s_nop 1
	v_mov_b32_dpp v92, v93 row_shr:4 row_mask:0xf bank_mask:0xa
	v_add_f32_e32 v89, v89, v92
	s_nop 1
	v_add_f32_dpp v89, v89, v89 row_ror:8 row_mask:0xf bank_mask:0xf bound_ctrl:1
	v_mov_b32_e32 v92, v89
	s_nop 1
	v_permlane16_swap_b32_e32 v89, v92
	v_add_f32_e32 v89, v89, v92
	v_mov_b32_e32 v92, v89
	s_nop 1
	v_permlane32_swap_b32_e32 v89, v92
	v_add_f32_e32 v89, v89, v92
	v_mul_f32_e32 v89, 0x3b800000, v89
	v_bitop3_b32 v92, v86, s1, v88 bitop3:0x6c
	v_readlane_b32 s44, v89, 0
	v_readlane_b32 s46, v89, 1
	v_readlane_b32 s48, v89, 2
	v_pk_add_f32 v[40:41], v[40:41], s[44:45] op_sel_hi:[1,0] neg_lo:[0,1] neg_hi:[0,1]
	v_pk_add_f32 v[36:37], v[36:37], s[46:47] op_sel_hi:[1,0] neg_lo:[0,1] neg_hi:[0,1]
	v_readlane_b32 s50, v89, 3
	v_readlane_b32 s52, v89, 4
	v_readlane_b32 s54, v89, 5
	v_readlane_b32 s42, v89, 6
	v_readlane_b32 s0, v89, 7
	v_mul_f32_e32 v89, v41, v41
	v_or3_b32 v145, v85, v92, v87
	v_pk_add_f32 v[92:93], v[34:35], s[46:47] op_sel_hi:[1,0] neg_lo:[0,1] neg_hi:[0,1]
	v_mul_f32_e32 v34, v37, v37
	v_pk_add_f32 v[38:39], v[38:39], s[44:45] op_sel_hi:[1,0] neg_lo:[0,1] neg_hi:[0,1]
	v_fmac_f32_e32 v89, v40, v40
	v_fmac_f32_e32 v34, v36, v36
	v_fmac_f32_e32 v89, v39, v39
	v_fmac_f32_e32 v34, v93, v93
	v_fmac_f32_e32 v89, v38, v38
	v_fmac_f32_e32 v34, v92, v92
	v_cndmask_b32_e64 v35, v34, v89, s[4:5]
	v_cndmask_b32_e64 v34, v89, v34, s[4:5]
	s_movk_i32 s1, 0xa0
	v_pk_add_f32 v[32:33], v[32:33], s[48:49] op_sel_hi:[1,0] neg_lo:[0,1] neg_hi:[0,1]
	v_add_f32_dpp v89, v35, v34 quad_perm:[1,0,3,2] row_mask:0xf bank_mask:0xf bound_ctrl:1
	v_bitop3_b32 v34, v86, s23, v88 bitop3:0x6c
	v_or3_b32 v139, v85, v34, v87
	v_pk_add_f32 v[34:35], v[30:31], s[48:49] op_sel_hi:[1,0] neg_lo:[0,1] neg_hi:[0,1]
	v_bitop3_b32 v30, v86, s1, v88 bitop3:0x6c
	v_pk_add_f32 v[28:29], v[28:29], s[50:51] op_sel_hi:[1,0] neg_lo:[0,1] neg_hi:[0,1]
	v_mul_f32_e32 v94, v33, v33
	v_or3_b32 v137, v85, v30, v87
	v_pk_add_f32 v[30:31], v[26:27], s[50:51] op_sel_hi:[1,0] neg_lo:[0,1] neg_hi:[0,1]
	v_mul_f32_e32 v26, v29, v29
	v_fmac_f32_e32 v94, v32, v32
	v_fmac_f32_e32 v26, v28, v28
	v_fmac_f32_e32 v94, v35, v35
	v_fmac_f32_e32 v26, v31, v31
	v_fmac_f32_e32 v94, v34, v34
	v_fmac_f32_e32 v26, v30, v30
	v_cndmask_b32_e64 v27, v26, v94, s[4:5]
	v_cndmask_b32_e64 v26, v94, v26, s[4:5]
	s_movk_i32 s1, 0xb0
	v_pk_add_f32 v[24:25], v[24:25], s[52:53] op_sel_hi:[1,0] neg_lo:[0,1] neg_hi:[0,1]
	v_add_f32_dpp v26, v27, v26 quad_perm:[1,0,3,2] row_mask:0xf bank_mask:0xf bound_ctrl:1
	v_cndmask_b32_e64 v27, v89, v26, s[6:7]
	v_cndmask_b32_e64 v26, v26, v89, s[6:7]
	v_pk_add_f32 v[20:21], v[20:21], s[54:55] op_sel_hi:[1,0] neg_lo:[0,1] neg_hi:[0,1]
	v_mul_f32_e32 v94, v25, v25
	v_add_f32_dpp v89, v27, v26 quad_perm:[2,3,0,1] row_mask:0xf bank_mask:0xf bound_ctrl:1
	v_bitop3_b32 v26, v86, s1, v88 bitop3:0x6c
	s_movk_i32 s1, 0xc0
	v_or3_b32 v136, v85, v26, v87
	v_pk_add_f32 v[26:27], v[22:23], s[52:53] op_sel_hi:[1,0] neg_lo:[0,1] neg_hi:[0,1]
	v_bitop3_b32 v22, v86, s1, v88 bitop3:0x6c
	v_or3_b32 v123, v85, v22, v87
	v_pk_add_f32 v[22:23], v[18:19], s[54:55] op_sel_hi:[1,0] neg_lo:[0,1] neg_hi:[0,1]
	v_mul_f32_e32 v18, v21, v21
	v_fmac_f32_e32 v94, v24, v24
	v_fmac_f32_e32 v18, v20, v20
	v_fmac_f32_e32 v94, v27, v27
	v_fmac_f32_e32 v18, v23, v23
	v_fmac_f32_e32 v94, v26, v26
	v_fmac_f32_e32 v18, v22, v22
	v_cndmask_b32_e64 v19, v18, v94, s[4:5]
	v_cndmask_b32_e64 v18, v94, v18, s[4:5]
	v_pk_add_f32 v[16:17], v[16:17], s[42:43] op_sel_hi:[1,0] neg_lo:[0,1] neg_hi:[0,1]
	s_nop 0
	v_add_f32_dpp v94, v19, v18 quad_perm:[1,0,3,2] row_mask:0xf bank_mask:0xf bound_ctrl:1
	v_pk_add_f32 v[18:19], v[14:15], s[42:43] op_sel_hi:[1,0] neg_lo:[0,1] neg_hi:[0,1]
	v_pk_add_f32 v[14:15], v[10:11], s[0:1] op_sel_hi:[1,0] neg_lo:[0,1] neg_hi:[0,1]
	v_pk_add_f32 v[10:11], v[12:13], s[0:1] op_sel_hi:[1,0] neg_lo:[0,1] neg_hi:[0,1]
	v_mul_f32_e32 v95, v17, v17
	v_mul_f32_e32 v12, v11, v11
	v_fmac_f32_e32 v95, v16, v16
	v_fmac_f32_e32 v12, v10, v10
	v_fmac_f32_e32 v95, v19, v19
	v_fmac_f32_e32 v12, v15, v15
	v_fmac_f32_e32 v95, v18, v18
	v_fmac_f32_e32 v12, v14, v14
	v_cndmask_b32_e64 v13, v12, v95, s[4:5]
	v_cndmask_b32_e64 v12, v95, v12, s[4:5]
	s_movk_i32 s0, 0xd0
	s_nop 0
	v_add_f32_dpp v12, v13, v12 quad_perm:[1,0,3,2] row_mask:0xf bank_mask:0xf bound_ctrl:1
	v_cndmask_b32_e64 v13, v94, v12, s[6:7]
	v_cndmask_b32_e64 v12, v12, v94, s[6:7]
	s_nop 1
	v_add_f32_dpp v12, v13, v12 quad_perm:[2,3,0,1] row_mask:0xf bank_mask:0xf bound_ctrl:1
	v_cndmask_b32_e64 v13, v89, v12, s[8:9]
	v_cndmask_b32_e64 v12, v12, v89, s[8:9]
	v_mov_b32_e32 v89, v13
	s_nop 1
	v_mov_b32_dpp v89, v89 row_shl:4 row_mask:0xf bank_mask:0x5
	s_nop 1
	v_mov_b32_dpp v89, v13 row_shr:4 row_mask:0xf bank_mask:0xa
	v_add_f32_e32 v12, v12, v89
	v_bitop3_b32 v89, v86, s0, v88 bitop3:0x6c
	v_or3_b32 v133, v85, v89, v87
	v_add_f32_dpp v12, v12, v12 row_ror:8 row_mask:0xf bank_mask:0xf bound_ctrl:1
	v_mov_b32_e32 v13, v12
	s_nop 1
	v_permlane16_swap_b32_e32 v12, v13
	v_add_f32_e32 v12, v12, v13
	v_mov_b32_e32 v13, v12
	s_nop 1
	v_permlane32_swap_b32_e32 v12, v13
	v_add_f32_e32 v12, v12, v13
	v_fmamk_f32 v12, v12, 0x3b800000, v116
	v_mul_f32_e32 v13, 0x4f800000, v12
	v_cmp_gt_f32_e32 vcc, s35, v12
	s_nop 1
	v_cndmask_b32_e32 v12, v12, v13, vcc
	v_sqrt_f32_e32 v13, v12
	s_nop 0
	v_add_u32_e32 v89, -1, v13
	v_fma_f32 v94, -v89, v13, v12
	v_cmp_ge_f32_e64 s[0:1], 0, v94
	v_add_u32_e32 v94, 1, v13
	s_nop 0
	v_cndmask_b32_e64 v89, v13, v89, s[0:1]
	v_fma_f32 v13, -v94, v13, v12
	v_cmp_lt_f32_e64 s[0:1], 0, v13
	s_nop 1
	v_cndmask_b32_e64 v13, v89, v94, s[0:1]
	v_mul_f32_e32 v89, 0x37800000, v13
	v_cndmask_b32_e32 v13, v13, v89, vcc
	v_cmp_class_f32_e32 vcc, v12, v117
	s_nop 1
	v_cndmask_b32_e32 v12, v13, v12, vcc
	v_div_scale_f32 v13, s[0:1], v12, v12, 1.0
	v_rcp_f32_e32 v89, v13
	s_movk_i32 s0, 0xe0
	v_bitop3_b32 v94, v86, s0, v88 bitop3:0x6c
	v_or3_b32 v119, v85, v94, v87
	v_fma_f32 v94, -v13, v89, 1.0
	v_fmac_f32_e32 v89, v94, v89
	v_div_scale_f32 v94, vcc, 1.0, v12, 1.0
	v_mul_f32_e32 v95, v94, v89
	v_fma_f32 v96, -v13, v95, v94
	v_fmac_f32_e32 v95, v96, v89
	v_fma_f32 v13, -v13, v95, v94
	v_div_fmas_f32 v13, v13, v89, v95
	v_div_fixup_f32 v12, v13, v12, 1.0
	s_nop 0
	v_readlane_b32 s0, v12, 0
	s_nop 1
	v_pk_mul_f32 v[38:39], s[0:1], v[38:39] op_sel_hi:[0,1]
	v_pk_fma_f32 v[38:39], v[38:39], v[238:239], v[242:243]
	v_pk_mul_f32 v[40:41], s[0:1], v[40:41] op_sel_hi:[0,1]
	v_fma_f32 v13, |v38|, s25, 1.0
	v_rcp_f32_e32 v96, v13
	v_fma_f32 v13, |v39|, s25, 1.0
	v_rcp_f32_e32 v97, v13
	v_pk_mul_f32 v[98:99], v[38:39], v[38:39]
	v_pk_fma_f32 v[40:41], v[40:41], v[240:241], v[244:245]
	v_mul_f32_e32 v13, 0xbf38aa3b, v98
	v_pk_fma_f32 v[100:101], v[96:97], s[22:23], v[90:91] op_sel_hi:[1,0,0]
	v_exp_f32_e32 v98, v13
	v_pk_fma_f32 v[100:101], v[96:97], v[100:101], s[24:25] op_sel_hi:[1,1,0]
	v_mul_f32_e32 v13, 0xbf38aa3b, v99
	v_pk_fma_f32 v[100:101], v[96:97], v[100:101], s[34:35] op_sel_hi:[1,1,0]
	v_and_b32_e32 v95, 0x7fffffff, v39
	v_pk_fma_f32 v[100:101], v[96:97], v[100:101], s[40:41] op_sel_hi:[1,1,0]
	v_and_b32_e32 v94, 0x7fffffff, v38
	v_exp_f32_e32 v99, v13
	v_pk_mul_f32 v[96:97], v[96:97], v[100:101]
	v_fma_f32 v13, |v40|, s25, 1.0
	v_pk_mul_f32 v[94:95], v[94:95], v[96:97]
	v_rcp_f32_e32 v96, v13
	v_fma_f32 v13, |v41|, s25, 1.0
	v_rcp_f32_e32 v97, v13
	v_max_f32_e32 v38, 0, v38
	v_max_f32_e32 v39, 0, v39
	v_pk_fma_f32 v[38:39], v[98:99], v[94:95], v[38:39] neg_lo:[1,0,0] neg_hi:[1,0,0]
	v_pk_mul_f32 v[98:99], v[40:41], v[40:41]
	v_pk_fma_f32 v[100:101], v[96:97], s[22:23], v[90:91] op_sel_hi:[1,0,0]
	v_mul_f32_e32 v13, 0xbf38aa3b, v98
	v_exp_f32_e32 v98, v13
	v_pk_fma_f32 v[100:101], v[96:97], v[100:101], s[24:25] op_sel_hi:[1,1,0]
	v_mul_f32_e32 v13, 0xbf38aa3b, v99
	v_pk_fma_f32 v[100:101], v[96:97], v[100:101], s[34:35] op_sel_hi:[1,1,0]
	v_exp_f32_e32 v99, v13
	v_pk_fma_f32 v[100:101], v[96:97], v[100:101], s[40:41] op_sel_hi:[1,1,0]
	v_and_b32_e32 v95, 0x7fffffff, v41
	v_and_b32_e32 v94, 0x7fffffff, v40
	v_pk_mul_f32 v[96:97], v[96:97], v[100:101]
	v_max_f32_e32 v40, 0, v40
	v_max_f32_e32 v41, 0, v41
	v_pk_mul_f32 v[94:95], v[94:95], v[96:97]
	v_cvt_pk_f16_f32 v38, v38, v39
	v_pk_fma_f32 v[40:41], v[98:99], v[94:95], v[40:41] neg_lo:[1,0,0] neg_hi:[1,0,0]
	v_readlane_b32 s0, v12, 1
	v_cvt_pk_f16_f32 v39, v40, v41
	ds_write_b64 v145, v[38:39] offset:36864
	v_pk_mul_f32 v[38:39], s[0:1], v[92:93] op_sel_hi:[0,1]
	v_pk_fma_f32 v[38:39], v[38:39], v[238:239], v[242:243]
	v_pk_mul_f32 v[36:37], s[0:1], v[36:37] op_sel_hi:[0,1]
	v_fma_f32 v13, |v38|, s25, 1.0
	v_rcp_f32_e32 v92, v13
	v_fma_f32 v13, |v39|, s25, 1.0
	v_rcp_f32_e32 v93, v13
	v_pk_mul_f32 v[94:95], v[38:39], v[38:39]
	v_pk_fma_f32 v[36:37], v[36:37], v[240:241], v[244:245]
	v_mul_f32_e32 v13, 0xbf38aa3b, v94
	v_pk_fma_f32 v[96:97], v[92:93], s[22:23], v[90:91] op_sel_hi:[1,0,0]
	v_exp_f32_e32 v94, v13
	v_pk_fma_f32 v[96:97], v[92:93], v[96:97], s[24:25] op_sel_hi:[1,1,0]
	v_mul_f32_e32 v13, 0xbf38aa3b, v95
	v_pk_fma_f32 v[96:97], v[92:93], v[96:97], s[34:35] op_sel_hi:[1,1,0]
	v_and_b32_e32 v41, 0x7fffffff, v39
	v_pk_fma_f32 v[96:97], v[92:93], v[96:97], s[40:41] op_sel_hi:[1,1,0]
	v_and_b32_e32 v40, 0x7fffffff, v38
	v_exp_f32_e32 v95, v13
	v_pk_mul_f32 v[92:93], v[92:93], v[96:97]
	v_fma_f32 v13, |v36|, s25, 1.0
	v_pk_mul_f32 v[40:41], v[40:41], v[92:93]
	v_rcp_f32_e32 v92, v13
	v_fma_f32 v13, |v37|, s25, 1.0
	v_rcp_f32_e32 v93, v13
	v_max_f32_e32 v38, 0, v38
	v_max_f32_e32 v39, 0, v39
	v_pk_fma_f32 v[38:39], v[94:95], v[40:41], v[38:39] neg_lo:[1,0,0] neg_hi:[1,0,0]
	v_pk_mul_f32 v[94:95], v[36:37], v[36:37]
	v_pk_fma_f32 v[96:97], v[92:93], s[22:23], v[90:91] op_sel_hi:[1,0,0]
	v_mul_f32_e32 v13, 0xbf38aa3b, v94
	v_exp_f32_e32 v94, v13
	v_pk_fma_f32 v[96:97], v[92:93], v[96:97], s[24:25] op_sel_hi:[1,1,0]
	v_mul_f32_e32 v13, 0xbf38aa3b, v95
	v_pk_fma_f32 v[96:97], v[92:93], v[96:97], s[34:35] op_sel_hi:[1,1,0]
	v_exp_f32_e32 v95, v13
	v_pk_fma_f32 v[96:97], v[92:93], v[96:97], s[40:41] op_sel_hi:[1,1,0]
	v_and_b32_e32 v41, 0x7fffffff, v37
	v_and_b32_e32 v40, 0x7fffffff, v36
	v_pk_mul_f32 v[92:93], v[92:93], v[96:97]
	v_readlane_b32 s0, v12, 2
	v_max_f32_e32 v36, 0, v36
	v_max_f32_e32 v37, 0, v37
	v_pk_mul_f32 v[40:41], v[40:41], v[92:93]
	v_pk_mul_f32 v[34:35], s[0:1], v[34:35] op_sel_hi:[0,1]
	v_pk_fma_f32 v[36:37], v[94:95], v[40:41], v[36:37] neg_lo:[1,0,0] neg_hi:[1,0,0]
	v_pk_fma_f32 v[34:35], v[34:35], v[238:239], v[242:243]
	v_cvt_pk_f16_f32 v38, v38, v39
	v_cvt_pk_f16_f32 v39, v36, v37
	v_fma_f32 v13, |v34|, s25, 1.0
	ds_write_b64 v139, v[38:39] offset:37376
	v_rcp_f32_e32 v38, v13
	v_fma_f32 v13, |v35|, s25, 1.0
	v_rcp_f32_e32 v39, v13
	v_pk_mul_f32 v[40:41], v[34:35], v[34:35]
	v_pk_mul_f32 v[32:33], s[0:1], v[32:33] op_sel_hi:[0,1]
	v_mul_f32_e32 v13, 0xbf38aa3b, v40
	v_pk_fma_f32 v[92:93], v[38:39], s[22:23], v[90:91] op_sel_hi:[1,0,0]
	v_exp_f32_e32 v40, v13
	v_pk_fma_f32 v[92:93], v[38:39], v[92:93], s[24:25] op_sel_hi:[1,1,0]
	v_mul_f32_e32 v13, 0xbf38aa3b, v41
	v_pk_fma_f32 v[92:93], v[38:39], v[92:93], s[34:35] op_sel_hi:[1,1,0]
	v_pk_fma_f32 v[32:33], v[32:33], v[240:241], v[244:245]
	v_pk_fma_f32 v[92:93], v[38:39], v[92:93], s[40:41] op_sel_hi:[1,1,0]
	v_and_b32_e32 v37, 0x7fffffff, v35
	v_and_b32_e32 v36, 0x7fffffff, v34
	v_exp_f32_e32 v41, v13
	v_pk_mul_f32 v[38:39], v[38:39], v[92:93]
	v_fma_f32 v13, |v32|, s25, 1.0
	v_pk_mul_f32 v[36:37], v[36:37], v[38:39]
	v_rcp_f32_e32 v38, v13
	v_fma_f32 v13, |v33|, s25, 1.0
	v_rcp_f32_e32 v39, v13
	v_max_f32_e32 v34, 0, v34
	v_max_f32_e32 v35, 0, v35
	v_pk_fma_f32 v[34:35], v[40:41], v[36:37], v[34:35] neg_lo:[1,0,0] neg_hi:[1,0,0]
	v_pk_mul_f32 v[40:41], v[32:33], v[32:33]
	v_pk_fma_f32 v[92:93], v[38:39], s[22:23], v[90:91] op_sel_hi:[1,0,0]
	v_mul_f32_e32 v13, 0xbf38aa3b, v40
	v_exp_f32_e32 v40, v13
	v_pk_fma_f32 v[92:93], v[38:39], v[92:93], s[24:25] op_sel_hi:[1,1,0]
	v_mul_f32_e32 v13, 0xbf38aa3b, v41
	v_pk_fma_f32 v[92:93], v[38:39], v[92:93], s[34:35] op_sel_hi:[1,1,0]
	v_exp_f32_e32 v41, v13
	v_pk_fma_f32 v[92:93], v[38:39], v[92:93], s[40:41] op_sel_hi:[1,1,0]
	v_and_b32_e32 v37, 0x7fffffff, v33
	v_and_b32_e32 v36, 0x7fffffff, v32
	v_pk_mul_f32 v[38:39], v[38:39], v[92:93]
	v_readlane_b32 s0, v12, 3
	v_max_f32_e32 v32, 0, v32
	v_max_f32_e32 v33, 0, v33
	v_pk_mul_f32 v[36:37], v[36:37], v[38:39]
	v_pk_mul_f32 v[30:31], s[0:1], v[30:31] op_sel_hi:[0,1]
	v_pk_fma_f32 v[32:33], v[40:41], v[36:37], v[32:33] neg_lo:[1,0,0] neg_hi:[1,0,0]
	v_pk_fma_f32 v[30:31], v[30:31], v[238:239], v[242:243]
	v_cvt_pk_f16_f32 v34, v34, v35
	v_cvt_pk_f16_f32 v35, v32, v33
	v_fma_f32 v13, |v30|, s25, 1.0
	ds_write_b64 v137, v[34:35] offset:37888
	v_rcp_f32_e32 v34, v13
	v_fma_f32 v13, |v31|, s25, 1.0
	v_rcp_f32_e32 v35, v13
	v_pk_mul_f32 v[36:37], v[30:31], v[30:31]
	v_pk_mul_f32 v[28:29], s[0:1], v[28:29] op_sel_hi:[0,1]
	v_mul_f32_e32 v13, 0xbf38aa3b, v36
	v_pk_fma_f32 v[38:39], v[34:35], s[22:23], v[90:91] op_sel_hi:[1,0,0]
	v_exp_f32_e32 v36, v13
	v_pk_fma_f32 v[38:39], v[34:35], v[38:39], s[24:25] op_sel_hi:[1,1,0]
	v_mul_f32_e32 v13, 0xbf38aa3b, v37
	v_pk_fma_f32 v[38:39], v[34:35], v[38:39], s[34:35] op_sel_hi:[1,1,0]
	v_pk_fma_f32 v[28:29], v[28:29], v[240:241], v[244:245]
	v_pk_fma_f32 v[38:39], v[34:35], v[38:39], s[40:41] op_sel_hi:[1,1,0]
	v_and_b32_e32 v33, 0x7fffffff, v31
	v_and_b32_e32 v32, 0x7fffffff, v30
	v_exp_f32_e32 v37, v13
	v_pk_mul_f32 v[34:35], v[34:35], v[38:39]
	v_fma_f32 v13, |v28|, s25, 1.0
	v_pk_mul_f32 v[32:33], v[32:33], v[34:35]
	v_rcp_f32_e32 v34, v13
	v_fma_f32 v13, |v29|, s25, 1.0
	v_rcp_f32_e32 v35, v13
	v_max_f32_e32 v30, 0, v30
	v_max_f32_e32 v31, 0, v31
	v_pk_fma_f32 v[30:31], v[36:37], v[32:33], v[30:31] neg_lo:[1,0,0] neg_hi:[1,0,0]
	v_pk_mul_f32 v[36:37], v[28:29], v[28:29]
	v_pk_fma_f32 v[38:39], v[34:35], s[22:23], v[90:91] op_sel_hi:[1,0,0]
	v_mul_f32_e32 v13, 0xbf38aa3b, v36
	v_exp_f32_e32 v36, v13
	v_pk_fma_f32 v[38:39], v[34:35], v[38:39], s[24:25] op_sel_hi:[1,1,0]
	v_mul_f32_e32 v13, 0xbf38aa3b, v37
	v_pk_fma_f32 v[38:39], v[34:35], v[38:39], s[34:35] op_sel_hi:[1,1,0]
	v_exp_f32_e32 v37, v13
	v_pk_fma_f32 v[38:39], v[34:35], v[38:39], s[40:41] op_sel_hi:[1,1,0]
	v_and_b32_e32 v33, 0x7fffffff, v29
	v_and_b32_e32 v32, 0x7fffffff, v28
	v_pk_mul_f32 v[34:35], v[34:35], v[38:39]
	v_readlane_b32 s0, v12, 4
	v_max_f32_e32 v28, 0, v28
	v_max_f32_e32 v29, 0, v29
	v_pk_mul_f32 v[32:33], v[32:33], v[34:35]
	v_pk_mul_f32 v[26:27], s[0:1], v[26:27] op_sel_hi:[0,1]
	v_pk_fma_f32 v[28:29], v[36:37], v[32:33], v[28:29] neg_lo:[1,0,0] neg_hi:[1,0,0]
	v_pk_fma_f32 v[26:27], v[26:27], v[238:239], v[242:243]
	v_cvt_pk_f16_f32 v30, v30, v31
	v_cvt_pk_f16_f32 v31, v28, v29
	v_fma_f32 v13, |v26|, s25, 1.0
	ds_write_b64 v136, v[30:31] offset:38400
	v_rcp_f32_e32 v30, v13
	v_fma_f32 v13, |v27|, s25, 1.0
	v_rcp_f32_e32 v31, v13
	v_pk_mul_f32 v[32:33], v[26:27], v[26:27]
	v_pk_mul_f32 v[24:25], s[0:1], v[24:25] op_sel_hi:[0,1]
	v_mul_f32_e32 v13, 0xbf38aa3b, v32
	v_pk_fma_f32 v[34:35], v[30:31], s[22:23], v[90:91] op_sel_hi:[1,0,0]
	v_exp_f32_e32 v32, v13
	v_pk_fma_f32 v[34:35], v[30:31], v[34:35], s[24:25] op_sel_hi:[1,1,0]
	v_mul_f32_e32 v13, 0xbf38aa3b, v33
	v_pk_fma_f32 v[34:35], v[30:31], v[34:35], s[34:35] op_sel_hi:[1,1,0]
	v_pk_fma_f32 v[24:25], v[24:25], v[240:241], v[244:245]
	v_pk_fma_f32 v[34:35], v[30:31], v[34:35], s[40:41] op_sel_hi:[1,1,0]
	v_and_b32_e32 v29, 0x7fffffff, v27
	v_and_b32_e32 v28, 0x7fffffff, v26
	v_exp_f32_e32 v33, v13
	v_pk_mul_f32 v[30:31], v[30:31], v[34:35]
	v_fma_f32 v13, |v24|, s25, 1.0
	v_pk_mul_f32 v[28:29], v[28:29], v[30:31]
	v_rcp_f32_e32 v30, v13
	v_fma_f32 v13, |v25|, s25, 1.0
	v_rcp_f32_e32 v31, v13
	v_max_f32_e32 v26, 0, v26
	v_max_f32_e32 v27, 0, v27
	v_pk_fma_f32 v[26:27], v[32:33], v[28:29], v[26:27] neg_lo:[1,0,0] neg_hi:[1,0,0]
	v_pk_mul_f32 v[32:33], v[24:25], v[24:25]
	v_pk_fma_f32 v[34:35], v[30:31], s[22:23], v[90:91] op_sel_hi:[1,0,0]
	v_mul_f32_e32 v13, 0xbf38aa3b, v32
	v_exp_f32_e32 v32, v13
	v_pk_fma_f32 v[34:35], v[30:31], v[34:35], s[24:25] op_sel_hi:[1,1,0]
	v_mul_f32_e32 v13, 0xbf38aa3b, v33
	v_pk_fma_f32 v[34:35], v[30:31], v[34:35], s[34:35] op_sel_hi:[1,1,0]
	v_exp_f32_e32 v33, v13
	v_pk_fma_f32 v[34:35], v[30:31], v[34:35], s[40:41] op_sel_hi:[1,1,0]
	v_and_b32_e32 v29, 0x7fffffff, v25
	v_and_b32_e32 v28, 0x7fffffff, v24
	v_pk_mul_f32 v[30:31], v[30:31], v[34:35]
	v_readlane_b32 s0, v12, 5
	v_max_f32_e32 v24, 0, v24
	v_max_f32_e32 v25, 0, v25
	v_pk_mul_f32 v[28:29], v[28:29], v[30:31]
	v_pk_mul_f32 v[22:23], s[0:1], v[22:23] op_sel_hi:[0,1]
	v_pk_fma_f32 v[24:25], v[32:33], v[28:29], v[24:25] neg_lo:[1,0,0] neg_hi:[1,0,0]
	v_pk_fma_f32 v[22:23], v[22:23], v[238:239], v[242:243]
	v_cvt_pk_f16_f32 v26, v26, v27
	v_cvt_pk_f16_f32 v27, v24, v25
	v_fma_f32 v13, |v22|, s25, 1.0
	ds_write_b64 v123, v[26:27] offset:38912
	v_rcp_f32_e32 v26, v13
	v_fma_f32 v13, |v23|, s25, 1.0
	v_rcp_f32_e32 v27, v13
	v_pk_mul_f32 v[28:29], v[22:23], v[22:23]
	v_pk_mul_f32 v[20:21], s[0:1], v[20:21] op_sel_hi:[0,1]
	v_mul_f32_e32 v13, 0xbf38aa3b, v28
	v_pk_fma_f32 v[30:31], v[26:27], s[22:23], v[90:91] op_sel_hi:[1,0,0]
	v_exp_f32_e32 v28, v13
	v_pk_fma_f32 v[30:31], v[26:27], v[30:31], s[24:25] op_sel_hi:[1,1,0]
	v_mul_f32_e32 v13, 0xbf38aa3b, v29
	v_pk_fma_f32 v[30:31], v[26:27], v[30:31], s[34:35] op_sel_hi:[1,1,0]
	v_pk_fma_f32 v[20:21], v[20:21], v[240:241], v[244:245]
	v_pk_fma_f32 v[30:31], v[26:27], v[30:31], s[40:41] op_sel_hi:[1,1,0]
	s_waitcnt vmcnt(7)
	v_add_f32_e32 v92, v170, v171
	v_add_f32_e32 v93, v172, v173
	v_and_b32_e32 v25, 0x7fffffff, v23
	v_and_b32_e32 v24, 0x7fffffff, v22
	v_exp_f32_e32 v29, v13
	v_pk_mul_f32 v[26:27], v[26:27], v[30:31]
	v_fma_f32 v13, |v20|, s25, 1.0
	v_add_f32_e32 v92, v92, v93
	s_waitcnt vmcnt(6)
	v_add_f32_e32 v93, v174, v175
	v_add_f32_e32 v94, v176, v177
	v_pk_mul_f32 v[24:25], v[24:25], v[26:27]
	v_rcp_f32_e32 v26, v13
	v_fma_f32 v13, |v21|, s25, 1.0
	v_add_f32_e32 v93, v93, v94
	s_waitcnt vmcnt(5)
	v_add_f32_e32 v94, v178, v179
	v_add_f32_e32 v95, v180, v181
	v_rcp_f32_e32 v27, v13
	v_add_f32_e32 v94, v94, v95
	s_waitcnt vmcnt(4)
	v_add_f32_e32 v95, v182, v183
	v_add_f32_e32 v96, v184, v185
	v_add_f32_e32 v95, v95, v96
	s_waitcnt vmcnt(3)
	v_add_f32_e32 v96, v186, v187
	v_add_f32_e32 v97, v188, v189
	v_max_f32_e32 v22, 0, v22
	v_max_f32_e32 v23, 0, v23
	v_add_f32_e32 v96, v96, v97
	s_waitcnt vmcnt(2)
	v_add_f32_e32 v97, v190, v191
	v_add_f32_e32 v98, v192, v193
	v_pk_fma_f32 v[22:23], v[28:29], v[24:25], v[22:23] neg_lo:[1,0,0] neg_hi:[1,0,0]
	v_pk_mul_f32 v[28:29], v[20:21], v[20:21]
	v_add_f32_e32 v97, v97, v98
	s_waitcnt vmcnt(1)
	v_add_f32_e32 v98, v194, v195
	v_add_f32_e32 v99, v196, v197
	v_mul_f32_e32 v13, 0xbf38aa3b, v28
	v_pk_fma_f32 v[30:31], v[26:27], s[22:23], v[90:91] op_sel_hi:[1,0,0]
	v_add_f32_e32 v98, v98, v99
	s_waitcnt vmcnt(0)
	v_add_f32_e32 v99, v198, v199
	v_add_f32_e32 v100, v200, v201
	v_exp_f32_e32 v28, v13
	v_pk_fma_f32 v[30:31], v[26:27], v[30:31], s[24:25] op_sel_hi:[1,1,0]
	v_mul_f32_e32 v13, 0xbf38aa3b, v29
	v_add_f32_e32 v99, v99, v100
	v_cndmask_b32_e64 v100, v93, v92, s[4:5]
	v_cndmask_b32_e64 v92, v92, v93, s[4:5]
	v_cndmask_b32_e64 v93, v95, v94, s[4:5]
	v_cndmask_b32_e64 v94, v94, v95, s[4:5]
	v_pk_fma_f32 v[30:31], v[26:27], v[30:31], s[34:35] op_sel_hi:[1,1,0]
	v_exp_f32_e32 v29, v13
	v_add_f32_dpp v93, v93, v94 quad_perm:[1,0,3,2] row_mask:0xf bank_mask:0xf bound_ctrl:1
	v_cndmask_b32_e64 v94, v97, v96, s[4:5]
	v_cndmask_b32_e64 v95, v96, v97, s[4:5]
	v_pk_fma_f32 v[30:31], v[26:27], v[30:31], s[40:41] op_sel_hi:[1,1,0]
	v_cndmask_b32_e64 v96, v98, v99, s[4:5]
	v_add_f32_dpp v94, v94, v95 quad_perm:[1,0,3,2] row_mask:0xf bank_mask:0xf bound_ctrl:1
	v_cndmask_b32_e64 v95, v99, v98, s[4:5]
	v_and_b32_e32 v25, 0x7fffffff, v21
	v_and_b32_e32 v24, 0x7fffffff, v20
	v_pk_mul_f32 v[26:27], v[26:27], v[30:31]
	v_readlane_b32 s0, v12, 6
	v_add_f32_dpp v92, v100, v92 quad_perm:[1,0,3,2] row_mask:0xf bank_mask:0xf bound_ctrl:1
	v_add_f32_dpp v95, v95, v96 quad_perm:[1,0,3,2] row_mask:0xf bank_mask:0xf bound_ctrl:1
	v_max_f32_e32 v20, 0, v20
	v_max_f32_e32 v21, 0, v21
	v_pk_mul_f32 v[24:25], v[24:25], v[26:27]
	v_pk_mul_f32 v[18:19], s[0:1], v[18:19] op_sel_hi:[0,1]
	v_cndmask_b32_e64 v96, v92, v93, s[6:7]
	v_cndmask_b32_e64 v92, v93, v92, s[6:7]
	v_cndmask_b32_e64 v93, v94, v95, s[6:7]
	v_cndmask_b32_e64 v94, v95, v94, s[6:7]
	v_pk_fma_f32 v[20:21], v[28:29], v[24:25], v[20:21] neg_lo:[1,0,0] neg_hi:[1,0,0]
	v_pk_fma_f32 v[18:19], v[18:19], v[238:239], v[242:243]
	v_add_f32_dpp v92, v96, v92 quad_perm:[2,3,0,1] row_mask:0xf bank_mask:0xf bound_ctrl:1
	v_add_f32_dpp v93, v93, v94 quad_perm:[2,3,0,1] row_mask:0xf bank_mask:0xf bound_ctrl:1
	v_cvt_pk_f16_f32 v22, v22, v23
	v_cvt_pk_f16_f32 v23, v20, v21
	v_fma_f32 v13, |v18|, s25, 1.0
	v_cndmask_b32_e64 v94, v92, v93, s[8:9]
	ds_write_b64 v133, v[22:23] offset:39424
	v_rcp_f32_e32 v22, v13
	v_fma_f32 v13, |v19|, s25, 1.0
	v_cndmask_b32_e64 v92, v93, v92, s[8:9]
	v_mov_b32_e32 v93, v94
	v_rcp_f32_e32 v23, v13
	v_pk_mul_f32 v[24:25], v[18:19], v[18:19]
	v_mov_b32_dpp v93, v93 row_shl:4 row_mask:0xf bank_mask:0x5
	v_mul_f32_e32 v13, 0xbf38aa3b, v24
	v_pk_fma_f32 v[26:27], v[22:23], s[22:23], v[90:91] op_sel_hi:[1,0,0]
	v_mov_b32_dpp v93, v94 row_shr:4 row_mask:0xf bank_mask:0xa
	v_add_f32_e32 v92, v92, v93
	v_pk_fma_f32 v[26:27], v[22:23], v[26:27], s[24:25] op_sel_hi:[1,1,0]
	v_pk_mul_f32 v[16:17], s[0:1], v[16:17] op_sel_hi:[0,1]
	v_add_f32_dpp v92, v92, v92 row_ror:8 row_mask:0xf bank_mask:0xf bound_ctrl:1
	v_mov_b32_e32 v93, v92
	s_nop 1
	v_permlane16_swap_b32_e32 v92, v93
	v_pk_fma_f32 v[26:27], v[22:23], v[26:27], s[34:35] op_sel_hi:[1,1,0]
	v_add_f32_e32 v92, v92, v93
	v_exp_f32_e32 v24, v13
	v_pk_fma_f32 v[26:27], v[22:23], v[26:27], s[40:41] op_sel_hi:[1,1,0]
	v_mul_f32_e32 v13, 0xbf38aa3b, v25
	v_pk_fma_f32 v[16:17], v[16:17], v[240:241], v[244:245]
	v_mov_b32_e32 v93, v92
	v_and_b32_e32 v21, 0x7fffffff, v19
	v_and_b32_e32 v20, 0x7fffffff, v18
	v_exp_f32_e32 v25, v13
	v_pk_mul_f32 v[22:23], v[22:23], v[26:27]
	v_fma_f32 v13, |v16|, s25, 1.0
	v_permlane32_swap_b32_e32 v92, v93
	v_pk_mul_f32 v[20:21], v[20:21], v[22:23]
	v_rcp_f32_e32 v22, v13
	v_fma_f32 v13, |v17|, s25, 1.0
	v_add_f32_e32 v92, v92, v93
	v_rcp_f32_e32 v23, v13
	v_mul_f32_e32 v92, 0x3b800000, v92
	v_max_f32_e32 v18, 0, v18
	v_max_f32_e32 v19, 0, v19
	v_readlane_b32 s42, v92, 0
	v_readlane_b32 s44, v92, 1
	v_readlane_b32 s46, v92, 2
	v_readlane_b32 s48, v92, 3
	v_pk_fma_f32 v[18:19], v[24:25], v[20:21], v[18:19] neg_lo:[1,0,0] neg_hi:[1,0,0]
	v_pk_mul_f32 v[24:25], v[16:17], v[16:17]
	v_pk_add_f32 v[160:161], v[172:173], s[42:43] op_sel_hi:[1, 0] neg_lo:[0, 1] neg_hi:[0, 1]
	v_pk_add_f32 v[110:111], v[176:177], s[44:45] op_sel_hi:[1, 0] neg_lo:[0, 1] neg_hi:[0, 1]
	v_pk_add_f32 v[104:105], v[180:181], s[46:47] op_sel_hi:[1, 0] neg_lo:[0, 1] neg_hi:[0, 1]
	v_pk_add_f32 v[100:101], v[184:185], s[48:49] op_sel_hi:[1, 0] neg_lo:[0, 1] neg_hi:[0, 1]
	v_mul_f32_e32 v13, 0xbf38aa3b, v24
	v_pk_add_f32 v[158:159], v[170:171], s[42:43] op_sel_hi:[1, 0] neg_lo:[0, 1] neg_hi:[0, 1]
	v_mul_f32_e32 v78, v161, v161
	v_pk_add_f32 v[162:163], v[174:175], s[44:45] op_sel_hi:[1, 0] neg_lo:[0, 1] neg_hi:[0, 1]
	v_mul_f32_e32 v74, v111, v111
	v_pk_add_f32 v[108:109], v[178:179], s[46:47] op_sel_hi:[1, 0] neg_lo:[0, 1] neg_hi:[0, 1]
	v_mul_f32_e32 v70, v105, v105
	v_pk_add_f32 v[102:103], v[182:183], s[48:49] op_sel_hi:[1, 0] neg_lo:[0, 1] neg_hi:[0, 1]
	v_mul_f32_e32 v66, v101, v101
	v_exp_f32_e32 v24, v13
	v_pk_fma_f32 v[26:27], v[22:23], s[22:23], v[90:91] op_sel_hi:[1,0,0]
	v_mul_f32_e32 v13, 0xbf38aa3b, v25
	v_readlane_b32 s0, v12, 7
	v_fmac_f32_e32 v78, v160, v160
	v_fmac_f32_e32 v74, v110, v110
	v_fmac_f32_e32 v70, v104, v104
	v_fmac_f32_e32 v66, v100, v100
	v_pk_fma_f32 v[26:27], v[22:23], v[26:27], s[24:25] op_sel_hi:[1,1,0]
	v_exp_f32_e32 v25, v13
	v_pk_mul_f32 v[12:13], s[0:1], v[14:15] op_sel_hi:[0,1]
	v_pk_mul_f32 v[10:11], s[0:1], v[10:11] op_sel_hi:[0,1]
	s_movk_i32 s0, 0x6000
	v_fmac_f32_e32 v78, v159, v159
	v_fmac_f32_e32 v74, v163, v163
	v_fmac_f32_e32 v70, v109, v109
	v_fmac_f32_e32 v66, v103, v103
	v_pk_fma_f32 v[26:27], v[22:23], v[26:27], s[34:35] op_sel_hi:[1,1,0]
	v_add_co_u32_e32 v154, vcc, s0, v82
	v_fmac_f32_e32 v78, v158, v158
	v_fmac_f32_e32 v74, v162, v162
	v_fmac_f32_e32 v70, v108, v108
	v_fmac_f32_e32 v66, v102, v102
	v_pk_fma_f32 v[26:27], v[22:23], v[26:27], s[40:41] op_sel_hi:[1,1,0]
	v_addc_co_u32_e32 v155, vcc, 0, v83, vcc
	s_movk_i32 s0, 0x7000
	v_cndmask_b32_e64 v75, v74, v78, s[4:5]
	v_cndmask_b32_e64 v74, v78, v74, s[4:5]
	v_cndmask_b32_e64 v67, v66, v70, s[4:5]
	v_cndmask_b32_e64 v66, v70, v66, s[4:5]
	v_and_b32_e32 v21, 0x7fffffff, v17
	v_and_b32_e32 v20, 0x7fffffff, v16
	v_pk_mul_f32 v[22:23], v[22:23], v[26:27]
	v_add_co_u32_e32 v156, vcc, s0, v82
	v_readlane_b32 s50, v92, 4
	v_readlane_b32 s52, v92, 5
	v_readlane_b32 s54, v92, 6
	v_readlane_b32 s0, v92, 7
	v_add_f32_dpp v74, v75, v74 quad_perm:[1,0,3,2] row_mask:0xf bank_mask:0xf bound_ctrl:1
	v_add_f32_dpp v66, v67, v66 quad_perm:[1,0,3,2] row_mask:0xf bank_mask:0xf bound_ctrl:1
	v_max_f32_e32 v16, 0, v16
	v_max_f32_e32 v17, 0, v17
	v_pk_mul_f32 v[20:21], v[20:21], v[22:23]
	v_cndmask_b32_e64 v67, v74, v66, s[6:7]
	v_cndmask_b32_e64 v66, v66, v74, s[6:7]
	v_pk_add_f32 v[96:97], v[188:189], s[50:51] op_sel_hi:[1, 0] neg_lo:[0, 1] neg_hi:[0, 1]
	v_pk_add_f32 v[92:93], v[192:193], s[52:53] op_sel_hi:[1, 0] neg_lo:[0, 1] neg_hi:[0, 1]
	v_pk_add_f32 v[78:79], v[196:197], s[54:55] op_sel_hi:[1, 0] neg_lo:[0, 1] neg_hi:[0, 1]
	v_pk_add_f32 v[74:75], v[200:201], s[0:1] op_sel_hi:[1, 0] neg_lo:[0, 1] neg_hi:[0, 1]
	v_pk_fma_f32 v[16:17], v[24:25], v[20:21], v[16:17] neg_lo:[1,0,0] neg_hi:[1,0,0]
	v_pk_fma_f32 v[12:13], v[12:13], v[238:239], v[242:243]
	v_pk_add_f32 v[98:99], v[186:187], s[50:51] op_sel_hi:[1, 0] neg_lo:[0, 1] neg_hi:[0, 1]
	v_mul_f32_e32 v62, v97, v97
	v_pk_add_f32 v[94:95], v[190:191], s[52:53] op_sel_hi:[1, 0] neg_lo:[0, 1] neg_hi:[0, 1]
	v_mul_f32_e32 v58, v93, v93
	v_pk_add_f32 v[80:81], v[194:195], s[54:55] op_sel_hi:[1, 0] neg_lo:[0, 1] neg_hi:[0, 1]
	v_mul_f32_e32 v54, v79, v79
	v_pk_add_f32 v[76:77], v[198:199], s[0:1] op_sel_hi:[1, 0] neg_lo:[0, 1] neg_hi:[0, 1]
	v_mul_f32_e32 v50, v75, v75
	v_cvt_pk_f16_f32 v18, v18, v19
	v_cvt_pk_f16_f32 v19, v16, v17
	v_fma_f32 v16, |v12|, s25, 1.0
	v_fma_f32 v17, |v13|, s25, 1.0
	v_fmac_f32_e32 v62, v96, v96
	v_fmac_f32_e32 v58, v92, v92
	v_fmac_f32_e32 v54, v78, v78
	v_fmac_f32_e32 v50, v74, v74
	v_rcp_f32_e32 v16, v16
	v_rcp_f32_e32 v17, v17
	v_fmac_f32_e32 v62, v99, v99
	v_fmac_f32_e32 v58, v95, v95
	v_fmac_f32_e32 v54, v81, v81
	v_fmac_f32_e32 v50, v77, v77
	v_fmac_f32_e32 v62, v98, v98
	v_fmac_f32_e32 v58, v94, v94
	v_fmac_f32_e32 v54, v80, v80
	v_fmac_f32_e32 v50, v76, v76
	v_cndmask_b32_e64 v59, v58, v62, s[4:5]
	v_cndmask_b32_e64 v58, v62, v58, s[4:5]
	v_cndmask_b32_e64 v51, v50, v54, s[4:5]
	v_cndmask_b32_e64 v50, v54, v50, s[4:5]
	v_add_f32_dpp v58, v59, v58 quad_perm:[1,0,3,2] row_mask:0xf bank_mask:0xf bound_ctrl:1
	ds_write_b64 v119, v[18:19] offset:39936
	v_add_f32_dpp v50, v51, v50 quad_perm:[1,0,3,2] row_mask:0xf bank_mask:0xf bound_ctrl:1
	v_pk_mul_f32 v[18:19], v[12:13], v[12:13]
	v_pk_fma_f32 v[20:21], v[16:17], s[22:23], v[90:91] op_sel_hi:[1,0,0]
	v_cndmask_b32_e64 v51, v58, v50, s[6:7]
	v_cndmask_b32_e64 v50, v50, v58, s[6:7]
	v_mul_f32_e32 v18, 0xbf38aa3b, v18
	v_pk_fma_f32 v[20:21], v[16:17], v[20:21], s[24:25] op_sel_hi:[1,1,0]
	v_mul_f32_e32 v19, 0xbf38aa3b, v19
	v_add_f32_dpp v66, v67, v66 quad_perm:[2,3,0,1] row_mask:0xf bank_mask:0xf bound_ctrl:1
	v_add_f32_dpp v50, v51, v50 quad_perm:[2,3,0,1] row_mask:0xf bank_mask:0xf bound_ctrl:1
	v_exp_f32_e32 v18, v18
	v_pk_fma_f32 v[20:21], v[16:17], v[20:21], s[34:35] op_sel_hi:[1,1,0]
	v_exp_f32_e32 v19, v19
	v_cndmask_b32_e64 v51, v66, v50, s[8:9]
	v_pk_fma_f32 v[20:21], v[16:17], v[20:21], s[40:41] op_sel_hi:[1,1,0]
	v_mov_b32_e32 v52, v51
	v_and_b32_e32 v15, 0x7fffffff, v13
	v_and_b32_e32 v14, 0x7fffffff, v12
	v_pk_mul_f32 v[16:17], v[16:17], v[20:21]
	v_mov_b32_dpp v52, v52 row_shl:4 row_mask:0xf bank_mask:0x5
	v_max_f32_e32 v12, 0, v12
	v_max_f32_e32 v13, 0, v13
	v_pk_mul_f32 v[14:15], v[14:15], v[16:17]
	v_cndmask_b32_e64 v50, v50, v66, s[8:9]
	v_mov_b32_dpp v52, v51 row_shr:4 row_mask:0xf bank_mask:0xa
	v_pk_fma_f32 v[12:13], v[18:19], v[14:15], v[12:13] neg_lo:[1,0,0] neg_hi:[1,0,0]
	v_pk_fma_f32 v[10:11], v[10:11], v[240:241], v[244:245]
	v_add_f32_e32 v50, v50, v52
	v_cvt_pk_f16_f32 v12, v12, v13
	v_fma_f32 v13, |v10|, s25, 1.0
	v_add_f32_dpp v50, v50, v50 row_ror:8 row_mask:0xf bank_mask:0xf bound_ctrl:1
	v_rcp_f32_e32 v16, v13
	v_fma_f32 v13, |v11|, s25, 1.0
	v_mov_b32_e32 v51, v50
	v_rcp_f32_e32 v17, v13
	s_nop 0
	v_permlane16_swap_b32_e32 v50, v51
	v_add_f32_e32 v50, v50, v51
	v_mov_b32_e32 v51, v50
	v_pk_mul_f32 v[18:19], v[10:11], v[10:11]
	s_nop 0
	v_permlane32_swap_b32_e32 v50, v51
	v_mul_f32_e32 v13, 0xbf38aa3b, v18
	v_pk_fma_f32 v[20:21], v[16:17], s[22:23], v[90:91] op_sel_hi:[1,0,0]
	v_add_f32_e32 v50, v50, v51
	v_exp_f32_e32 v18, v13
	v_pk_fma_f32 v[20:21], v[16:17], v[20:21], s[24:25] op_sel_hi:[1,1,0]
	v_mul_f32_e32 v13, 0xbf38aa3b, v19
	v_addc_co_u32_e32 v157, vcc, 0, v83, vcc
	v_fmamk_f32 v50, v50, 0x3b800000, v116
	v_pk_fma_f32 v[20:21], v[16:17], v[20:21], s[34:35] op_sel_hi:[1,1,0]
	v_exp_f32_e32 v19, v13
	v_mul_f32_e32 v51, 0x4f800000, v50
	v_cmp_gt_f32_e32 vcc, s35, v50
	v_pk_fma_f32 v[20:21], v[16:17], v[20:21], s[40:41] op_sel_hi:[1,1,0]
	v_and_b32_e32 v15, 0x7fffffff, v11
	v_cndmask_b32_e32 v50, v50, v51, vcc
	v_and_b32_e32 v14, 0x7fffffff, v10
	v_pk_mul_f32 v[16:17], v[16:17], v[20:21]
	v_sqrt_f32_e32 v51, v50
	v_max_f32_e32 v10, 0, v10
	v_max_f32_e32 v11, 0, v11
	v_pk_mul_f32 v[14:15], v[14:15], v[16:17]
	v_add_u32_e32 v52, -1, v51
	v_pk_fma_f32 v[10:11], v[18:19], v[14:15], v[10:11] neg_lo:[1,0,0] neg_hi:[1,0,0]
	v_fma_f32 v53, -v52, v51, v50
	v_cvt_pk_f16_f32 v13, v10, v11
	v_bitop3_b32 v10, v86, s41, v88 bitop3:0x6c
	v_or3_b32 v146, v85, v10, v87
	v_lshlrev_b32_e32 v10, 4, v141
	v_and_or_b32 v147, v10, s41, v84
	v_lshlrev_b32_e32 v10, 4, v142
	v_and_or_b32 v148, v10, s41, v84
	v_lshlrev_b32_e32 v10, 4, v143
	v_cmp_ge_f32_e64 s[0:1], 0, v53
	v_add_u32_e32 v53, 1, v51
	v_and_or_b32 v149, v10, s41, v84
	v_bitop3_b32 v10, v125, v0, 15 bitop3:0x78
	v_cndmask_b32_e64 v52, v51, v52, s[0:1]
	v_fma_f32 v51, -v53, v51, v50
	v_lshl_or_b32 v150, v10, 4, v84
	v_bitop3_b32 v10, v125, v107, 4 bitop3:0x36
	v_cmp_lt_f32_e64 s[0:1], 0, v51
	v_lshl_or_b32 v151, v10, 4, v84
	v_bitop3_b32 v10, v125, v107, 8 bitop3:0x36
	v_cndmask_b32_e64 v51, v52, v53, s[0:1]
	v_lshl_or_b32 v152, v10, 4, v84
	v_bitop3_b32 v10, v125, v107, 12 bitop3:0x36
	v_mul_f32_e32 v52, 0x37800000, v51
	ds_write_b64 v146, v[12:13] offset:40448
	v_lshl_or_b32 v153, v10, 4, v84
	v_cndmask_b32_e32 v51, v51, v52, vcc
	v_cmp_class_f32_e32 vcc, v50, v117
	ds_read_b128 v[38:41], v115 offset:32768
	ds_read_b128 v[34:37], v147 offset:32768
	ds_read_b128 v[30:33], v148 offset:32768
	ds_read_b128 v[26:29], v149 offset:32768
	ds_read_b128 v[22:25], v150 offset:33024
	ds_read_b128 v[18:21], v151 offset:33024
	ds_read_b128 v[14:17], v152 offset:33024
	ds_read_b128 v[10:13], v153 offset:33024
	s_movk_i32 s57, 0x7000
	s_nop 1
	v_add_co_u32_e64 v236, s[60:61], s57, v82
	s_nop 1
	v_addc_co_u32_e64 v237, s[60:61], 0, v83, s[60:61]
	s_nop 1
	global_load_dwordx4 v[206:209], v[236:237], off offset:-3072 nt
	global_load_dwordx4 v[210:213], v[236:237], off offset:-2048 nt
	global_load_dwordx4 v[214:217], v[236:237], off offset:-1024 nt
	global_load_dwordx4 v[202:205], v[236:237], off offset:-4096 nt
	global_load_dwordx4 v[218:221], v[236:237], off nt
	v_cndmask_b32_e32 v154, v51, v50, vcc
	v_div_scale_f32 v155, s[0:1], v154, v154, 1.0
	v_rcp_f32_e32 v164, v155
	global_load_dwordx4 v[222:225], v[236:237], off offset:1024 nt
	global_load_dwordx4 v[226:229], v[236:237], off offset:2048 nt
	global_load_dwordx4 v[230:233], v[236:237], off offset:3072 nt
	v_fma_f32 v156, -v155, v164, 1.0
	v_fmac_f32_e32 v164, v156, v164
	v_div_scale_f32 v156, vcc, 1.0, v154, 1.0
	v_mul_f32_e32 v157, v156, v164
	v_fma_f32 v165, -v155, v157, v156
	v_fmac_f32_e32 v157, v165, v164
	v_fma_f32 v155, -v155, v157, v156
	v_div_fmas_f32 v155, v155, v164, v157
	v_div_fixup_f32 v154, v155, v154, 1.0
	s_nop 0
	v_readlane_b32 s0, v154, 0
	s_nop 1
	v_pk_mul_f32 v[156:157], s[0:1], v[158:159] op_sel_hi:[0,1]
	v_pk_fma_f32 v[156:157], v[156:157], v[238:239], v[242:243]
	s_nop 0
	v_fma_f32 v155, |v156|, s25, 1.0
	v_rcp_f32_e32 v164, v155
	v_fma_f32 v155, |v157|, s25, 1.0
	v_rcp_f32_e32 v165, v155
	v_pk_mul_f32 v[166:167], v[156:157], v[156:157]
	v_and_b32_e32 v159, 0x7fffffff, v157
	v_mul_f32_e32 v155, 0xbf38aa3b, v166
	v_pk_fma_f32 v[168:169], v[164:165], s[22:23], v[90:91] op_sel_hi:[1,0,0]
	v_exp_f32_e32 v166, v155
	v_pk_fma_f32 v[168:169], v[164:165], v[168:169], s[24:25] op_sel_hi:[1,1,0]
	v_mul_f32_e32 v155, 0xbf38aa3b, v167
	v_pk_fma_f32 v[168:169], v[164:165], v[168:169], s[34:35] op_sel_hi:[1,1,0]
	v_exp_f32_e32 v167, v155
	v_pk_fma_f32 v[168:169], v[164:165], v[168:169], s[40:41] op_sel_hi:[1,1,0]
	v_and_b32_e32 v158, 0x7fffffff, v156
	v_pk_mul_f32 v[164:165], v[164:165], v[168:169]
	v_max_f32_e32 v156, 0, v156
	v_max_f32_e32 v157, 0, v157
	v_pk_mul_f32 v[158:159], v[158:159], v[164:165]
	s_nop 0
	v_pk_fma_f32 v[156:157], v[166:167], v[158:159], v[156:157] neg_lo:[1,0,0] neg_hi:[1,0,0]
	v_pk_mul_f32 v[158:159], s[0:1], v[160:161] op_sel_hi:[0,1]
	v_pk_fma_f32 v[158:159], v[158:159], v[240:241], v[244:245]
	v_cvt_pk_f16_f32 v156, v156, v157
	v_fma_f32 v155, |v158|, s25, 1.0
	v_rcp_f32_e32 v164, v155
	v_fma_f32 v155, |v159|, s25, 1.0
	v_rcp_f32_e32 v165, v155
	v_pk_mul_f32 v[166:167], v[158:159], v[158:159]
	v_and_b32_e32 v161, 0x7fffffff, v159
	v_mul_f32_e32 v155, 0xbf38aa3b, v166
	v_pk_fma_f32 v[168:169], v[164:165], s[22:23], v[90:91] op_sel_hi:[1,0,0]
	v_exp_f32_e32 v166, v155
	v_pk_fma_f32 v[168:169], v[164:165], v[168:169], s[24:25] op_sel_hi:[1,1,0]
	v_mul_f32_e32 v155, 0xbf38aa3b, v167
	v_pk_fma_f32 v[168:169], v[164:165], v[168:169], s[34:35] op_sel_hi:[1,1,0]
	v_exp_f32_e32 v167, v155
	v_pk_fma_f32 v[168:169], v[164:165], v[168:169], s[40:41] op_sel_hi:[1,1,0]
	v_and_b32_e32 v160, 0x7fffffff, v158
	v_pk_mul_f32 v[164:165], v[164:165], v[168:169]
	v_max_f32_e32 v158, 0, v158
	v_max_f32_e32 v159, 0, v159
	v_pk_mul_f32 v[160:161], v[160:161], v[164:165]
	v_readlane_b32 s0, v154, 1
	v_pk_fma_f32 v[158:159], v[166:167], v[160:161], v[158:159] neg_lo:[1,0,0] neg_hi:[1,0,0]
	s_nop 0
	v_cvt_pk_f16_f32 v157, v158, v159
	ds_write_b64 v140, v[156:157] offset:32768
	v_pk_mul_f32 v[156:157], s[0:1], v[162:163] op_sel_hi:[0,1]
	v_pk_fma_f32 v[156:157], v[156:157], v[238:239], v[242:243]
	v_pk_mul_f32 v[110:111], s[0:1], v[110:111] op_sel_hi:[0,1]
	v_fma_f32 v140, |v156|, s25, 1.0
	v_rcp_f32_e32 v160, v140
	v_fma_f32 v140, |v157|, s25, 1.0
	v_rcp_f32_e32 v161, v140
	v_pk_mul_f32 v[162:163], v[156:157], v[156:157]
	v_pk_fma_f32 v[110:111], v[110:111], v[240:241], v[244:245]
	v_mul_f32_e32 v140, 0xbf38aa3b, v162
	v_pk_fma_f32 v[164:165], v[160:161], s[22:23], v[90:91] op_sel_hi:[1,0,0]
	v_exp_f32_e32 v162, v140
	v_pk_fma_f32 v[164:165], v[160:161], v[164:165], s[24:25] op_sel_hi:[1,1,0]
	v_mul_f32_e32 v140, 0xbf38aa3b, v163
	v_pk_fma_f32 v[164:165], v[160:161], v[164:165], s[34:35] op_sel_hi:[1,1,0]
	v_and_b32_e32 v159, 0x7fffffff, v157
	v_pk_fma_f32 v[164:165], v[160:161], v[164:165], s[40:41] op_sel_hi:[1,1,0]
	v_and_b32_e32 v158, 0x7fffffff, v156
	v_exp_f32_e32 v163, v140
	v_pk_mul_f32 v[160:161], v[160:161], v[164:165]
	v_fma_f32 v140, |v110|, s25, 1.0
	v_pk_mul_f32 v[158:159], v[158:159], v[160:161]
	v_rcp_f32_e32 v160, v140
	v_fma_f32 v140, |v111|, s25, 1.0
	v_rcp_f32_e32 v161, v140
	v_max_f32_e32 v156, 0, v156
	v_max_f32_e32 v157, 0, v157
	v_pk_fma_f32 v[156:157], v[162:163], v[158:159], v[156:157] neg_lo:[1,0,0] neg_hi:[1,0,0]
	v_pk_mul_f32 v[162:163], v[110:111], v[110:111]
	v_pk_fma_f32 v[164:165], v[160:161], s[22:23], v[90:91] op_sel_hi:[1,0,0]
	v_mul_f32_e32 v140, 0xbf38aa3b, v162
	v_exp_f32_e32 v162, v140
	v_pk_fma_f32 v[164:165], v[160:161], v[164:165], s[24:25] op_sel_hi:[1,1,0]
	v_mul_f32_e32 v140, 0xbf38aa3b, v163
	v_pk_fma_f32 v[164:165], v[160:161], v[164:165], s[34:35] op_sel_hi:[1,1,0]
	v_exp_f32_e32 v163, v140
	v_pk_fma_f32 v[164:165], v[160:161], v[164:165], s[40:41] op_sel_hi:[1,1,0]
	v_and_b32_e32 v159, 0x7fffffff, v111
	v_and_b32_e32 v158, 0x7fffffff, v110
	v_pk_mul_f32 v[160:161], v[160:161], v[164:165]
	v_max_f32_e32 v110, 0, v110
	v_max_f32_e32 v111, 0, v111
	v_pk_mul_f32 v[158:159], v[158:159], v[160:161]
	v_readlane_b32 s0, v154, 2
	v_pk_fma_f32 v[110:111], v[162:163], v[158:159], v[110:111] neg_lo:[1,0,0] neg_hi:[1,0,0]
	v_cvt_pk_f16_f32 v156, v156, v157
	v_pk_mul_f32 v[108:109], s[0:1], v[108:109] op_sel_hi:[0,1]
	v_cvt_pk_f16_f32 v157, v110, v111
	v_pk_fma_f32 v[108:109], v[108:109], v[238:239], v[242:243]
	ds_write_b64 v138, v[156:157] offset:33280
	v_fma_f32 v138, |v108|, s25, 1.0
	v_rcp_f32_e32 v156, v138
	v_fma_f32 v138, |v109|, s25, 1.0
	v_rcp_f32_e32 v157, v138
	v_pk_mul_f32 v[158:159], v[108:109], v[108:109]
	v_and_b32_e32 v111, 0x7fffffff, v109
	v_mul_f32_e32 v138, 0xbf38aa3b, v158
	v_pk_fma_f32 v[160:161], v[156:157], s[22:23], v[90:91] op_sel_hi:[1,0,0]
	v_exp_f32_e32 v158, v138
	v_pk_fma_f32 v[160:161], v[156:157], v[160:161], s[24:25] op_sel_hi:[1,1,0]
	v_mul_f32_e32 v138, 0xbf38aa3b, v159
	v_pk_fma_f32 v[160:161], v[156:157], v[160:161], s[34:35] op_sel_hi:[1,1,0]
	v_exp_f32_e32 v159, v138
	v_pk_fma_f32 v[160:161], v[156:157], v[160:161], s[40:41] op_sel_hi:[1,1,0]
	v_and_b32_e32 v110, 0x7fffffff, v108
	v_pk_mul_f32 v[156:157], v[156:157], v[160:161]
	v_max_f32_e32 v108, 0, v108
	v_max_f32_e32 v109, 0, v109
	v_pk_mul_f32 v[110:111], v[110:111], v[156:157]
	v_pk_mul_f32 v[104:105], s[0:1], v[104:105] op_sel_hi:[0,1]
	v_pk_fma_f32 v[108:109], v[158:159], v[110:111], v[108:109] neg_lo:[1,0,0] neg_hi:[1,0,0]
	v_pk_fma_f32 v[104:105], v[104:105], v[240:241], v[244:245]
	v_cvt_pk_f16_f32 v108, v108, v109
	v_fma_f32 v109, |v104|, s25, 1.0
	v_rcp_f32_e32 v156, v109
	v_fma_f32 v109, |v105|, s25, 1.0
	v_rcp_f32_e32 v157, v109
	v_pk_mul_f32 v[158:159], v[104:105], v[104:105]
	v_and_b32_e32 v111, 0x7fffffff, v105
	v_mul_f32_e32 v109, 0xbf38aa3b, v158
	v_pk_fma_f32 v[160:161], v[156:157], s[22:23], v[90:91] op_sel_hi:[1,0,0]
	v_exp_f32_e32 v158, v109
	v_pk_fma_f32 v[160:161], v[156:157], v[160:161], s[24:25] op_sel_hi:[1,1,0]
	v_mul_f32_e32 v109, 0xbf38aa3b, v159
	v_pk_fma_f32 v[160:161], v[156:157], v[160:161], s[34:35] op_sel_hi:[1,1,0]
	v_exp_f32_e32 v159, v109
	v_pk_fma_f32 v[160:161], v[156:157], v[160:161], s[40:41] op_sel_hi:[1,1,0]
	v_and_b32_e32 v110, 0x7fffffff, v104
	v_pk_mul_f32 v[156:157], v[156:157], v[160:161]
	v_max_f32_e32 v104, 0, v104
	v_max_f32_e32 v105, 0, v105
	v_pk_mul_f32 v[110:111], v[110:111], v[156:157]
	v_readlane_b32 s0, v154, 3
	v_pk_fma_f32 v[104:105], v[158:159], v[110:111], v[104:105] neg_lo:[1,0,0] neg_hi:[1,0,0]
	s_nop 0
	v_pk_mul_f32 v[102:103], s[0:1], v[102:103] op_sel_hi:[0,1]
	v_cvt_pk_f16_f32 v109, v104, v105
	v_pk_fma_f32 v[102:103], v[102:103], v[238:239], v[242:243]
	ds_write_b64 v135, v[108:109] offset:33792
	v_fma_f32 v108, |v102|, s25, 1.0
	v_fma_f32 v109, |v103|, s25, 1.0
	v_rcp_f32_e32 v108, v108
	v_rcp_f32_e32 v109, v109
	v_pk_mul_f32 v[110:111], v[102:103], v[102:103]
	v_and_b32_e32 v105, 0x7fffffff, v103
	v_mul_f32_e32 v110, 0xbf38aa3b, v110
	v_pk_fma_f32 v[156:157], v[108:109], s[22:23], v[90:91] op_sel_hi:[1,0,0]
	v_mul_f32_e32 v111, 0xbf38aa3b, v111
	v_pk_fma_f32 v[156:157], v[108:109], v[156:157], s[24:25] op_sel_hi:[1,1,0]
	v_exp_f32_e32 v110, v110
	v_pk_fma_f32 v[156:157], v[108:109], v[156:157], s[34:35] op_sel_hi:[1,1,0]
	v_exp_f32_e32 v111, v111
	v_pk_fma_f32 v[156:157], v[108:109], v[156:157], s[40:41] op_sel_hi:[1,1,0]
	v_and_b32_e32 v104, 0x7fffffff, v102
	v_pk_mul_f32 v[108:109], v[108:109], v[156:157]
	v_max_f32_e32 v102, 0, v102
	v_max_f32_e32 v103, 0, v103
	v_pk_mul_f32 v[104:105], v[104:105], v[108:109]
	v_pk_mul_f32 v[100:101], s[0:1], v[100:101] op_sel_hi:[0,1]
	v_pk_fma_f32 v[102:103], v[110:111], v[104:105], v[102:103] neg_lo:[1,0,0] neg_hi:[1,0,0]
	v_pk_fma_f32 v[100:101], v[100:101], v[240:241], v[244:245]
	v_cvt_pk_f16_f32 v102, v102, v103
	v_fma_f32 v103, |v100|, s25, 1.0
	v_rcp_f32_e32 v108, v103
	v_fma_f32 v103, |v101|, s25, 1.0
	v_rcp_f32_e32 v109, v103
	v_pk_mul_f32 v[110:111], v[100:101], v[100:101]
	v_and_b32_e32 v105, 0x7fffffff, v101
	v_mul_f32_e32 v103, 0xbf38aa3b, v110
	v_pk_fma_f32 v[156:157], v[108:109], s[22:23], v[90:91] op_sel_hi:[1,0,0]
	v_exp_f32_e32 v110, v103
	v_pk_fma_f32 v[156:157], v[108:109], v[156:157], s[24:25] op_sel_hi:[1,1,0]
	v_mul_f32_e32 v103, 0xbf38aa3b, v111
	v_pk_fma_f32 v[156:157], v[108:109], v[156:157], s[34:35] op_sel_hi:[1,1,0]
	v_exp_f32_e32 v111, v103
	v_pk_fma_f32 v[156:157], v[108:109], v[156:157], s[40:41] op_sel_hi:[1,1,0]
	v_and_b32_e32 v104, 0x7fffffff, v100
	v_pk_mul_f32 v[108:109], v[108:109], v[156:157]
	v_max_f32_e32 v100, 0, v100
	v_max_f32_e32 v101, 0, v101
	v_pk_mul_f32 v[104:105], v[104:105], v[108:109]
	v_readlane_b32 s0, v154, 4
	v_pk_fma_f32 v[100:101], v[110:111], v[104:105], v[100:101] neg_lo:[1,0,0] neg_hi:[1,0,0]
	s_nop 0
	v_pk_mul_f32 v[98:99], s[0:1], v[98:99] op_sel_hi:[0,1]
	v_cvt_pk_f16_f32 v103, v100, v101
	v_pk_fma_f32 v[98:99], v[98:99], v[238:239], v[242:243]
	ds_write_b64 v134, v[102:103] offset:34304
	v_fma_f32 v102, |v98|, s25, 1.0
	v_fma_f32 v103, |v99|, s25, 1.0
	v_rcp_f32_e32 v102, v102
	v_rcp_f32_e32 v103, v103
	v_pk_mul_f32 v[104:105], v[98:99], v[98:99]
	v_and_b32_e32 v101, 0x7fffffff, v99
	v_mul_f32_e32 v104, 0xbf38aa3b, v104
	v_pk_fma_f32 v[108:109], v[102:103], s[22:23], v[90:91] op_sel_hi:[1,0,0]
	v_mul_f32_e32 v105, 0xbf38aa3b, v105
	v_pk_fma_f32 v[108:109], v[102:103], v[108:109], s[24:25] op_sel_hi:[1,1,0]
	v_exp_f32_e32 v104, v104
	v_pk_fma_f32 v[108:109], v[102:103], v[108:109], s[34:35] op_sel_hi:[1,1,0]
	v_exp_f32_e32 v105, v105
	v_pk_fma_f32 v[108:109], v[102:103], v[108:109], s[40:41] op_sel_hi:[1,1,0]
	v_and_b32_e32 v100, 0x7fffffff, v98
	v_pk_mul_f32 v[102:103], v[102:103], v[108:109]
	v_max_f32_e32 v98, 0, v98
	v_max_f32_e32 v99, 0, v99
	v_pk_mul_f32 v[100:101], v[100:101], v[102:103]
	v_pk_mul_f32 v[96:97], s[0:1], v[96:97] op_sel_hi:[0,1]
	v_pk_fma_f32 v[98:99], v[104:105], v[100:101], v[98:99] neg_lo:[1,0,0] neg_hi:[1,0,0]
	v_pk_fma_f32 v[96:97], v[96:97], v[240:241], v[244:245]
	v_cvt_pk_f16_f32 v98, v98, v99
	v_fma_f32 v99, |v96|, s25, 1.0
	v_rcp_f32_e32 v102, v99
	v_fma_f32 v99, |v97|, s25, 1.0
	v_rcp_f32_e32 v103, v99
	v_pk_mul_f32 v[104:105], v[96:97], v[96:97]
	v_and_b32_e32 v101, 0x7fffffff, v97
	v_mul_f32_e32 v99, 0xbf38aa3b, v104
	v_pk_fma_f32 v[108:109], v[102:103], s[22:23], v[90:91] op_sel_hi:[1,0,0]
	v_exp_f32_e32 v104, v99
	v_pk_fma_f32 v[108:109], v[102:103], v[108:109], s[24:25] op_sel_hi:[1,1,0]
	v_mul_f32_e32 v99, 0xbf38aa3b, v105
	v_pk_fma_f32 v[108:109], v[102:103], v[108:109], s[34:35] op_sel_hi:[1,1,0]
	v_exp_f32_e32 v105, v99
	v_pk_fma_f32 v[108:109], v[102:103], v[108:109], s[40:41] op_sel_hi:[1,1,0]
	v_and_b32_e32 v100, 0x7fffffff, v96
	v_pk_mul_f32 v[102:103], v[102:103], v[108:109]
	v_max_f32_e32 v96, 0, v96
	v_max_f32_e32 v97, 0, v97
	v_pk_mul_f32 v[100:101], v[100:101], v[102:103]
	v_readlane_b32 s0, v154, 5
	v_pk_fma_f32 v[96:97], v[104:105], v[100:101], v[96:97] neg_lo:[1,0,0] neg_hi:[1,0,0]
	v_mov_b32_e32 v104, 0
	v_pk_mul_f32 v[94:95], s[0:1], v[94:95] op_sel_hi:[0,1]
	v_cvt_pk_f16_f32 v99, v96, v97
	v_pk_fma_f32 v[94:95], v[94:95], v[238:239], v[242:243]
	ds_write_b64 v120, v[98:99] offset:34816
	v_fma_f32 v98, |v94|, s25, 1.0
	v_fma_f32 v99, |v95|, s25, 1.0
	v_rcp_f32_e32 v98, v98
	v_rcp_f32_e32 v99, v99
	v_pk_mul_f32 v[100:101], v[94:95], v[94:95]
	v_and_b32_e32 v97, 0x7fffffff, v95
	v_mul_f32_e32 v100, 0xbf38aa3b, v100
	v_pk_fma_f32 v[102:103], v[98:99], s[22:23], v[90:91] op_sel_hi:[1,0,0]
	v_mul_f32_e32 v101, 0xbf38aa3b, v101
	v_pk_fma_f32 v[102:103], v[98:99], v[102:103], s[24:25] op_sel_hi:[1,1,0]
	v_exp_f32_e32 v100, v100
	v_pk_fma_f32 v[102:103], v[98:99], v[102:103], s[34:35] op_sel_hi:[1,1,0]
	v_exp_f32_e32 v101, v101
	v_pk_fma_f32 v[102:103], v[98:99], v[102:103], s[40:41] op_sel_hi:[1,1,0]
	v_and_b32_e32 v96, 0x7fffffff, v94
	v_pk_mul_f32 v[98:99], v[98:99], v[102:103]
	v_max_f32_e32 v94, 0, v94
	v_max_f32_e32 v95, 0, v95
	v_pk_mul_f32 v[96:97], v[96:97], v[98:99]
	v_pk_mul_f32 v[92:93], s[0:1], v[92:93] op_sel_hi:[0,1]
	v_pk_fma_f32 v[94:95], v[100:101], v[96:97], v[94:95] neg_lo:[1,0,0] neg_hi:[1,0,0]
	v_pk_fma_f32 v[92:93], v[92:93], v[240:241], v[244:245]
	v_cvt_pk_f16_f32 v94, v94, v95
	v_fma_f32 v95, |v92|, s25, 1.0
	v_rcp_f32_e32 v98, v95
	v_fma_f32 v95, |v93|, s25, 1.0
	v_rcp_f32_e32 v99, v95
	v_pk_mul_f32 v[100:101], v[92:93], v[92:93]
	v_and_b32_e32 v97, 0x7fffffff, v93
	v_mul_f32_e32 v95, 0xbf38aa3b, v100
	v_pk_fma_f32 v[102:103], v[98:99], s[22:23], v[90:91] op_sel_hi:[1,0,0]
	v_exp_f32_e32 v100, v95
	v_pk_fma_f32 v[102:103], v[98:99], v[102:103], s[24:25] op_sel_hi:[1,1,0]
	v_mul_f32_e32 v95, 0xbf38aa3b, v101
	v_pk_fma_f32 v[102:103], v[98:99], v[102:103], s[34:35] op_sel_hi:[1,1,0]
	v_exp_f32_e32 v101, v95
	v_pk_fma_f32 v[102:103], v[98:99], v[102:103], s[40:41] op_sel_hi:[1,1,0]
	v_and_b32_e32 v96, 0x7fffffff, v92
	v_pk_mul_f32 v[98:99], v[98:99], v[102:103]
	v_max_f32_e32 v92, 0, v92
	v_max_f32_e32 v93, 0, v93
	v_pk_mul_f32 v[96:97], v[96:97], v[98:99]
	v_readlane_b32 s0, v154, 6
	v_pk_fma_f32 v[92:93], v[100:101], v[96:97], v[92:93] neg_lo:[1,0,0] neg_hi:[1,0,0]
	s_waitcnt vmcnt(1)
	v_add_f32_e32 v100, v228, v229
	v_pk_mul_f32 v[80:81], s[0:1], v[80:81] op_sel_hi:[0,1]
	v_cvt_pk_f16_f32 v95, v92, v93
	v_pk_fma_f32 v[80:81], v[80:81], v[238:239], v[242:243]
	ds_write_b64 v121, v[94:95] offset:35328
	v_fma_f32 v94, |v80|, s25, 1.0
	v_fma_f32 v95, |v81|, s25, 1.0
	v_rcp_f32_e32 v94, v94
	v_rcp_f32_e32 v95, v95
	v_pk_mul_f32 v[96:97], v[80:81], v[80:81]
	v_and_b32_e32 v93, 0x7fffffff, v81
	v_mul_f32_e32 v96, 0xbf38aa3b, v96
	v_pk_fma_f32 v[98:99], v[94:95], s[22:23], v[90:91] op_sel_hi:[1,0,0]
	v_mul_f32_e32 v97, 0xbf38aa3b, v97
	v_pk_fma_f32 v[98:99], v[94:95], v[98:99], s[24:25] op_sel_hi:[1,1,0]
	v_exp_f32_e32 v96, v96
	v_pk_fma_f32 v[98:99], v[94:95], v[98:99], s[34:35] op_sel_hi:[1,1,0]
	v_exp_f32_e32 v97, v97
	v_pk_fma_f32 v[98:99], v[94:95], v[98:99], s[40:41] op_sel_hi:[1,1,0]
	v_and_b32_e32 v92, 0x7fffffff, v80
	v_pk_mul_f32 v[94:95], v[94:95], v[98:99]
	v_max_f32_e32 v80, 0, v80
	v_max_f32_e32 v81, 0, v81
	v_pk_mul_f32 v[92:93], v[92:93], v[94:95]
	v_pk_mul_f32 v[78:79], s[0:1], v[78:79] op_sel_hi:[0,1]
	v_pk_fma_f32 v[80:81], v[96:97], v[92:93], v[80:81] neg_lo:[1,0,0] neg_hi:[1,0,0]
	v_pk_fma_f32 v[78:79], v[78:79], v[240:241], v[244:245]
	v_cvt_pk_f16_f32 v80, v80, v81
	v_fma_f32 v81, |v78|, s25, 1.0
	v_rcp_f32_e32 v94, v81
	v_fma_f32 v81, |v79|, s25, 1.0
	v_rcp_f32_e32 v95, v81
	v_pk_mul_f32 v[96:97], v[78:79], v[78:79]
	v_and_b32_e32 v93, 0x7fffffff, v79
	v_mul_f32_e32 v81, 0xbf38aa3b, v96
	v_pk_fma_f32 v[98:99], v[94:95], s[22:23], v[90:91] op_sel_hi:[1,0,0]
	v_exp_f32_e32 v96, v81
	v_pk_fma_f32 v[98:99], v[94:95], v[98:99], s[24:25] op_sel_hi:[1,1,0]
	v_mul_f32_e32 v81, 0xbf38aa3b, v97
	v_pk_fma_f32 v[98:99], v[94:95], v[98:99], s[34:35] op_sel_hi:[1,1,0]
	v_exp_f32_e32 v97, v81
	v_pk_fma_f32 v[98:99], v[94:95], v[98:99], s[40:41] op_sel_hi:[1,1,0]
	v_and_b32_e32 v92, 0x7fffffff, v78
	v_pk_mul_f32 v[94:95], v[94:95], v[98:99]
	v_max_f32_e32 v78, 0, v78
	v_max_f32_e32 v79, 0, v79
	v_pk_mul_f32 v[92:93], v[92:93], v[94:95]
	v_readlane_b32 s0, v154, 7
	v_pk_fma_f32 v[78:79], v[96:97], v[92:93], v[78:79] neg_lo:[1,0,0] neg_hi:[1,0,0]
	v_add_f32_e32 v97, v224, v225
	v_pk_mul_f32 v[76:77], s[0:1], v[76:77] op_sel_hi:[0,1]
	v_cvt_pk_f16_f32 v81, v78, v79
	v_pk_fma_f32 v[76:77], v[76:77], v[238:239], v[242:243]
	ds_write_b64 v118, v[80:81] offset:35840
	v_fma_f32 v80, |v76|, s25, 1.0
	v_fma_f32 v81, |v77|, s25, 1.0
	v_rcp_f32_e32 v80, v80
	v_rcp_f32_e32 v81, v81
	v_pk_mul_f32 v[92:93], v[76:77], v[76:77]
	v_and_b32_e32 v79, 0x7fffffff, v77
	v_mul_f32_e32 v92, 0xbf38aa3b, v92
	v_pk_fma_f32 v[94:95], v[80:81], s[22:23], v[90:91] op_sel_hi:[1,0,0]
	v_mul_f32_e32 v93, 0xbf38aa3b, v93
	v_pk_fma_f32 v[94:95], v[80:81], v[94:95], s[24:25] op_sel_hi:[1,1,0]
	v_exp_f32_e32 v92, v92
	v_pk_fma_f32 v[94:95], v[80:81], v[94:95], s[34:35] op_sel_hi:[1,1,0]
	v_exp_f32_e32 v93, v93
	v_pk_fma_f32 v[94:95], v[80:81], v[94:95], s[40:41] op_sel_hi:[1,1,0]
	v_and_b32_e32 v78, 0x7fffffff, v76
	v_pk_mul_f32 v[80:81], v[80:81], v[94:95]
	v_max_f32_e32 v76, 0, v76
	v_max_f32_e32 v77, 0, v77
	v_pk_mul_f32 v[78:79], v[78:79], v[80:81]
	v_pk_mul_f32 v[74:75], s[0:1], v[74:75] op_sel_hi:[0,1]
	v_pk_fma_f32 v[76:77], v[92:93], v[78:79], v[76:77] neg_lo:[1,0,0] neg_hi:[1,0,0]
	v_pk_fma_f32 v[92:93], v[74:75], v[240:241], v[244:245]
	v_cvt_pk_f16_f32 v80, v76, v77
	v_fma_f32 v74, |v92|, s25, 1.0
	v_fma_f32 v75, |v93|, s25, 1.0
	v_rcp_f32_e32 v74, v74
	v_rcp_f32_e32 v75, v75
	v_pk_mul_f32 v[76:77], v[92:93], v[92:93]
	s_waitcnt vmcnt(0)
	v_add_f32_e32 v101, v232, v233
	v_mul_f32_e32 v76, 0xbf38aa3b, v76
	v_pk_fma_f32 v[78:79], v[74:75], s[22:23], v[90:91] op_sel_hi:[1,0,0]
	v_exp_f32_e32 v96, v76
	v_pk_fma_f32 v[78:79], v[74:75], v[78:79], s[24:25] op_sel_hi:[1,1,0]
	v_add_f32_e32 v76, v208, v209
	v_pk_fma_f32 v[78:79], v[74:75], v[78:79], s[34:35] op_sel_hi:[1,1,0]
	v_mul_f32_e32 v81, 0xbf38aa3b, v77
	v_pk_fma_f32 v[78:79], v[74:75], v[78:79], s[40:41] op_sel_hi:[1,1,0]
	v_add_f32_e32 v77, v212, v213
	v_pk_mul_f32 v[98:99], v[74:75], v[78:79]
	v_add_f32_e32 v74, v202, v203
	v_add_f32_e32 v75, v204, v205
	v_add_f32_e32 v74, v74, v75
	v_add_f32_e32 v75, v206, v207
	v_add_f32_e32 v75, v75, v76
	v_add_f32_e32 v76, v210, v211
	v_add_f32_e32 v76, v76, v77
	v_add_f32_e32 v77, v214, v215
	v_add_f32_e32 v78, v216, v217
	v_add_f32_e32 v77, v77, v78
	v_add_f32_e32 v78, v218, v219
	v_add_f32_e32 v79, v220, v221
	v_add_f32_e32 v78, v78, v79
	v_add_f32_e32 v79, v222, v223
	v_add_f32_e32 v79, v79, v97
	v_add_f32_e32 v97, v226, v227
	v_add_f32_e32 v97, v97, v100
	v_add_f32_e32 v100, v230, v231
	v_add_f32_e32 v100, v100, v101
	v_cndmask_b32_e64 v101, v75, v74, s[4:5]
	v_cndmask_b32_e64 v74, v74, v75, s[4:5]
	v_cndmask_b32_e64 v75, v77, v76, s[4:5]
	v_cndmask_b32_e64 v76, v76, v77, s[4:5]
	v_cndmask_b32_e64 v77, v78, v79, s[4:5]
	v_add_f32_dpp v74, v101, v74 quad_perm:[1,0,3,2] row_mask:0xf bank_mask:0xf bound_ctrl:1
	v_add_f32_dpp v75, v75, v76 quad_perm:[1,0,3,2] row_mask:0xf bank_mask:0xf bound_ctrl:1
	v_cndmask_b32_e64 v76, v79, v78, s[4:5]
	v_cndmask_b32_e64 v78, v97, v100, s[4:5]
	v_and_b32_e32 v95, 0x7fffffff, v93
	v_add_f32_dpp v76, v76, v77 quad_perm:[1,0,3,2] row_mask:0xf bank_mask:0xf bound_ctrl:1
	v_cndmask_b32_e64 v77, v100, v97, s[4:5]
	v_exp_f32_e32 v97, v81
	v_and_b32_e32 v94, 0x7fffffff, v92
	v_add_f32_dpp v77, v77, v78 quad_perm:[1,0,3,2] row_mask:0xf bank_mask:0xf bound_ctrl:1
	v_cndmask_b32_e64 v78, v74, v75, s[6:7]
	v_cndmask_b32_e64 v74, v75, v74, s[6:7]
	v_cndmask_b32_e64 v75, v76, v77, s[6:7]
	v_cndmask_b32_e64 v76, v77, v76, s[6:7]
	v_add_f32_dpp v74, v78, v74 quad_perm:[2,3,0,1] row_mask:0xf bank_mask:0xf bound_ctrl:1
	v_max_f32_e32 v92, 0, v92
	v_add_f32_dpp v75, v75, v76 quad_perm:[2,3,0,1] row_mask:0xf bank_mask:0xf bound_ctrl:1
	v_cndmask_b32_e64 v76, v74, v75, s[8:9]
	v_cndmask_b32_e64 v74, v75, v74, s[8:9]
	v_mov_b32_e32 v75, v76
	v_max_f32_e32 v93, 0, v93
	s_waitcnt lgkmcnt(14)
	v_dot2c_f32_f16_e32 v104, v38, v38
	v_mov_b32_dpp v75, v75 row_shl:4 row_mask:0xf bank_mask:0x5
	v_mov_b32_e32 v105, 0
	v_dot2c_f32_f16_e32 v104, v39, v39
	v_mov_b32_dpp v75, v76 row_shr:4 row_mask:0xf bank_mask:0xa
	v_add_f32_e32 v74, v74, v75
	v_dot2c_f32_f16_e32 v104, v40, v40
	v_dot2c_f32_f16_e32 v104, v41, v41
	v_add_f32_dpp v74, v74, v74 row_ror:8 row_mask:0xf bank_mask:0xf bound_ctrl:1
	v_mov_b32_e32 v75, v74
	s_nop 1
	v_permlane16_swap_b32_e32 v74, v75
	v_add_f32_e32 v74, v74, v75
	v_mov_b32_e32 v75, v74
	s_nop 1
	v_permlane32_swap_b32_e32 v74, v75
	v_add_f32_e32 v74, v74, v75
	v_mul_f32_e32 v74, 0x3b800000, v74
	s_waitcnt lgkmcnt(13)
	v_dot2c_f32_f16_e32 v104, v34, v34
	v_readlane_b32 s42, v74, 0
	v_readlane_b32 s44, v74, 1
	v_readlane_b32 s46, v74, 2
	v_pk_add_f32 v[102:103], v[204:205], s[42:43] op_sel_hi:[1, 0] neg_lo:[0, 1] neg_hi:[0, 1]
	v_pk_add_f32 v[78:79], v[208:209], s[44:45] op_sel_hi:[1, 0] neg_lo:[0, 1] neg_hi:[0, 1]
	v_pk_add_f32 v[100:101], v[202:203], s[42:43] op_sel_hi:[1, 0] neg_lo:[0, 1] neg_hi:[0, 1]
	v_mul_f32_e32 v70, v103, v103
	v_mul_f32_e32 v71, v79, v79
	v_fmac_f32_e32 v70, v102, v102
	v_pk_add_f32 v[86:87], v[206:207], s[44:45] op_sel_hi:[1, 0] neg_lo:[0, 1] neg_hi:[0, 1]
	v_fmac_f32_e32 v71, v78, v78
	v_fmac_f32_e32 v70, v101, v101
	v_fmac_f32_e32 v71, v87, v87
	v_fmac_f32_e32 v70, v100, v100
	v_fmac_f32_e32 v71, v86, v86
	v_readlane_b32 s48, v74, 3
	v_cndmask_b32_e64 v72, v71, v70, s[4:5]
	v_cndmask_b32_e64 v70, v70, v71, s[4:5]
	v_readlane_b32 s50, v74, 4
	v_readlane_b32 s52, v74, 5
	v_readlane_b32 s54, v74, 6
	v_readlane_b32 s0, v74, 7
	v_add_f32_dpp v88, v72, v70 quad_perm:[1,0,3,2] row_mask:0xf bank_mask:0xf bound_ctrl:1
	v_pk_add_f32 v[74:75], v[212:213], s[46:47] op_sel_hi:[1, 0] neg_lo:[0, 1] neg_hi:[0, 1]
	v_pk_add_f32 v[70:71], v[216:217], s[48:49] op_sel_hi:[1, 0] neg_lo:[0, 1] neg_hi:[0, 1]
	v_pk_add_f32 v[76:77], v[210:211], s[46:47] op_sel_hi:[1, 0] neg_lo:[0, 1] neg_hi:[0, 1]
	v_mul_f32_e32 v82, v75, v75
	v_pk_add_f32 v[72:73], v[214:215], s[48:49] op_sel_hi:[1, 0] neg_lo:[0, 1] neg_hi:[0, 1]
	v_mul_f32_e32 v66, v71, v71
	v_fmac_f32_e32 v82, v74, v74
	v_fmac_f32_e32 v66, v70, v70
	v_fmac_f32_e32 v82, v77, v77
	v_fmac_f32_e32 v66, v73, v73
	v_fmac_f32_e32 v82, v76, v76
	v_fmac_f32_e32 v66, v72, v72
	v_cndmask_b32_e64 v67, v66, v82, s[4:5]
	v_cndmask_b32_e64 v66, v82, v66, s[4:5]
	v_pk_add_f32 v[68:69], v[218:219], s[50:51] op_sel_hi:[1, 0] neg_lo:[0, 1] neg_hi:[0, 1]
	v_pk_add_f32 v[62:63], v[222:223], s[52:53] op_sel_hi:[1, 0] neg_lo:[0, 1] neg_hi:[0, 1]
	v_add_f32_dpp v66, v67, v66 quad_perm:[1,0,3,2] row_mask:0xf bank_mask:0xf bound_ctrl:1
	v_cndmask_b32_e64 v67, v88, v66, s[6:7]
	v_cndmask_b32_e64 v66, v66, v88, s[6:7]
	v_pk_add_f32 v[56:57], v[228:229], s[54:55] op_sel_hi:[1, 0] neg_lo:[0, 1] neg_hi:[0, 1]
	v_dot2c_f32_f16_e32 v104, v35, v35
	v_add_f32_dpp v82, v67, v66 quad_perm:[2,3,0,1] row_mask:0xf bank_mask:0xf bound_ctrl:1
	v_pk_add_f32 v[66:67], v[220:221], s[50:51] op_sel_hi:[1, 0] neg_lo:[0, 1] neg_hi:[0, 1]
	v_pk_add_f32 v[60:61], v[224:225], s[52:53] op_sel_hi:[1, 0] neg_lo:[0, 1] neg_hi:[0, 1]
	v_mul_f32_e32 v58, v67, v67
	v_mul_f32_e32 v59, v61, v61
	v_fmac_f32_e32 v58, v66, v66
	v_fmac_f32_e32 v59, v60, v60
	v_fmac_f32_e32 v58, v69, v69
	v_fmac_f32_e32 v59, v63, v63
	v_fmac_f32_e32 v58, v68, v68
	v_fmac_f32_e32 v59, v62, v62
	v_cndmask_b32_e64 v64, v59, v58, s[4:5]
	v_cndmask_b32_e64 v58, v58, v59, s[4:5]
	v_mul_f32_e32 v65, v57, v57
	v_fmac_f32_e32 v65, v56, v56
	v_add_f32_dpp v64, v64, v58 quad_perm:[1,0,3,2] row_mask:0xf bank_mask:0xf bound_ctrl:1
	v_pk_add_f32 v[58:59], v[226:227], s[54:55] op_sel_hi:[1, 0] neg_lo:[0, 1] neg_hi:[0, 1]
	v_pk_add_f32 v[54:55], v[230:231], s[0:1] op_sel_hi:[1, 0] neg_lo:[0, 1] neg_hi:[0, 1]
	v_pk_add_f32 v[50:51], v[232:233], s[0:1] op_sel_hi:[1, 0] neg_lo:[0, 1] neg_hi:[0, 1]
	v_fmac_f32_e32 v65, v59, v59
	v_mul_f32_e32 v52, v51, v51
	v_fmac_f32_e32 v52, v50, v50
	v_fmac_f32_e32 v52, v55, v55
	v_fmac_f32_e32 v65, v58, v58
	v_fmac_f32_e32 v52, v54, v54
	v_cndmask_b32_e64 v53, v52, v65, s[4:5]
	v_cndmask_b32_e64 v52, v65, v52, s[4:5]
	v_dot2c_f32_f16_e32 v104, v36, v36
	v_dot2c_f32_f16_e32 v104, v37, v37
	v_add_f32_dpp v52, v53, v52 quad_perm:[1,0,3,2] row_mask:0xf bank_mask:0xf bound_ctrl:1
	v_cndmask_b32_e64 v53, v64, v52, s[6:7]
	v_cndmask_b32_e64 v52, v52, v64, s[6:7]
	s_waitcnt lgkmcnt(12)
	v_dot2c_f32_f16_e32 v104, v30, v30
	v_dot2c_f32_f16_e32 v104, v31, v31
	v_add_f32_dpp v52, v53, v52 quad_perm:[2,3,0,1] row_mask:0xf bank_mask:0xf bound_ctrl:1
	v_cndmask_b32_e64 v53, v82, v52, s[8:9]
	v_mov_b32_e32 v64, v53
	v_cndmask_b32_e64 v52, v52, v82, s[8:9]
	v_dot2c_f32_f16_e32 v104, v32, v32
	v_mov_b32_dpp v64, v64 row_shl:4 row_mask:0xf bank_mask:0x5
	v_dot2c_f32_f16_e32 v104, v33, v33
	s_waitcnt lgkmcnt(11)
	v_dot2c_f32_f16_e32 v104, v26, v26
	v_mov_b32_dpp v64, v53 row_shr:4 row_mask:0xf bank_mask:0xa
	v_add_f32_e32 v52, v52, v64
	v_dot2c_f32_f16_e32 v104, v27, v27
	v_dot2c_f32_f16_e32 v104, v28, v28
	v_add_f32_dpp v52, v52, v52 row_ror:8 row_mask:0xf bank_mask:0xf bound_ctrl:1
	v_mov_b32_e32 v53, v52
	s_nop 1
	v_permlane16_swap_b32_e32 v52, v53
	v_add_f32_e32 v52, v52, v53
	v_mov_b32_e32 v53, v52
	s_nop 1
	v_permlane32_swap_b32_e32 v52, v53
	v_add_f32_e32 v52, v52, v53
	v_fmac_f32_e32 v116, 0x3b800000, v52
	v_mul_f32_e32 v52, 0x4f800000, v116
	v_cmp_gt_f32_e32 vcc, s35, v116
	v_dot2c_f32_f16_e32 v104, v29, v29
	s_waitcnt lgkmcnt(10)
	v_dot2c_f32_f16_e32 v104, v22, v22
	v_cndmask_b32_e32 v64, v116, v52, vcc
	v_sqrt_f32_e32 v65, v64
	v_pk_mul_f32 v[52:53], v[94:95], v[98:99]
	v_and_b32_e32 v94, 48, v0
	v_pk_fma_f32 v[52:53], v[96:97], v[52:53], v[92:93] neg_lo:[1,0,0] neg_hi:[1,0,0]
	v_add_u32_e32 v81, -1, v65
	v_fma_f32 v82, -v81, v65, v64
	v_cmp_ge_f32_e64 s[0:1], 0, v82
	v_add_u32_e32 v82, 1, v65
	v_add_u32_e32 v95, 0x19860, v94
	v_cndmask_b32_e64 v81, v65, v81, s[0:1]
	v_fma_f32 v65, -v82, v65, v64
	v_cmp_lt_f32_e64 s[0:1], 0, v65
	v_dot2c_f32_f16_e32 v104, v23, v23
	v_dot2c_f32_f16_e32 v104, v24, v24
	v_cndmask_b32_e64 v65, v81, v82, s[0:1]
	v_mul_f32_e32 v81, 0x37800000, v65
	v_cndmask_b32_e32 v65, v65, v81, vcc
	v_cmp_class_f32_e32 vcc, v64, v117
	v_cvt_pk_f16_f32 v81, v52, v53
	ds_write_b64 v144, v[80:81] offset:36352
	v_cndmask_b32_e32 v64, v65, v64, vcc
	v_div_scale_f32 v65, s[0:1], v64, v64, 1.0
	v_rcp_f32_e32 v82, v65
	v_dot2c_f32_f16_e32 v104, v25, v25
	s_waitcnt lgkmcnt(10)
	v_dot2c_f32_f16_e32 v104, v18, v18
	v_dot2c_f32_f16_e32 v104, v19, v19
	v_fma_f32 v52, -v65, v82, 1.0
	v_fmac_f32_e32 v82, v52, v82
	v_div_scale_f32 v52, vcc, 1.0, v64, 1.0
	v_mul_f32_e32 v53, v52, v82
	v_fma_f32 v80, -v65, v53, v52
	v_fmac_f32_e32 v53, v80, v82
	v_fma_f32 v52, -v65, v53, v52
	v_div_fmas_f32 v52, v52, v82, v53
	v_div_fixup_f32 v52, v52, v64, 1.0
	v_dot2c_f32_f16_e32 v104, v20, v20
	v_readlane_b32 s0, v52, 0
	v_dot2c_f32_f16_e32 v104, v21, v21
	s_waitcnt lgkmcnt(9)
	v_dot2c_f32_f16_e32 v104, v14, v14
	v_pk_mul_f32 v[64:65], s[0:1], v[100:101] op_sel_hi:[0,1]
	v_pk_fma_f32 v[64:65], v[64:65], v[238:239], v[242:243]
	v_dot2c_f32_f16_e32 v104, v15, v15
	v_fma_f32 v53, |v64|, s25, 1.0
	v_rcp_f32_e32 v82, v53
	v_fma_f32 v53, |v65|, s25, 1.0
	v_rcp_f32_e32 v83, v53
	v_pk_mul_f32 v[84:85], v[64:65], v[64:65]
	v_and_b32_e32 v81, 0x7fffffff, v65
	v_mul_f32_e32 v53, 0xbf38aa3b, v84
	v_pk_fma_f32 v[88:89], v[82:83], s[22:23], v[90:91] op_sel_hi:[1,0,0]
	v_exp_f32_e32 v84, v53
	v_pk_fma_f32 v[88:89], v[82:83], v[88:89], s[24:25] op_sel_hi:[1,1,0]
	v_mul_f32_e32 v53, 0xbf38aa3b, v85
	v_pk_fma_f32 v[88:89], v[82:83], v[88:89], s[34:35] op_sel_hi:[1,1,0]
	v_exp_f32_e32 v85, v53
	v_pk_fma_f32 v[88:89], v[82:83], v[88:89], s[40:41] op_sel_hi:[1,1,0]
	v_and_b32_e32 v80, 0x7fffffff, v64
	v_pk_mul_f32 v[82:83], v[82:83], v[88:89]
	v_max_f32_e32 v64, 0, v64
	v_max_f32_e32 v65, 0, v65
	v_pk_mul_f32 v[80:81], v[80:81], v[82:83]
	v_dot2c_f32_f16_e32 v104, v16, v16
	v_pk_fma_f32 v[64:65], v[84:85], v[80:81], v[64:65] neg_lo:[1,0,0] neg_hi:[1,0,0]
	v_pk_mul_f32 v[80:81], s[0:1], v[102:103] op_sel_hi:[0,1]
	v_pk_fma_f32 v[80:81], v[80:81], v[240:241], v[244:245]
	v_cvt_pk_f16_f32 v64, v64, v65
	v_fma_f32 v53, |v80|, s25, 1.0
	v_rcp_f32_e32 v84, v53
	v_fma_f32 v53, |v81|, s25, 1.0
	v_rcp_f32_e32 v85, v53
	v_pk_mul_f32 v[88:89], v[80:81], v[80:81]
	v_and_b32_e32 v83, 0x7fffffff, v81
	v_mul_f32_e32 v53, 0xbf38aa3b, v88
	v_pk_fma_f32 v[92:93], v[84:85], s[22:23], v[90:91] op_sel_hi:[1,0,0]
	v_exp_f32_e32 v88, v53
	v_pk_fma_f32 v[92:93], v[84:85], v[92:93], s[24:25] op_sel_hi:[1,1,0]
	v_mul_f32_e32 v53, 0xbf38aa3b, v89
	v_pk_fma_f32 v[92:93], v[84:85], v[92:93], s[34:35] op_sel_hi:[1,1,0]
	v_exp_f32_e32 v89, v53
	v_pk_fma_f32 v[92:93], v[84:85], v[92:93], s[40:41] op_sel_hi:[1,1,0]
	v_and_b32_e32 v82, 0x7fffffff, v80
	v_pk_mul_f32 v[84:85], v[84:85], v[92:93]
	v_max_f32_e32 v80, 0, v80
	v_max_f32_e32 v81, 0, v81
	v_pk_mul_f32 v[82:83], v[82:83], v[84:85]
	v_readlane_b32 s0, v52, 1
	v_pk_fma_f32 v[80:81], v[88:89], v[82:83], v[80:81] neg_lo:[1,0,0] neg_hi:[1,0,0]
	v_dot2c_f32_f16_e32 v104, v17, v17
	v_cvt_pk_f16_f32 v65, v80, v81
	ds_write_b64 v145, v[64:65] offset:36864
	v_pk_mul_f32 v[64:65], s[0:1], v[86:87] op_sel_hi:[0,1]
	v_pk_fma_f32 v[64:65], v[64:65], v[238:239], v[242:243]
	v_pk_mul_f32 v[78:79], s[0:1], v[78:79] op_sel_hi:[0,1]
	v_fma_f32 v53, |v64|, s25, 1.0
	v_rcp_f32_e32 v82, v53
	v_fma_f32 v53, |v65|, s25, 1.0
	v_rcp_f32_e32 v83, v53
	v_pk_mul_f32 v[84:85], v[64:65], v[64:65]
	v_pk_fma_f32 v[78:79], v[78:79], v[240:241], v[244:245]
	v_mul_f32_e32 v53, 0xbf38aa3b, v84
	v_pk_fma_f32 v[86:87], v[82:83], s[22:23], v[90:91] op_sel_hi:[1,0,0]
	v_exp_f32_e32 v84, v53
	v_pk_fma_f32 v[86:87], v[82:83], v[86:87], s[24:25] op_sel_hi:[1,1,0]
	v_mul_f32_e32 v53, 0xbf38aa3b, v85
	v_pk_fma_f32 v[86:87], v[82:83], v[86:87], s[34:35] op_sel_hi:[1,1,0]
	v_and_b32_e32 v81, 0x7fffffff, v65
	v_pk_fma_f32 v[86:87], v[82:83], v[86:87], s[40:41] op_sel_hi:[1,1,0]
	v_and_b32_e32 v80, 0x7fffffff, v64
	v_exp_f32_e32 v85, v53
	v_pk_mul_f32 v[82:83], v[82:83], v[86:87]
	v_fma_f32 v53, |v78|, s25, 1.0
	v_pk_mul_f32 v[80:81], v[80:81], v[82:83]
	v_rcp_f32_e32 v82, v53
	v_fma_f32 v53, |v79|, s25, 1.0
	v_rcp_f32_e32 v83, v53
	v_max_f32_e32 v64, 0, v64
	v_max_f32_e32 v65, 0, v65
	v_pk_fma_f32 v[64:65], v[84:85], v[80:81], v[64:65] neg_lo:[1,0,0] neg_hi:[1,0,0]
	v_pk_mul_f32 v[84:85], v[78:79], v[78:79]
	v_pk_fma_f32 v[86:87], v[82:83], s[22:23], v[90:91] op_sel_hi:[1,0,0]
	v_mul_f32_e32 v53, 0xbf38aa3b, v84
	v_exp_f32_e32 v84, v53
	v_pk_fma_f32 v[86:87], v[82:83], v[86:87], s[24:25] op_sel_hi:[1,1,0]
	v_mul_f32_e32 v53, 0xbf38aa3b, v85
	v_pk_fma_f32 v[86:87], v[82:83], v[86:87], s[34:35] op_sel_hi:[1,1,0]
	v_exp_f32_e32 v85, v53
	v_pk_fma_f32 v[86:87], v[82:83], v[86:87], s[40:41] op_sel_hi:[1,1,0]
	v_and_b32_e32 v81, 0x7fffffff, v79
	v_and_b32_e32 v80, 0x7fffffff, v78
	v_pk_mul_f32 v[82:83], v[82:83], v[86:87]
	v_max_f32_e32 v78, 0, v78
	v_max_f32_e32 v79, 0, v79
	v_pk_mul_f32 v[80:81], v[80:81], v[82:83]
	v_cvt_pk_f16_f32 v64, v64, v65
	v_pk_fma_f32 v[78:79], v[84:85], v[80:81], v[78:79] neg_lo:[1,0,0] neg_hi:[1,0,0]
	v_readlane_b32 s0, v52, 2
	v_cvt_pk_f16_f32 v65, v78, v79
	ds_write_b64 v139, v[64:65] offset:37376
	v_pk_mul_f32 v[64:65], s[0:1], v[76:77] op_sel_hi:[0,1]
	v_pk_fma_f32 v[64:65], v[64:65], v[238:239], v[242:243]
	v_pk_mul_f32 v[74:75], s[0:1], v[74:75] op_sel_hi:[0,1]
	v_fma_f32 v53, |v64|, s25, 1.0
	v_rcp_f32_e32 v78, v53
	v_fma_f32 v53, |v65|, s25, 1.0
	v_rcp_f32_e32 v79, v53
	v_pk_mul_f32 v[80:81], v[64:65], v[64:65]
	v_pk_fma_f32 v[74:75], v[74:75], v[240:241], v[244:245]
	v_mul_f32_e32 v53, 0xbf38aa3b, v80
	v_pk_fma_f32 v[82:83], v[78:79], s[22:23], v[90:91] op_sel_hi:[1,0,0]
	v_exp_f32_e32 v80, v53
	v_pk_fma_f32 v[82:83], v[78:79], v[82:83], s[24:25] op_sel_hi:[1,1,0]
	v_mul_f32_e32 v53, 0xbf38aa3b, v81
	v_pk_fma_f32 v[82:83], v[78:79], v[82:83], s[34:35] op_sel_hi:[1,1,0]
	v_and_b32_e32 v77, 0x7fffffff, v65
	v_pk_fma_f32 v[82:83], v[78:79], v[82:83], s[40:41] op_sel_hi:[1,1,0]
	v_and_b32_e32 v76, 0x7fffffff, v64
	v_exp_f32_e32 v81, v53
	v_pk_mul_f32 v[78:79], v[78:79], v[82:83]
	v_fma_f32 v53, |v74|, s25, 1.0
	v_pk_mul_f32 v[76:77], v[76:77], v[78:79]
	v_rcp_f32_e32 v78, v53
	v_fma_f32 v53, |v75|, s25, 1.0
	v_rcp_f32_e32 v79, v53
	v_max_f32_e32 v64, 0, v64
	v_max_f32_e32 v65, 0, v65
	v_pk_fma_f32 v[64:65], v[80:81], v[76:77], v[64:65] neg_lo:[1,0,0] neg_hi:[1,0,0]
	v_pk_mul_f32 v[80:81], v[74:75], v[74:75]
	v_pk_fma_f32 v[82:83], v[78:79], s[22:23], v[90:91] op_sel_hi:[1,0,0]
	v_mul_f32_e32 v53, 0xbf38aa3b, v80
	v_exp_f32_e32 v80, v53
	v_pk_fma_f32 v[82:83], v[78:79], v[82:83], s[24:25] op_sel_hi:[1,1,0]
	v_mul_f32_e32 v53, 0xbf38aa3b, v81
	v_pk_fma_f32 v[82:83], v[78:79], v[82:83], s[34:35] op_sel_hi:[1,1,0]
	v_exp_f32_e32 v81, v53
	v_pk_fma_f32 v[82:83], v[78:79], v[82:83], s[40:41] op_sel_hi:[1,1,0]
	v_and_b32_e32 v77, 0x7fffffff, v75
	v_and_b32_e32 v76, 0x7fffffff, v74
	v_pk_mul_f32 v[78:79], v[78:79], v[82:83]
	v_max_f32_e32 v74, 0, v74
	v_max_f32_e32 v75, 0, v75
	v_pk_mul_f32 v[76:77], v[76:77], v[78:79]
	v_cvt_pk_f16_f32 v64, v64, v65
	v_pk_fma_f32 v[74:75], v[80:81], v[76:77], v[74:75] neg_lo:[1,0,0] neg_hi:[1,0,0]
	v_readlane_b32 s0, v52, 3
	v_cvt_pk_f16_f32 v65, v74, v75
	ds_write_b64 v137, v[64:65] offset:37888
	v_pk_mul_f32 v[64:65], s[0:1], v[72:73] op_sel_hi:[0,1]
	v_pk_fma_f32 v[64:65], v[64:65], v[238:239], v[242:243]
	v_pk_mul_f32 v[70:71], s[0:1], v[70:71] op_sel_hi:[0,1]
	v_fma_f32 v53, |v64|, s25, 1.0
	v_rcp_f32_e32 v74, v53
	v_fma_f32 v53, |v65|, s25, 1.0
	v_rcp_f32_e32 v75, v53
	v_pk_mul_f32 v[76:77], v[64:65], v[64:65]
	v_pk_fma_f32 v[70:71], v[70:71], v[240:241], v[244:245]
	v_mul_f32_e32 v53, 0xbf38aa3b, v76
	v_pk_fma_f32 v[78:79], v[74:75], s[22:23], v[90:91] op_sel_hi:[1,0,0]
	v_exp_f32_e32 v76, v53
	v_pk_fma_f32 v[78:79], v[74:75], v[78:79], s[24:25] op_sel_hi:[1,1,0]
	v_mul_f32_e32 v53, 0xbf38aa3b, v77
	v_pk_fma_f32 v[78:79], v[74:75], v[78:79], s[34:35] op_sel_hi:[1,1,0]
	v_and_b32_e32 v73, 0x7fffffff, v65
	v_pk_fma_f32 v[78:79], v[74:75], v[78:79], s[40:41] op_sel_hi:[1,1,0]
	v_and_b32_e32 v72, 0x7fffffff, v64
	v_exp_f32_e32 v77, v53
	v_pk_mul_f32 v[74:75], v[74:75], v[78:79]
	v_fma_f32 v53, |v70|, s25, 1.0
	v_pk_mul_f32 v[72:73], v[72:73], v[74:75]
	v_rcp_f32_e32 v74, v53
	v_fma_f32 v53, |v71|, s25, 1.0
	v_rcp_f32_e32 v75, v53
	v_max_f32_e32 v64, 0, v64
	v_max_f32_e32 v65, 0, v65
	v_pk_fma_f32 v[64:65], v[76:77], v[72:73], v[64:65] neg_lo:[1,0,0] neg_hi:[1,0,0]
	v_pk_mul_f32 v[76:77], v[70:71], v[70:71]
	v_pk_fma_f32 v[78:79], v[74:75], s[22:23], v[90:91] op_sel_hi:[1,0,0]
	v_mul_f32_e32 v53, 0xbf38aa3b, v76
	v_exp_f32_e32 v76, v53
	v_pk_fma_f32 v[78:79], v[74:75], v[78:79], s[24:25] op_sel_hi:[1,1,0]
	v_mul_f32_e32 v53, 0xbf38aa3b, v77
	v_pk_fma_f32 v[78:79], v[74:75], v[78:79], s[34:35] op_sel_hi:[1,1,0]
	v_exp_f32_e32 v77, v53
	v_pk_fma_f32 v[78:79], v[74:75], v[78:79], s[40:41] op_sel_hi:[1,1,0]
	v_and_b32_e32 v73, 0x7fffffff, v71
	v_and_b32_e32 v72, 0x7fffffff, v70
	v_pk_mul_f32 v[74:75], v[74:75], v[78:79]
	v_max_f32_e32 v70, 0, v70
	v_max_f32_e32 v71, 0, v71
	v_pk_mul_f32 v[72:73], v[72:73], v[74:75]
	v_cvt_pk_f16_f32 v64, v64, v65
	v_pk_fma_f32 v[70:71], v[76:77], v[72:73], v[70:71] neg_lo:[1,0,0] neg_hi:[1,0,0]
	v_readlane_b32 s0, v52, 4
	v_cvt_pk_f16_f32 v65, v70, v71
	ds_write_b64 v136, v[64:65] offset:38400
	v_pk_mul_f32 v[64:65], s[0:1], v[68:69] op_sel_hi:[0,1]
	v_pk_fma_f32 v[64:65], v[64:65], v[238:239], v[242:243]
	v_pk_mul_f32 v[66:67], s[0:1], v[66:67] op_sel_hi:[0,1]
	v_fma_f32 v53, |v64|, s25, 1.0
	v_rcp_f32_e32 v70, v53
	v_fma_f32 v53, |v65|, s25, 1.0
	v_rcp_f32_e32 v71, v53
	v_pk_mul_f32 v[72:73], v[64:65], v[64:65]
	v_pk_fma_f32 v[66:67], v[66:67], v[240:241], v[244:245]
	v_mul_f32_e32 v53, 0xbf38aa3b, v72
	v_pk_fma_f32 v[74:75], v[70:71], s[22:23], v[90:91] op_sel_hi:[1,0,0]
	v_exp_f32_e32 v72, v53
	v_pk_fma_f32 v[74:75], v[70:71], v[74:75], s[24:25] op_sel_hi:[1,1,0]
	v_mul_f32_e32 v53, 0xbf38aa3b, v73
	v_pk_fma_f32 v[74:75], v[70:71], v[74:75], s[34:35] op_sel_hi:[1,1,0]
	v_and_b32_e32 v69, 0x7fffffff, v65
	v_pk_fma_f32 v[74:75], v[70:71], v[74:75], s[40:41] op_sel_hi:[1,1,0]
	v_and_b32_e32 v68, 0x7fffffff, v64
	v_exp_f32_e32 v73, v53
	v_pk_mul_f32 v[70:71], v[70:71], v[74:75]
	v_fma_f32 v53, |v66|, s25, 1.0
	v_pk_mul_f32 v[68:69], v[68:69], v[70:71]
	v_rcp_f32_e32 v70, v53
	v_fma_f32 v53, |v67|, s25, 1.0
	v_rcp_f32_e32 v71, v53
	v_max_f32_e32 v64, 0, v64
	v_max_f32_e32 v65, 0, v65
	v_pk_fma_f32 v[64:65], v[72:73], v[68:69], v[64:65] neg_lo:[1,0,0] neg_hi:[1,0,0]
	v_pk_mul_f32 v[72:73], v[66:67], v[66:67]
	v_pk_fma_f32 v[74:75], v[70:71], s[22:23], v[90:91] op_sel_hi:[1,0,0]
	v_mul_f32_e32 v53, 0xbf38aa3b, v72
	v_exp_f32_e32 v72, v53
	v_pk_fma_f32 v[74:75], v[70:71], v[74:75], s[24:25] op_sel_hi:[1,1,0]
	v_mul_f32_e32 v53, 0xbf38aa3b, v73
	v_pk_fma_f32 v[74:75], v[70:71], v[74:75], s[34:35] op_sel_hi:[1,1,0]
	v_exp_f32_e32 v73, v53
	v_pk_fma_f32 v[74:75], v[70:71], v[74:75], s[40:41] op_sel_hi:[1,1,0]
	v_readlane_b32 s0, v52, 5
	v_and_b32_e32 v69, 0x7fffffff, v67
	v_and_b32_e32 v68, 0x7fffffff, v66
	v_pk_mul_f32 v[70:71], v[70:71], v[74:75]
	v_pk_mul_f32 v[62:63], s[0:1], v[62:63] op_sel_hi:[0,1]
	v_max_f32_e32 v66, 0, v66
	v_max_f32_e32 v67, 0, v67
	v_pk_mul_f32 v[68:69], v[68:69], v[70:71]
	v_pk_fma_f32 v[62:63], v[62:63], v[238:239], v[242:243]
	v_pk_fma_f32 v[66:67], v[72:73], v[68:69], v[66:67] neg_lo:[1,0,0] neg_hi:[1,0,0]
	v_fma_f32 v53, |v62|, s25, 1.0
	v_cvt_pk_f16_f32 v64, v64, v65
	v_cvt_pk_f16_f32 v65, v66, v67
	v_rcp_f32_e32 v66, v53
	v_fma_f32 v53, |v63|, s25, 1.0
	v_rcp_f32_e32 v67, v53
	v_pk_mul_f32 v[68:69], v[62:63], v[62:63]
	v_pk_mul_f32 v[60:61], s[0:1], v[60:61] op_sel_hi:[0,1]
	v_mul_f32_e32 v53, 0xbf38aa3b, v68
	v_pk_fma_f32 v[70:71], v[66:67], s[22:23], v[90:91] op_sel_hi:[1,0,0]
	v_exp_f32_e32 v68, v53
	v_pk_fma_f32 v[70:71], v[66:67], v[70:71], s[24:25] op_sel_hi:[1,1,0]
	v_mul_f32_e32 v53, 0xbf38aa3b, v69
	v_pk_fma_f32 v[70:71], v[66:67], v[70:71], s[34:35] op_sel_hi:[1,1,0]
	v_pk_fma_f32 v[60:61], v[60:61], v[240:241], v[244:245]
	v_pk_fma_f32 v[70:71], v[66:67], v[70:71], s[40:41] op_sel_hi:[1,1,0]
	ds_write_b64 v123, v[64:65] offset:38912
	v_and_b32_e32 v65, 0x7fffffff, v63
	v_and_b32_e32 v64, 0x7fffffff, v62
	v_exp_f32_e32 v69, v53
	v_pk_mul_f32 v[66:67], v[66:67], v[70:71]
	v_fma_f32 v53, |v60|, s25, 1.0
	v_pk_mul_f32 v[64:65], v[64:65], v[66:67]
	v_rcp_f32_e32 v66, v53
	v_fma_f32 v53, |v61|, s25, 1.0
	v_rcp_f32_e32 v67, v53
	v_max_f32_e32 v62, 0, v62
	v_max_f32_e32 v63, 0, v63
	v_pk_fma_f32 v[62:63], v[68:69], v[64:65], v[62:63] neg_lo:[1,0,0] neg_hi:[1,0,0]
	v_pk_mul_f32 v[68:69], v[60:61], v[60:61]
	v_pk_fma_f32 v[70:71], v[66:67], s[22:23], v[90:91] op_sel_hi:[1,0,0]
	v_mul_f32_e32 v53, 0xbf38aa3b, v68
	v_exp_f32_e32 v68, v53
	v_pk_fma_f32 v[70:71], v[66:67], v[70:71], s[24:25] op_sel_hi:[1,1,0]
	v_mul_f32_e32 v53, 0xbf38aa3b, v69
	v_pk_fma_f32 v[70:71], v[66:67], v[70:71], s[34:35] op_sel_hi:[1,1,0]
	v_exp_f32_e32 v69, v53
	v_pk_fma_f32 v[70:71], v[66:67], v[70:71], s[40:41] op_sel_hi:[1,1,0]
	v_and_b32_e32 v65, 0x7fffffff, v61
	v_and_b32_e32 v64, 0x7fffffff, v60
	v_pk_mul_f32 v[66:67], v[66:67], v[70:71]
	v_readlane_b32 s0, v52, 6
	v_max_f32_e32 v60, 0, v60
	v_max_f32_e32 v61, 0, v61
	v_pk_mul_f32 v[64:65], v[64:65], v[66:67]
	v_pk_mul_f32 v[58:59], s[0:1], v[58:59] op_sel_hi:[0,1]
	v_pk_fma_f32 v[60:61], v[68:69], v[64:65], v[60:61] neg_lo:[1,0,0] neg_hi:[1,0,0]
	v_pk_fma_f32 v[58:59], v[58:59], v[238:239], v[242:243]
	v_cvt_pk_f16_f32 v62, v62, v63
	v_cvt_pk_f16_f32 v63, v60, v61
	v_fma_f32 v53, |v58|, s25, 1.0
	ds_write_b64 v133, v[62:63] offset:39424
	v_rcp_f32_e32 v62, v53
	v_fma_f32 v53, |v59|, s25, 1.0
	v_rcp_f32_e32 v63, v53
	v_pk_mul_f32 v[64:65], v[58:59], v[58:59]
	v_pk_mul_f32 v[56:57], s[0:1], v[56:57] op_sel_hi:[0,1]
	v_mul_f32_e32 v53, 0xbf38aa3b, v64
	v_pk_fma_f32 v[66:67], v[62:63], s[22:23], v[90:91] op_sel_hi:[1,0,0]
	v_exp_f32_e32 v64, v53
	v_pk_fma_f32 v[66:67], v[62:63], v[66:67], s[24:25] op_sel_hi:[1,1,0]
	v_mul_f32_e32 v53, 0xbf38aa3b, v65
	v_pk_fma_f32 v[66:67], v[62:63], v[66:67], s[34:35] op_sel_hi:[1,1,0]
	v_exp_f32_e32 v65, v53
	v_pk_fma_f32 v[66:67], v[62:63], v[66:67], s[40:41] op_sel_hi:[1,1,0]
	v_pk_fma_f32 v[56:57], v[56:57], v[240:241], v[244:245]
	v_and_b32_e32 v61, 0x7fffffff, v59
	v_and_b32_e32 v60, 0x7fffffff, v58
	v_pk_mul_f32 v[62:63], v[62:63], v[66:67]
	v_fma_f32 v53, |v56|, s25, 1.0
	v_pk_mul_f32 v[60:61], v[60:61], v[62:63]
	v_rcp_f32_e32 v62, v53
	v_fma_f32 v53, |v57|, s25, 1.0
	v_max_f32_e32 v58, 0, v58
	v_max_f32_e32 v59, 0, v59
	v_rcp_f32_e32 v63, v53
	v_pk_fma_f32 v[58:59], v[64:65], v[60:61], v[58:59] neg_lo:[1,0,0] neg_hi:[1,0,0]
	v_pk_mul_f32 v[64:65], v[56:57], v[56:57]
	v_readlane_b32 s0, v52, 7
	v_mul_f32_e32 v53, 0xbf38aa3b, v64
	v_exp_f32_e32 v64, v53
	v_mul_f32_e32 v53, 0xbf38aa3b, v65
	v_pk_fma_f32 v[66:67], v[62:63], s[22:23], v[90:91] op_sel_hi:[1,0,0]
	v_exp_f32_e32 v65, v53
	v_pk_mul_f32 v[52:53], s[0:1], v[54:55] op_sel_hi:[0,1]
	v_pk_fma_f32 v[66:67], v[62:63], v[66:67], s[24:25] op_sel_hi:[1,1,0]
	v_pk_fma_f32 v[42:43], v[52:53], v[238:239], v[242:243]
	v_pk_fma_f32 v[66:67], v[62:63], v[66:67], s[34:35] op_sel_hi:[1,1,0]
	v_fma_f32 v52, |v42|, s25, 1.0
	v_fma_f32 v53, |v43|, s25, 1.0
	v_pk_fma_f32 v[66:67], v[62:63], v[66:67], s[40:41] op_sel_hi:[1,1,0]
	v_rcp_f32_e32 v52, v52
	v_rcp_f32_e32 v53, v53
	v_and_b32_e32 v61, 0x7fffffff, v57
	v_and_b32_e32 v60, 0x7fffffff, v56
	v_pk_mul_f32 v[62:63], v[62:63], v[66:67]
	v_max_f32_e32 v56, 0, v56
	v_max_f32_e32 v57, 0, v57
	v_pk_mul_f32 v[60:61], v[60:61], v[62:63]
	v_cvt_pk_f16_f32 v58, v58, v59
	v_pk_fma_f32 v[56:57], v[64:65], v[60:61], v[56:57] neg_lo:[1,0,0] neg_hi:[1,0,0]
	v_pk_mul_f32 v[54:55], v[42:43], v[42:43]
	v_cvt_pk_f16_f32 v59, v56, v57
	v_pk_fma_f32 v[56:57], v[52:53], s[22:23], v[90:91] op_sel_hi:[1,0,0]
	v_mul_f32_e32 v54, 0xbf38aa3b, v54
	v_pk_fma_f32 v[56:57], v[52:53], v[56:57], s[24:25] op_sel_hi:[1,1,0]
	v_mul_f32_e32 v55, 0xbf38aa3b, v55
	v_exp_f32_e32 v54, v54
	v_pk_fma_f32 v[56:57], v[52:53], v[56:57], s[34:35] op_sel_hi:[1,1,0]
	v_exp_f32_e32 v55, v55
	v_pk_fma_f32 v[56:57], v[52:53], v[56:57], s[40:41] op_sel_hi:[1,1,0]
	v_and_b32_e32 v47, 0x7fffffff, v43
	v_and_b32_e32 v46, 0x7fffffff, v42
	v_pk_mul_f32 v[52:53], v[52:53], v[56:57]
	v_max_f32_e32 v42, 0, v42
	v_max_f32_e32 v43, 0, v43
	v_pk_mul_f32 v[46:47], v[46:47], v[52:53]
	ds_write_b64 v119, v[58:59] offset:39936
	v_pk_fma_f32 v[42:43], v[54:55], v[46:47], v[42:43] neg_lo:[1,0,0] neg_hi:[1,0,0]
	v_pk_mul_f32 v[46:47], s[0:1], v[50:51] op_sel_hi:[0,1]
	v_pk_fma_f32 v[44:45], v[46:47], v[240:241], v[244:245]
	v_cvt_pk_f16_f32 v42, v42, v43
	v_fma_f32 v43, |v44|, s25, 1.0
	v_rcp_f32_e32 v48, v43
	v_fma_f32 v43, |v45|, s25, 1.0
	v_rcp_f32_e32 v49, v43
	v_pk_mul_f32 v[50:51], v[44:45], v[44:45]
	v_and_b32_e32 v47, 0x7fffffff, v45
	v_mul_f32_e32 v43, 0xbf38aa3b, v50
	v_pk_fma_f32 v[52:53], v[48:49], s[22:23], v[90:91] op_sel_hi:[1,0,0]
	v_exp_f32_e32 v50, v43
	v_pk_fma_f32 v[52:53], v[48:49], v[52:53], s[24:25] op_sel_hi:[1,1,0]
	v_mul_f32_e32 v43, 0xbf38aa3b, v51
	v_pk_fma_f32 v[52:53], v[48:49], v[52:53], s[34:35] op_sel_hi:[1,1,0]
	v_exp_f32_e32 v51, v43
	v_pk_fma_f32 v[52:53], v[48:49], v[52:53], s[40:41] op_sel_hi:[1,1,0]
	v_and_b32_e32 v46, 0x7fffffff, v44
	v_pk_mul_f32 v[48:49], v[48:49], v[52:53]
	v_max_f32_e32 v44, 0, v44
	v_max_f32_e32 v45, 0, v45
	v_pk_mul_f32 v[46:47], v[46:47], v[48:49]
	s_waitcnt lgkmcnt(14)
	v_dot2c_f32_f16_e32 v104, v10, v10
	v_pk_fma_f32 v[44:45], v[50:51], v[46:47], v[44:45] neg_lo:[1,0,0] neg_hi:[1,0,0]
	v_dot2c_f32_f16_e32 v104, v11, v11
	v_cvt_pk_f16_f32 v43, v44, v45
	ds_write_b64 v146, v[42:43] offset:40448
	ds_read_b128 v[70:73], v115 offset:32768
	ds_read_b128 v[66:69], v147 offset:32768
	ds_read_b128 v[62:65], v148 offset:32768
	ds_read_b128 v[58:61], v149 offset:32768
	ds_read_b128 v[54:57], v150 offset:33024
	ds_read_b128 v[50:53], v151 offset:33024
	ds_read_b128 v[46:49], v152 offset:33024
	ds_read_b128 v[42:45], v153 offset:33024
	ds_read_b128 v[74:77], v95
	ds_read_b128 v[78:81], v95 offset:64
	ds_read_b128 v[82:85], v95 offset:128
	ds_read_b128 v[86:89], v95 offset:192
	ds_read_b128 v[90:93], v95 offset:256
	ds_read_b128 v[96:99], v95 offset:320
	s_waitcnt lgkmcnt(5)
	v_dot2c_f32_f16_e32 v105, v38, v74
	v_dot2c_f32_f16_e32 v105, v39, v75
	ds_read_b128 v[100:103], v95 offset:384
	ds_read_b128 v[108:111], v95 offset:448
	v_mov_b32_e32 v95, 0
	v_dot2c_f32_f16_e32 v105, v40, v76
	v_dot2c_f32_f16_e32 v95, v70, v70
	v_dot2c_f32_f16_e32 v105, v41, v77
	v_mov_b32_e32 v115, 0
	v_dot2c_f32_f16_e32 v95, v71, v71
	s_waitcnt lgkmcnt(6)
	v_dot2c_f32_f16_e32 v105, v34, v78
	v_dot2c_f32_f16_e32 v115, v70, v74
	v_dot2c_f32_f16_e32 v95, v72, v72
	v_dot2c_f32_f16_e32 v105, v35, v79
	v_dot2c_f32_f16_e32 v115, v71, v75
	v_dot2c_f32_f16_e32 v95, v73, v73
	v_dot2c_f32_f16_e32 v105, v36, v80
	v_dot2c_f32_f16_e32 v115, v72, v76
	v_dot2c_f32_f16_e32 v95, v66, v66
	v_dot2c_f32_f16_e32 v105, v37, v81
	v_dot2c_f32_f16_e32 v115, v73, v77
	v_dot2c_f32_f16_e32 v95, v67, v67
	s_waitcnt lgkmcnt(5)
	v_dot2c_f32_f16_e32 v105, v30, v82
	v_dot2c_f32_f16_e32 v115, v66, v78
	v_dot2c_f32_f16_e32 v95, v68, v68
	v_dot2c_f32_f16_e32 v105, v31, v83
	v_dot2c_f32_f16_e32 v115, v67, v79
	v_dot2c_f32_f16_e32 v95, v69, v69
	v_dot2c_f32_f16_e32 v105, v32, v84
	v_dot2c_f32_f16_e32 v115, v68, v80
	v_dot2c_f32_f16_e32 v95, v62, v62
	v_dot2c_f32_f16_e32 v105, v33, v85
	v_dot2c_f32_f16_e32 v115, v69, v81
	v_dot2c_f32_f16_e32 v95, v63, v63
	s_waitcnt lgkmcnt(4)
	v_dot2c_f32_f16_e32 v105, v26, v86
	v_dot2c_f32_f16_e32 v115, v62, v82
	v_dot2c_f32_f16_e32 v95, v64, v64
	v_dot2c_f32_f16_e32 v105, v27, v87
	v_dot2c_f32_f16_e32 v115, v63, v83
	v_dot2c_f32_f16_e32 v95, v65, v65
	v_dot2c_f32_f16_e32 v105, v28, v88
	v_dot2c_f32_f16_e32 v115, v64, v84
	v_dot2c_f32_f16_e32 v95, v58, v58
	v_dot2c_f32_f16_e32 v105, v29, v89
	v_dot2c_f32_f16_e32 v115, v65, v85
	v_dot2c_f32_f16_e32 v95, v59, v59
	s_waitcnt lgkmcnt(3)
	v_dot2c_f32_f16_e32 v105, v22, v90
	v_dot2c_f32_f16_e32 v115, v58, v86
	v_dot2c_f32_f16_e32 v95, v60, v60
	v_dot2c_f32_f16_e32 v105, v23, v91
	v_dot2c_f32_f16_e32 v115, v59, v87
	v_dot2c_f32_f16_e32 v95, v61, v61
	v_dot2c_f32_f16_e32 v105, v24, v92
	v_dot2c_f32_f16_e32 v115, v60, v88
	v_dot2c_f32_f16_e32 v95, v54, v54
	v_dot2c_f32_f16_e32 v105, v25, v93
	v_dot2c_f32_f16_e32 v115, v61, v89
	v_dot2c_f32_f16_e32 v95, v55, v55
	s_waitcnt lgkmcnt(2)
	v_dot2c_f32_f16_e32 v105, v18, v96
	v_dot2c_f32_f16_e32 v115, v54, v90
	v_dot2c_f32_f16_e32 v95, v56, v56
	v_dot2c_f32_f16_e32 v105, v19, v97
	v_dot2c_f32_f16_e32 v115, v55, v91
	v_dot2c_f32_f16_e32 v95, v57, v57
	v_dot2c_f32_f16_e32 v105, v20, v98
	v_dot2c_f32_f16_e32 v115, v56, v92
	v_dot2c_f32_f16_e32 v95, v50, v50
	v_dot2c_f32_f16_e32 v105, v21, v99
	v_dot2c_f32_f16_e32 v115, v57, v93
	v_dot2c_f32_f16_e32 v95, v51, v51
	s_waitcnt lgkmcnt(1)
	v_dot2c_f32_f16_e32 v105, v14, v100
	v_dot2c_f32_f16_e32 v115, v50, v96
	v_dot2c_f32_f16_e32 v95, v52, v52
	v_dot2c_f32_f16_e32 v105, v15, v101
	v_dot2c_f32_f16_e32 v115, v51, v97
	v_dot2c_f32_f16_e32 v95, v53, v53
	v_dot2c_f32_f16_e32 v105, v16, v102
	v_dot2c_f32_f16_e32 v115, v52, v98
	v_dot2c_f32_f16_e32 v95, v46, v46
	v_dot2c_f32_f16_e32 v105, v17, v103
	v_dot2c_f32_f16_e32 v115, v53, v99
	v_dot2c_f32_f16_e32 v95, v47, v47
	s_waitcnt lgkmcnt(0)
	v_dot2c_f32_f16_e32 v105, v10, v108
	v_dot2c_f32_f16_e32 v104, v12, v12
	v_dot2c_f32_f16_e32 v115, v46, v100
	v_dot2c_f32_f16_e32 v95, v48, v48
	v_dot2c_f32_f16_e32 v105, v11, v109
	v_dot2c_f32_f16_e32 v104, v13, v13
	v_dot2c_f32_f16_e32 v115, v47, v101
	v_dot2c_f32_f16_e32 v95, v49, v49
	v_dot2c_f32_f16_e32 v105, v12, v110
	v_dot2c_f32_f16_e32 v115, v48, v102
	v_dot2c_f32_f16_e32 v95, v42, v42
	v_mov_b32_e32 v74, v104
	v_dot2c_f32_f16_e32 v105, v13, v111
	v_dot2c_f32_f16_e32 v115, v49, v103
	v_dot2c_f32_f16_e32 v95, v43, v43
	v_permlane16_swap_b32_e32 v104, v74
	v_dot2c_f32_f16_e32 v115, v42, v108
	v_dot2c_f32_f16_e32 v95, v44, v44
	v_add_f32_e32 v133, v104, v74
	v_mov_b32_e32 v74, v105
	v_dot2c_f32_f16_e32 v115, v43, v109
	v_dot2c_f32_f16_e32 v95, v45, v45
	v_permlane16_swap_b32_e32 v105, v74
	v_dot2c_f32_f16_e32 v115, v44, v110
	v_add_f32_e32 v137, v105, v74
	v_mov_b32_e32 v74, v95
	v_dot2c_f32_f16_e32 v115, v45, v111
	s_nop 0
	v_permlane16_swap_b32_e32 v95, v74
	v_add_f32_e32 v135, v95, v74
	v_mov_b32_e32 v74, v115
	s_nop 1
	v_permlane16_swap_b32_e32 v115, v74
	v_add_f32_e32 v139, v115, v74
	v_lshlrev_b32_e32 v74, 8, v107
	v_lshlrev_b32_e32 v75, 3, v114
	s_movk_i32 s0, 0x78
	v_and_or_b32 v76, v75, s0, v74
	v_lshlrev_b32_e32 v75, 3, v141
	v_and_or_b32 v77, v75, s0, v74
	v_lshlrev_b32_e32 v75, 3, v142
	v_and_or_b32 v78, v75, s0, v74
	v_lshlrev_b32_e32 v75, 3, v143
	v_and_or_b32 v79, v75, s0, v74
	s_add_u32 s0, s26, 0x8000
	v_or_b32_e32 v108, 0x8000, v112
	v_mov_b32_e32 v123, 0
	s_addc_u32 s1, s27, 0
	v_readfirstlane_b32 s4, v108
	s_waitcnt vmcnt(0)
	s_barrier
	v_lshl_add_u64 v[74:75], s[0:1], 0, v[122:123]
	s_mov_b32 m0, s4
	s_nop 0
	global_load_lds_dwordx4 v[74:75], off
	s_addk_i32 s4, 0x400
	v_mov_b32_e32 v107, v123
	v_lshl_add_u64 v[74:75], s[0:1], 0, v[106:107]
	s_add_u32 s0, s26, 0xc000
	s_mov_b32 m0, s4
	s_nop 0
	global_load_lds_dwordx4 v[74:75], off
	s_addc_u32 s1, s27, 0
	v_or_b32_e32 v109, 0xc000, v112
	v_lshl_add_u64 v[74:75], s[0:1], 0, v[122:123]
	v_readfirstlane_b32 s4, v109
	s_mov_b32 m0, s4
	s_nop 0
	global_load_lds_dwordx4 v[74:75], off
	s_addk_i32 s4, 0x400
	v_lshl_add_u64 v[74:75], s[0:1], 0, v[106:107]
	s_mov_b32 m0, s4
	s_nop 0
	global_load_lds_dwordx4 v[74:75], off
	v_mov_b32_e32 v134, v133
	v_mov_b32_e32 v138, v137
	v_mov_b32_e32 v136, v135
	v_mov_b32_e32 v140, v139
	v_lshlrev_b32_e32 v144, 1, v76
	v_lshlrev_b32_e32 v143, 1, v77
	v_lshlrev_b32_e32 v142, 1, v78
	v_lshlrev_b32_e32 v141, 1, v79
	s_add_u32 s0, s26, 0x14000
	v_mov_b32_e32 v74, 0x7f61b1e6
	v_permlane32_swap_b32_e32 v133, v134
	v_permlane32_swap_b32_e32 v137, v138
	v_permlane32_swap_b32_e32 v135, v136
	v_permlane32_swap_b32_e32 v139, v140
	v_or_b32_e32 v160, 0x10000, v144
	v_or_b32_e32 v158, 0x10000, v143
	v_or_b32_e32 v156, 0x10000, v142
	v_or_b32_e32 v154, 0x10000, v141
	v_or_b32_e32 v159, 0x12000, v144
	v_or_b32_e32 v157, 0x12000, v143
	v_or_b32_e32 v155, 0x12000, v142
	v_or_b32_e32 v153, 0x12000, v141
	v_or_b32_e32 v152, 0x14000, v144
	v_or_b32_e32 v150, 0x14000, v143
	v_or_b32_e32 v148, 0x14000, v142
	v_or_b32_e32 v146, 0x14000, v141
	v_or_b32_e32 v151, 0x16000, v144
	v_or_b32_e32 v149, 0x16000, v143
	v_or_b32_e32 v147, 0x16000, v142
	v_or_b32_e32 v145, 0x16000, v141
	s_addc_u32 s1, s27, 0
	v_mov_b32_e32 v98, 0x7f800000
	s_mov_b32 s22, 0
	v_mov_b32_e32 v100, 0x7f800000
	v_mov_b32_e32 v99, 0x7f800000
	v_mov_b32_e32 v111, 0x7f800000
	v_mov_b32_e32 v101, 0x7f800000
	v_mov_b32_e32 v110, 0x7f800000
	v_mov_b32_e32 v75, v74
	v_mov_b32_e32 v76, v74
	v_mov_b32_e32 v77, v74
	v_mov_b32_e32 v78, v74
	v_mov_b32_e32 v79, v74
	v_mov_b32_e32 v80, v74
	v_mov_b32_e32 v81, v74
	v_mov_b32_e32 v82, v74
	v_mov_b32_e32 v83, v74
	v_mov_b32_e32 v84, v74
	v_mov_b32_e32 v85, v74
	v_mov_b32_e32 v86, v74
	v_mov_b32_e32 v87, v74
	v_mov_b32_e32 v88, v74
	v_mov_b32_e32 v89, v74
	v_mov_b32_e32 v247, 0xfffffc00
	v_readfirstlane_b32 s96, v1
	s_nop 3
	s_cmp_lt_u32 s96, 4
	s_cbranch_scc0 .Lmy_prio_done
	s_setprio 1
.Lmy_prio_done:
.LBB1_7:
	s_add_u32 s4, s0, 0xffffc000
	v_readfirstlane_b32 s8, v112
	s_addc_u32 s5, s1, -1
	s_add_i32 s35, s8, 0x10000
	v_lshl_add_u64 v[96:97], s[4:5], 0, v[122:123]
	s_mov_b32 m0, s35
	s_nop 0
	global_load_lds_dwordx4 v[96:97], off
	s_add_i32 s34, s8, 0x10400
	v_lshl_add_u64 v[102:103], s[4:5], 0, v[106:107]
	s_mov_b32 m0, s34
	s_nop 0
	global_load_lds_dwordx4 v[102:103], off
	v_lshl_add_u64 v[90:91], s[0:1], 0, v[122:123]
	s_add_i32 s6, s8, 0x14000
	s_mov_b32 m0, s6
	s_nop 0
	global_load_lds_dwordx4 v[90:91], off
	v_lshl_add_u64 v[92:93], s[0:1], 0, v[106:107]
	s_add_i32 s7, s8, 0x14400
	s_mov_b32 m0, s7
	s_nop 0
	global_load_lds_dwordx4 v[92:93], off
	ds_read_b128 v[90:93], v144
	ds_read_b128 v[118:121], v144 offset:8192
	v_add_u32_e32 v95, s3, v94
	v_add_u32_e32 v96, 0x18060, v95
	v_add_u32_e32 v97, 0x180a0, v95
	ds_read_b128 v[102:105], v96
	ds_read_b128 v[162:165], v97
	s_lshl_b32 s24, s22, 5
	s_or_b32 s70, s24, 1
	s_or_b32 s71, s24, 2
	s_or_b32 s72, s24, 3
	s_or_b32 s73, s24, 17
	s_or_b32 s74, s24, 18
	s_or_b32 s75, s24, 19
	v_and_or_b32 v86, v86, v247, s24
	v_med3_f32 v111, v101, v111, v86
	v_med3_f32 v101, v110, v101, v86
	v_min_f32 v110, v110, v86
	s_waitcnt lgkmcnt(1)
	v_mfma_f32_16x16x32_f16 v[114:117], v[90:93], v[38:41], v[102:105]
	s_or_b32 s41, s24, 16
	ds_read_b128 v[166:169], v143 offset:8448
	ds_read_b128 v[170:173], v142 offset:8448
	v_mfma_f32_16x16x32_f16 v[90:93], v[90:93], v[70:73], v[102:105]
	v_and_or_b32 v96, v89, v247, s72
	ds_read_b128 v[102:105], v143
	v_and_or_b32 v97, v87, v247, s70
	v_and_or_b32 v161, v88, v247, s71
	s_waitcnt lgkmcnt(3)
	v_mfma_f32_16x16x32_f16 v[86:89], v[118:121], v[38:41], v[162:165]
	ds_read_b128 v[174:177], v141 offset:8448
	v_med3_f32 v111, v101, v111, v97
	v_med3_f32 v101, v110, v101, v97
	v_mfma_f32_16x16x32_f16 v[118:121], v[118:121], v[70:73], v[162:165]
	ds_read_b128 v[162:165], v143 offset:8192
	v_and_or_b32 v230, v82, v247, s24
	v_and_or_b32 v231, v83, v247, s70
	s_waitcnt lgkmcnt(2)
	v_mfma_f32_16x16x32_f16 v[114:117], v[102:105], v[34:37], v[114:117]
	v_min_f32 v97, v110, v97
	ds_read_b128 v[202:205], v144 offset:24576
	v_med3_f32 v110, v101, v111, v161
	v_mfma_f32_16x16x32_f16 v[90:93], v[102:105], v[66:69], v[90:93]
	v_and_or_b32 v232, v84, v247, s71
	v_and_or_b32 v233, v85, v247, s72
	s_waitcnt lgkmcnt(1)
	v_mfma_f32_16x16x32_f16 v[82:85], v[162:165], v[34:37], v[86:89]
	v_med3_f32 v101, v97, v101, v161
	v_min_f32 v97, v97, v161
	v_med3_f32 v98, v100, v98, v230
	v_mfma_f32_16x16x32_f16 v[102:105], v[162:165], v[66:69], v[118:121]
	v_and_or_b32 v234, v78, v247, s41
	s_nop 0
	ds_read_b128 v[86:89], v142
	ds_read_b128 v[118:121], v142 offset:8192
	v_and_or_b32 v235, v79, v247, s73
	v_and_or_b32 v236, v80, v247, s74
	s_waitcnt lgkmcnt(1)
	v_mfma_f32_16x16x32_f16 v[114:117], v[86:89], v[30:33], v[114:117]
	ds_read_b128 v[162:165], v144 offset:8448
	v_med3_f32 v100, v99, v100, v230
	ds_read_b128 v[178:181], v143 offset:16384
	v_mfma_f32_16x16x32_f16 v[86:89], v[86:89], v[62:65], v[90:93]
	v_and_or_b32 v237, v81, v247, s75
	v_and_or_b32 v238, v74, v247, s41
	s_waitcnt lgkmcnt(2)
	v_mfma_f32_16x16x32_f16 v[78:81], v[118:121], v[30:33], v[82:85]
	ds_read_b128 v[206:209], v143 offset:24576
	s_add_i32 s9, s23, 0xffffff70
	s_or_b32 s76, s9, 1
	s_or_b32 s77, s9, 2
	s_or_b32 s78, s9, 3
	s_or_b32 s79, s9, 17
	s_or_b32 s80, s9, 18
	s_or_b32 s81, s9, 19
	ds_read_b128 v[182:185], v142 offset:16384
	ds_read_b128 v[82:85], v141
	v_mfma_f32_16x16x32_f16 v[90:93], v[118:121], v[62:65], v[102:105]
	v_and_or_b32 v239, v75, v247, s73
	v_and_or_b32 v240, v76, v247, s74
	v_and_or_b32 v241, v77, v247, s75
	s_waitcnt lgkmcnt(0)
	v_mfma_f32_16x16x32_f16 v[74:77], v[82:85], v[26:29], v[114:117]
	ds_read_b128 v[102:105], v144 offset:256
	s_nop 1
	ds_read_b128 v[114:117], v143 offset:256
	ds_read_b128 v[118:121], v141 offset:256
	v_mfma_f32_16x16x32_f16 v[82:85], v[82:85], v[58:61], v[86:89]
	ds_read_b128 v[210:213], v142 offset:24576
	s_add_i32 s25, s23, 0xffffff80
	ds_read_b128 v[186:189], v141 offset:16384
	ds_read_b128 v[86:89], v141 offset:8192
	s_waitcnt lgkmcnt(0)
	v_mfma_f32_16x16x32_f16 v[78:81], v[86:89], v[26:29], v[78:81]
	ds_read_b128 v[214:217], v141 offset:24576
	ds_read_b128 v[190:193], v144 offset:16640
	s_add_u32 s4, s0, 0x4000
	v_mfma_f32_16x16x32_f16 v[86:89], v[86:89], v[58:61], v[90:93]
	s_addc_u32 s5, s1, 0
	s_add_i32 s40, s8, 0x400
	s_add_u32 s6, s0, 0x8000
	ds_read_b128 v[90:93], v142 offset:256
	v_mfma_f32_16x16x32_f16 v[74:77], v[102:105], v[22:25], v[74:77]
	s_addc_u32 s7, s1, 0
	ds_read_b128 v[194:197], v143 offset:16640
	ds_read_b128 v[218:221], v143 offset:24832
	v_mfma_f32_16x16x32_f16 v[82:85], v[102:105], v[54:57], v[82:85]
	ds_read_b128 v[102:105], v144 offset:16384
	ds_read_b128 v[222:225], v142 offset:24832
	ds_read_b128 v[198:201], v141 offset:16640
	v_mfma_f32_16x16x32_f16 v[78:81], v[162:165], v[22:25], v[78:81]
	ds_read_b128 v[226:229], v141 offset:24832
	s_add_i32 s35, s23, 0xffffff90
	s_or_b32 s82, s35, 1
	s_or_b32 s83, s35, 2
	s_or_b32 s84, s35, 3
	s_or_b32 s85, s35, 17
	s_or_b32 s86, s35, 18
	s_or_b32 s87, s35, 19
	s_add_i32 s41, s23, 0xffffffa0
	v_mfma_f32_16x16x32_f16 v[86:89], v[162:165], v[54:57], v[86:89]
	ds_read_b128 v[162:165], v142 offset:16640
	s_add_i32 s24, s23, 0xffffffb0
	s_or_b32 s70, s24, 1
	s_or_b32 s71, s24, 2
	s_or_b32 s72, s24, 3
	s_or_b32 s73, s24, 17
	s_or_b32 s74, s24, 18
	s_or_b32 s75, s24, 19
	s_sub_i32 s34, s23, 64
	v_mfma_f32_16x16x32_f16 v[74:77], v[114:117], v[18:21], v[74:77]
	s_mov_b32 s22, s33
	v_mfma_f32_16x16x32_f16 v[82:85], v[114:117], v[50:53], v[82:85]
	ds_read_b128 v[114:117], v144 offset:24832
	v_mfma_f32_16x16x32_f16 v[78:81], v[166:169], v[18:21], v[78:81]
	v_mfma_f32_16x16x32_f16 v[86:89], v[166:169], v[50:53], v[86:89]
	s_waitcnt lgkmcnt(8)
	v_mfma_f32_16x16x32_f16 v[74:77], v[90:93], v[14:17], v[74:77]
	v_mfma_f32_16x16x32_f16 v[82:85], v[90:93], v[46:49], v[82:85]
	v_min_f32 v90, v99, v230
	v_med3_f32 v91, v101, v110, v96
	v_med3_f32 v92, v97, v101, v96
	v_min_f32 v93, v97, v96
	v_med3_f32 v96, v100, v98, v231
	v_add_u32_e32 v99, 0x18120, v95
	v_med3_f32 v97, v90, v100, v231
	v_min_f32 v90, v90, v231
	v_med3_f32 v110, v92, v91, v234
	v_med3_f32 v111, v93, v92, v234
	s_nop 0
	v_med3_f32 v96, v97, v96, v232
	v_med3_f32 v97, v90, v97, v232
	v_min_f32 v98, v90, v232
	v_add_u32_e32 v90, 0x180e0, v95
	v_mfma_f32_16x16x32_f16 v[78:81], v[170:173], v[14:17], v[78:81]
	v_med3_f32 v167, v98, v97, v233
	v_min_f32 v168, v98, v233
	v_mfma_f32_16x16x32_f16 v[86:89], v[170:173], v[46:49], v[86:89]
	v_mfma_f32_16x16x32_f16 v[74:77], v[118:121], v[10:13], v[74:77]
	v_mfma_f32_16x16x32_f16 v[82:85], v[118:121], v[42:45], v[82:85]
	v_min_f32 v119, v93, v234
	ds_read_b128 v[90:93], v90
	v_med3_f32 v120, v97, v96, v233
	ds_read_b128 v[96:99], v99
	s_nop 4
	v_and_or_b32 v118, v74, v247, s9
	v_and_or_b32 v121, v75, v247, s76
	v_mfma_f32_16x16x32_f16 v[78:81], v[174:177], v[10:13], v[78:81]
	s_waitcnt vmcnt(4)
	s_waitcnt lgkmcnt(0)
	s_barrier
	v_mfma_f32_16x16x32_f16 v[86:89], v[174:177], v[42:45], v[86:89]
	v_and_or_b32 v161, v76, v247, s77
	v_and_or_b32 v166, v77, v247, s78
	s_waitcnt lgkmcnt(1)
	v_mfma_f32_16x16x32_f16 v[74:77], v[102:105], v[38:41], v[90:93]
	v_mfma_f32_16x16x32_f16 v[90:93], v[102:105], v[70:73], v[90:93]
	v_and_or_b32 v104, v82, v247, s9
	v_and_or_b32 v105, v83, v247, s76
	v_med3_f32 v82, v111, v110, v235
	v_med3_f32 v83, v119, v111, v235
	v_and_or_b32 v111, v84, v247, s77
	s_waitcnt lgkmcnt(0)
	v_mfma_f32_16x16x32_f16 v[100:103], v[202:205], v[38:41], v[96:99]
	v_min_f32 v110, v119, v235
	v_med3_f32 v170, v83, v82, v236
	v_mfma_f32_16x16x32_f16 v[96:99], v[202:205], v[70:73], v[96:99]
	v_and_or_b32 v169, v78, v247, s25
	v_and_or_b32 v119, v85, v247, s78
	v_mfma_f32_16x16x32_f16 v[74:77], v[178:181], v[34:37], v[74:77]
	v_med3_f32 v171, v110, v83, v236
	v_min_f32 v110, v110, v236
	v_mfma_f32_16x16x32_f16 v[82:85], v[178:181], v[66:69], v[90:93]
	v_and_b32_e32 v172, 0xfffffc00, v81
	v_and_or_b32 v173, v79, v247, s79
	v_and_or_b32 v174, v80, v247, s80
	v_mfma_f32_16x16x32_f16 v[90:93], v[206:209], v[66:69], v[96:99]
	v_min_f32 v99, v168, v238
	v_mfma_f32_16x16x32_f16 v[78:81], v[206:209], v[34:37], v[100:103]
	s_nop 0
	v_and_or_b32 v97, v86, v247, s25
	v_and_or_b32 v98, v87, v247, s79
	v_med3_f32 v86, v167, v120, v238
	v_med3_f32 v87, v168, v167, v238
	v_med3_f32 v100, v171, v170, v237
	v_med3_f32 v101, v110, v171, v237
	v_min_f32 v102, v110, v237
	v_or3_b32 v96, s9, v172, 19
	v_mfma_f32_16x16x32_f16 v[74:77], v[182:185], v[30:33], v[74:77]
	v_med3_f32 v120, v87, v86, v239
	v_med3_f32 v167, v99, v87, v239
	v_min_f32 v99, v99, v239
	v_mfma_f32_16x16x32_f16 v[82:85], v[182:185], v[62:65], v[82:85]
	v_and_or_b32 v103, v88, v247, s80
	v_and_or_b32 v110, v89, v247, s81
	v_mfma_f32_16x16x32_f16 v[86:89], v[210:213], v[62:65], v[90:93]
	v_med3_f32 v90, v167, v120, v240
	v_med3_f32 v91, v99, v167, v240
	v_min_f32 v92, v99, v240
	v_med3_f32 v93, v101, v100, v118
	v_med3_f32 v99, v102, v101, v118
	v_min_f32 v100, v102, v118
	v_mfma_f32_16x16x32_f16 v[78:81], v[210:213], v[30:33], v[78:81]
	v_med3_f32 v90, v91, v90, v241
	v_med3_f32 v91, v92, v91, v241
	v_min_f32 v92, v92, v241
	v_med3_f32 v93, v99, v93, v121
	v_med3_f32 v99, v100, v99, v121
	v_min_f32 v100, v100, v121
	v_mfma_f32_16x16x32_f16 v[74:77], v[186:189], v[26:29], v[74:77]
	v_med3_f32 v90, v91, v90, v104
	v_med3_f32 v91, v92, v91, v104
	v_min_f32 v92, v92, v104
	v_med3_f32 v93, v99, v93, v161
	v_med3_f32 v99, v100, v99, v161
	v_min_f32 v100, v100, v161
	v_mfma_f32_16x16x32_f16 v[82:85], v[186:189], v[58:61], v[82:85]
	v_med3_f32 v90, v91, v90, v105
	v_med3_f32 v91, v92, v91, v105
	v_min_f32 v92, v92, v105
	v_med3_f32 v93, v99, v93, v166
	v_med3_f32 v99, v100, v99, v166
	v_min_f32 v100, v100, v166
	s_nop 0
	v_med3_f32 v90, v91, v90, v111
	v_med3_f32 v91, v92, v91, v111
	v_min_f32 v92, v92, v111
	v_med3_f32 v93, v99, v93, v169
	v_med3_f32 v99, v100, v99, v169
	v_min_f32 v100, v100, v169
	s_nop 0
	v_med3_f32 v90, v91, v90, v119
	v_med3_f32 v91, v92, v91, v119
	v_min_f32 v92, v92, v119
	v_med3_f32 v93, v99, v93, v173
	v_med3_f32 v99, v100, v99, v173
	v_min_f32 v100, v100, v173
	s_nop 0
	v_med3_f32 v90, v91, v90, v97
	v_med3_f32 v91, v92, v91, v97
	v_min_f32 v92, v92, v97
	v_med3_f32 v93, v99, v93, v174
	v_med3_f32 v99, v100, v99, v174
	v_min_f32 v100, v100, v174
	s_nop 0
	v_med3_f32 v90, v91, v90, v98
	v_med3_f32 v91, v92, v91, v98
	v_min_f32 v92, v92, v98
	v_med3_f32 v104, v99, v93, v96
	v_med3_f32 v105, v100, v99, v96
	v_min_f32 v111, v100, v96
	v_lshl_add_u64 v[96:97], s[6:7], 0, v[122:123]
	v_med3_f32 v100, v91, v90, v103
	v_med3_f32 v101, v92, v91, v103
	v_min_f32 v102, v92, v103
	v_lshl_add_u64 v[90:91], s[4:5], 0, v[122:123]
	v_lshl_add_u64 v[92:93], s[4:5], 0, v[106:107]
	v_readfirstlane_b32 s5, v113
	v_lshl_add_u64 v[98:99], s[6:7], 0, v[106:107]
	v_mfma_f32_16x16x32_f16 v[78:81], v[214:217], v[26:29], v[78:81]
	s_mov_b32 m0, s8
	s_nop 0
	global_load_lds_dwordx4 v[90:91], off
	s_add_i32 s6, s5, 0x400
	s_mov_b32 m0, s40
	s_nop 0
	global_load_lds_dwordx4 v[92:93], off
	v_mfma_f32_16x16x32_f16 v[86:89], v[214:217], v[58:61], v[86:89]
	s_mov_b32 m0, s5
	s_nop 0
	global_load_lds_dwordx4 v[96:97], off
	v_med3_f32 v161, v101, v100, v110
	v_med3_f32 v230, v102, v101, v110
	v_mfma_f32_16x16x32_f16 v[74:77], v[190:193], v[22:25], v[74:77]
	s_mov_b32 m0, s6
	s_nop 0
	global_load_lds_dwordx4 v[98:99], off
	ds_read_b128 v[90:93], v144 offset:32768
	v_min_f32 v110, v102, v110
	v_mfma_f32_16x16x32_f16 v[82:85], v[190:193], v[54:57], v[82:85]
	ds_read_b128 v[166:169], v143 offset:41216
	ds_read_b128 v[170:173], v142 offset:41216
	ds_read_b128 v[174:177], v141 offset:41216
	v_mfma_f32_16x16x32_f16 v[78:81], v[114:117], v[22:25], v[78:81]
	ds_read_b128 v[202:205], v144 offset:57344
	ds_read_b128 v[178:181], v143 offset:49152
	ds_read_b128 v[182:185], v142 offset:49152
	v_mfma_f32_16x16x32_f16 v[86:89], v[114:117], v[54:57], v[86:89]
	ds_read_b128 v[114:117], v144 offset:40960
	ds_read_b128 v[206:209], v143 offset:57344
	ds_read_b128 v[186:189], v141 offset:49152
	v_mfma_f32_16x16x32_f16 v[74:77], v[194:197], v[18:21], v[74:77]
	ds_read_b128 v[210:213], v142 offset:57344
	ds_read_b128 v[190:193], v144 offset:49408
	ds_read_b128 v[214:217], v141 offset:57344
	v_mfma_f32_16x16x32_f16 v[82:85], v[194:197], v[50:53], v[82:85]
	ds_read_b128 v[194:197], v143 offset:49408
	s_add_u32 s4, s0, 0xc000
	s_addc_u32 s5, s1, 0
	v_mfma_f32_16x16x32_f16 v[78:81], v[218:221], v[18:21], v[78:81]
	v_mfma_f32_16x16x32_f16 v[86:89], v[218:221], v[50:53], v[86:89]
	ds_read_b128 v[218:221], v143 offset:57600
	v_mfma_f32_16x16x32_f16 v[74:77], v[162:165], v[14:17], v[74:77]
	v_mfma_f32_16x16x32_f16 v[82:85], v[162:165], v[46:49], v[82:85]
	ds_read_b128 v[162:165], v144 offset:41216
	v_mfma_f32_16x16x32_f16 v[78:81], v[222:225], v[14:17], v[78:81]
	v_mfma_f32_16x16x32_f16 v[86:89], v[222:225], v[46:49], v[86:89]
	ds_read_b128 v[222:225], v142 offset:57600
	v_mfma_f32_16x16x32_f16 v[74:77], v[198:201], v[10:13], v[74:77]
	v_mfma_f32_16x16x32_f16 v[82:85], v[198:201], v[42:45], v[82:85]
	ds_read_b128 v[198:201], v141 offset:49408
	v_mfma_f32_16x16x32_f16 v[78:81], v[226:229], v[10:13], v[78:81]
	v_mfma_f32_16x16x32_f16 v[86:89], v[226:229], v[42:45], v[86:89]
	v_add_u32_e32 v100, 0x18160, v95
	ds_read_b128 v[96:99], v100
	s_nop 1
	v_add_u32_e32 v118, 0x181a0, v95
	v_and_or_b32 v231, v74, v247, s35
	s_waitcnt lgkmcnt(0)
	v_mfma_f32_16x16x32_f16 v[100:103], v[90:93], v[38:41], v[96:99]
	ds_read_b128 v[118:121], v118
	v_med3_f32 v104, v105, v104, v231
	v_med3_f32 v105, v111, v105, v231
	v_mfma_f32_16x16x32_f16 v[90:93], v[90:93], v[70:73], v[96:99]
	v_and_or_b32 v232, v75, v247, s82
	ds_read_b128 v[96:99], v143 offset:32768
	v_and_or_b32 v233, v76, v247, s83
	v_and_or_b32 v234, v77, v247, s84
	s_waitcnt lgkmcnt(1)
	v_mfma_f32_16x16x32_f16 v[74:77], v[114:117], v[38:41], v[118:121]
	v_min_f32 v111, v111, v231
	v_med3_f32 v104, v105, v104, v232
	ds_read_b128 v[226:229], v141 offset:57600
	v_mfma_f32_16x16x32_f16 v[114:117], v[114:117], v[70:73], v[118:121]
	v_and_or_b32 v235, v82, v247, s35
	v_and_or_b32 v236, v83, v247, s82
	s_waitcnt lgkmcnt(1)
	v_mfma_f32_16x16x32_f16 v[100:103], v[96:99], v[34:37], v[100:103]
	ds_read_b128 v[118:121], v143 offset:40960
	v_med3_f32 v105, v111, v105, v232
	v_min_f32 v111, v111, v232
	v_mfma_f32_16x16x32_f16 v[90:93], v[96:99], v[66:69], v[90:93]
	v_and_or_b32 v237, v84, v247, s83
	v_and_or_b32 v238, v85, v247, s84
	ds_read_b128 v[82:85], v142 offset:32768
	v_and_or_b32 v239, v78, v247, s41
	s_waitcnt lgkmcnt(1)
	v_mfma_f32_16x16x32_f16 v[74:77], v[118:121], v[34:37], v[74:77]
	v_med3_f32 v104, v105, v104, v233
	v_med3_f32 v105, v111, v105, v233
	v_min_f32 v111, v111, v233
	v_mfma_f32_16x16x32_f16 v[96:99], v[118:121], v[66:69], v[114:117]
	v_and_or_b32 v240, v79, v247, s85
	v_and_or_b32 v242, v81, v247, s87
	v_and_or_b32 v241, v80, v247, s86
	s_waitcnt lgkmcnt(0)
	v_mfma_f32_16x16x32_f16 v[78:81], v[82:85], v[30:33], v[100:103]
	ds_read_b128 v[118:121], v141 offset:33024
	v_med3_f32 v104, v105, v104, v234
	v_med3_f32 v105, v111, v105, v234
	v_mfma_f32_16x16x32_f16 v[82:85], v[82:85], v[62:65], v[90:93]
	ds_read_b128 v[100:103], v142 offset:40960
	ds_read_b128 v[90:93], v141 offset:32768
	v_and_or_b32 v243, v86, v247, s41
	v_and_or_b32 v244, v87, v247, s85
	s_waitcnt lgkmcnt(1)
	v_mfma_f32_16x16x32_f16 v[74:77], v[100:103], v[30:33], v[74:77]
	ds_read_b128 v[114:117], v143 offset:33024
	v_min_f32 v111, v111, v234
	v_mfma_f32_16x16x32_f16 v[96:99], v[100:103], v[62:65], v[96:99]
	v_and_or_b32 v245, v88, v247, s86
	v_and_or_b32 v246, v89, v247, s87
	ds_read_b128 v[86:89], v141 offset:40960
	ds_read_b128 v[100:103], v144 offset:33024
	s_waitcnt lgkmcnt(3)
	v_mfma_f32_16x16x32_f16 v[78:81], v[90:93], v[26:29], v[78:81]
	v_mfma_f32_16x16x32_f16 v[82:85], v[90:93], v[58:61], v[82:85]
	ds_read_b128 v[90:93], v142 offset:33024
	s_waitcnt lgkmcnt(2)
	v_mfma_f32_16x16x32_f16 v[74:77], v[86:89], v[26:29], v[74:77]
	v_mfma_f32_16x16x32_f16 v[86:89], v[86:89], v[58:61], v[96:99]
	s_waitcnt lgkmcnt(1)
	v_mfma_f32_16x16x32_f16 v[78:81], v[100:103], v[22:25], v[78:81]
	s_nop 0
	ds_read_b128 v[96:99], v144 offset:49152
	v_mfma_f32_16x16x32_f16 v[82:85], v[100:103], v[54:57], v[82:85]
	ds_read_b128 v[100:103], v142 offset:49408
	v_mfma_f32_16x16x32_f16 v[74:77], v[162:165], v[22:25], v[74:77]
	v_mfma_f32_16x16x32_f16 v[86:89], v[162:165], v[54:57], v[86:89]
	ds_read_b128 v[162:165], v144 offset:57600
	v_mfma_f32_16x16x32_f16 v[78:81], v[114:117], v[18:21], v[78:81]
	v_mfma_f32_16x16x32_f16 v[82:85], v[114:117], v[50:53], v[82:85]
	v_med3_f32 v114, v230, v161, v235
	v_med3_f32 v115, v110, v230, v235
	v_mfma_f32_16x16x32_f16 v[74:77], v[166:169], v[18:21], v[74:77]
	v_mfma_f32_16x16x32_f16 v[86:89], v[166:169], v[50:53], v[86:89]
	s_waitcnt lgkmcnt(3)
	v_mfma_f32_16x16x32_f16 v[78:81], v[90:93], v[14:17], v[78:81]
	v_mfma_f32_16x16x32_f16 v[82:85], v[90:93], v[46:49], v[82:85]
	v_min_f32 v90, v110, v235
	v_med3_f32 v91, v115, v114, v236
	s_nop 0
	v_med3_f32 v92, v90, v115, v236
	v_min_f32 v90, v90, v236
	s_nop 0
	v_med3_f32 v91, v92, v91, v237
	v_med3_f32 v92, v90, v92, v237
	v_min_f32 v90, v90, v237
	s_nop 0
	v_med3_f32 v110, v92, v91, v238
	v_med3_f32 v161, v90, v92, v238
	v_min_f32 v166, v90, v238
	v_med3_f32 v90, v105, v104, v239
	v_med3_f32 v104, v111, v105, v239
	v_add_u32_e32 v91, 0x181e0, v95
	v_add_u32_e32 v105, 0x18220, v95
	v_mfma_f32_16x16x32_f16 v[74:77], v[170:173], v[14:17], v[74:77]
	ds_read_b128 v[114:117], v105
	v_min_f32 v111, v111, v239
	v_mfma_f32_16x16x32_f16 v[86:89], v[170:173], v[46:49], v[86:89]
	v_mfma_f32_16x16x32_f16 v[78:81], v[118:121], v[10:13], v[78:81]
	v_mfma_f32_16x16x32_f16 v[82:85], v[118:121], v[42:45], v[82:85]
	v_med3_f32 v119, v104, v90, v240
	ds_read_b128 v[90:93], v91
	s_nop 5
	v_and_or_b32 v118, v78, v247, s24
	v_and_or_b32 v120, v79, v247, s70
	v_mfma_f32_16x16x32_f16 v[74:77], v[174:177], v[10:13], v[74:77]
	v_med3_f32 v104, v111, v104, v240
	v_min_f32 v111, v111, v240
	s_waitcnt vmcnt(4)
	v_mfma_f32_16x16x32_f16 v[86:89], v[174:177], v[42:45], v[86:89]
	v_and_or_b32 v121, v80, v247, s71
	v_and_or_b32 v167, v81, v247, s72
	s_waitcnt lgkmcnt(0)
	v_mfma_f32_16x16x32_f16 v[78:81], v[96:99], v[38:41], v[90:93]
	s_waitcnt lgkmcnt(0)
	s_barrier
	v_mfma_f32_16x16x32_f16 v[90:93], v[96:99], v[70:73], v[90:93]
	v_and_or_b32 v105, v82, v247, s24
	v_and_or_b32 v168, v83, v247, s70
	v_med3_f32 v82, v104, v119, v241
	v_med3_f32 v83, v111, v104, v241
	v_min_f32 v104, v111, v241
	v_and_or_b32 v111, v84, v247, s71
	v_mfma_f32_16x16x32_f16 v[96:99], v[202:205], v[38:41], v[114:117]
	v_med3_f32 v170, v83, v82, v242
	v_med3_f32 v171, v104, v83, v242
	v_min_f32 v104, v104, v242
	v_mfma_f32_16x16x32_f16 v[114:117], v[202:205], v[70:73], v[114:117]
	v_and_or_b32 v119, v85, v247, s72
	v_and_or_b32 v169, v74, v247, s34
	v_mfma_f32_16x16x32_f16 v[78:81], v[178:181], v[34:37], v[78:81]
	v_mfma_f32_16x16x32_f16 v[82:85], v[178:181], v[66:69], v[90:93]
	v_and_b32_e32 v172, 0xfffffc00, v77
	v_and_or_b32 v173, v75, v247, s73
	v_and_or_b32 v174, v76, v247, s74
	v_mfma_f32_16x16x32_f16 v[74:77], v[206:209], v[34:37], v[96:99]
	v_med3_f32 v96, v161, v110, v243
	v_med3_f32 v97, v166, v161, v243
	v_min_f32 v98, v166, v243
	v_mfma_f32_16x16x32_f16 v[90:93], v[206:209], v[66:69], v[114:117]
	v_and_or_b32 v110, v86, v247, s34
	s_nop 0
	v_or3_b32 v99, s24, v172, 19
	v_and_or_b32 v114, v87, v247, s73
	v_mfma_f32_16x16x32_f16 v[78:81], v[182:185], v[30:33], v[78:81]
	v_med3_f32 v86, v97, v96, v244
	v_med3_f32 v87, v98, v97, v244
	v_min_f32 v96, v98, v244
	v_mfma_f32_16x16x32_f16 v[82:85], v[182:185], v[62:65], v[82:85]
	v_and_or_b32 v97, v88, v247, s74
	v_and_or_b32 v98, v89, v247, s75
	v_med3_f32 v115, v87, v86, v245
	v_mfma_f32_16x16x32_f16 v[74:77], v[210:213], v[30:33], v[74:77]
	v_med3_f32 v116, v96, v87, v245
	v_min_f32 v96, v96, v245
	v_mfma_f32_16x16x32_f16 v[86:89], v[210:213], v[62:65], v[90:93]
	v_med3_f32 v90, v116, v115, v246
	v_med3_f32 v91, v96, v116, v246
	v_min_f32 v92, v96, v246
	v_mfma_f32_16x16x32_f16 v[78:81], v[186:189], v[26:29], v[78:81]
	v_med3_f32 v93, v171, v170, v118
	v_med3_f32 v90, v91, v90, v105
	v_med3_f32 v91, v92, v91, v105
	v_mfma_f32_16x16x32_f16 v[82:85], v[186:189], v[58:61], v[82:85]
	v_min_f32 v92, v92, v105
	v_med3_f32 v96, v104, v171, v118
	v_med3_f32 v90, v91, v90, v168
	v_mfma_f32_16x16x32_f16 v[74:77], v[214:217], v[26:29], v[74:77]
	v_med3_f32 v93, v96, v93, v120
	v_med3_f32 v91, v92, v91, v168
	v_min_f32 v92, v92, v168
	v_mfma_f32_16x16x32_f16 v[86:89], v[214:217], v[58:61], v[86:89]
	v_min_f32 v104, v104, v118
	v_med3_f32 v90, v91, v90, v111
	v_med3_f32 v91, v92, v91, v111
	v_mfma_f32_16x16x32_f16 v[78:81], v[190:193], v[22:25], v[78:81]
	v_med3_f32 v96, v104, v96, v120
	v_min_f32 v92, v92, v111
	v_min_f32 v104, v104, v120
	v_mfma_f32_16x16x32_f16 v[82:85], v[190:193], v[54:57], v[82:85]
	v_med3_f32 v93, v96, v93, v121
	v_med3_f32 v96, v104, v96, v121
	v_med3_f32 v90, v91, v90, v119
	v_mfma_f32_16x16x32_f16 v[74:77], v[162:165], v[22:25], v[74:77]
	v_med3_f32 v93, v96, v93, v167
	v_med3_f32 v91, v92, v91, v119
	v_min_f32 v92, v92, v119
	v_mfma_f32_16x16x32_f16 v[86:89], v[162:165], v[54:57], v[86:89]
	v_min_f32 v104, v104, v121
	v_med3_f32 v90, v91, v90, v110
	v_med3_f32 v91, v92, v91, v110
	v_mfma_f32_16x16x32_f16 v[78:81], v[194:197], v[18:21], v[78:81]
	v_med3_f32 v96, v104, v96, v167
	v_min_f32 v92, v92, v110
	v_min_f32 v104, v104, v167
	v_mfma_f32_16x16x32_f16 v[82:85], v[194:197], v[50:53], v[82:85]
	v_med3_f32 v93, v96, v93, v169
	v_med3_f32 v96, v104, v96, v169
	v_med3_f32 v90, v91, v90, v114
	v_mfma_f32_16x16x32_f16 v[74:77], v[218:221], v[18:21], v[74:77]
	v_med3_f32 v93, v96, v93, v173
	v_med3_f32 v91, v92, v91, v114
	v_min_f32 v92, v92, v114
	v_mfma_f32_16x16x32_f16 v[86:89], v[218:221], v[50:53], v[86:89]
	v_min_f32 v104, v104, v169
	v_med3_f32 v90, v91, v90, v97
	v_med3_f32 v91, v92, v91, v97
	v_mfma_f32_16x16x32_f16 v[78:81], v[100:103], v[14:17], v[78:81]
	v_med3_f32 v96, v104, v96, v173
	v_min_f32 v92, v92, v97
	v_min_f32 v104, v104, v173
	v_mfma_f32_16x16x32_f16 v[82:85], v[100:103], v[46:49], v[82:85]
	v_med3_f32 v93, v96, v93, v174
	v_med3_f32 v96, v104, v96, v174
	v_med3_f32 v111, v91, v90, v98
	v_mfma_f32_16x16x32_f16 v[74:77], v[222:225], v[14:17], v[74:77]
	v_med3_f32 v105, v96, v93, v99
	v_med3_f32 v161, v92, v91, v98
	v_min_f32 v230, v92, v98
	v_mfma_f32_16x16x32_f16 v[86:89], v[222:225], v[46:49], v[86:89]
	v_min_f32 v104, v104, v174
	v_mfma_f32_16x16x32_f16 v[78:81], v[198:201], v[10:13], v[78:81]
	v_med3_f32 v110, v104, v96, v99
	v_min_f32 v104, v104, v99
	v_mfma_f32_16x16x32_f16 v[82:85], v[198:201], v[42:45], v[82:85]
	v_readfirstlane_b32 s6, v108
	v_lshl_add_u64 v[90:91], s[4:5], 0, v[122:123]
	v_lshl_add_u64 v[92:93], s[4:5], 0, v[106:107]
	s_add_i32 s4, s6, 0x400
	s_mov_b32 m0, s6
	s_nop 0
	global_load_lds_dwordx4 v[90:91], off
	s_add_u32 s6, s0, 0x10000
	s_mov_b32 m0, s4
	s_nop 0
	global_load_lds_dwordx4 v[92:93], off
	s_addc_u32 s7, s1, 0
	v_readfirstlane_b32 s5, v109
	v_lshl_add_u64 v[90:91], s[6:7], 0, v[122:123]
	s_mov_b32 m0, s5
	s_nop 0
	global_load_lds_dwordx4 v[90:91], off
	s_add_i32 s8, s5, 0x400
	v_mfma_f32_16x16x32_f16 v[74:77], v[226:229], v[10:13], v[74:77]
	s_sub_i32 s9, s23, 48
	s_or_b32 s76, s9, 1
	s_or_b32 s77, s9, 2
	s_or_b32 s78, s9, 3
	s_or_b32 s79, s9, 17
	s_or_b32 s80, s9, 18
	s_or_b32 s81, s9, 19
	s_sub_i32 s24, s23, 32
	s_or_b32 s70, s24, 1
	s_or_b32 s71, s24, 2
	s_or_b32 s72, s24, 3
	s_or_b32 s73, s24, 17
	s_or_b32 s74, s24, 18
	s_or_b32 s75, s24, 19
	s_add_i32 s4, s23, -16
	s_or_b32 s88, s4, 1
	s_or_b32 s89, s4, 2
	s_or_b32 s90, s4, 3
	s_or_b32 s91, s4, 17
	s_or_b32 s92, s4, 18
	s_or_b32 s93, s4, 19
	v_mfma_f32_16x16x32_f16 v[86:89], v[226:229], v[42:45], v[86:89]
	v_lshl_add_u64 v[92:93], s[6:7], 0, v[106:107]
	s_mov_b32 m0, s8
	s_nop 0
	global_load_lds_dwordx4 v[92:93], off
	ds_read_b128 v[90:93], v160
	ds_read_b128 v[114:117], v159
	v_add_u32_e32 v96, 0x18260, v95
	ds_read_b128 v[96:99], v96
	v_add_u32_e32 v118, 0x182a0, v95
	ds_read_b128 v[118:121], v118
	v_and_or_b32 v162, v78, v247, s9
	s_waitcnt lgkmcnt(1)
	v_mfma_f32_16x16x32_f16 v[100:103], v[90:93], v[38:41], v[96:99]
	v_med3_f32 v105, v110, v105, v162
	v_med3_f32 v110, v104, v110, v162
	v_min_f32 v104, v104, v162
	v_mfma_f32_16x16x32_f16 v[90:93], v[90:93], v[70:73], v[96:99]
	v_and_or_b32 v228, v81, v247, s78
	ds_read_b128 v[96:99], v158
	v_and_or_b32 v226, v79, v247, s76
	v_and_or_b32 v227, v80, v247, s77
	s_waitcnt lgkmcnt(1)
	v_mfma_f32_16x16x32_f16 v[78:81], v[114:117], v[38:41], v[118:121]
	ds_read_b128 v[166:169], v155 offset:256
	v_med3_f32 v105, v110, v105, v226
	v_med3_f32 v110, v104, v110, v226
	v_mfma_f32_16x16x32_f16 v[114:117], v[114:117], v[70:73], v[118:121]
	ds_read_b128 v[118:121], v157
	v_and_or_b32 v229, v82, v247, s9
	v_and_or_b32 v231, v83, v247, s76
	s_waitcnt lgkmcnt(2)
	v_mfma_f32_16x16x32_f16 v[100:103], v[96:99], v[34:37], v[100:103]
	ds_read_b128 v[162:165], v157 offset:256
	v_med3_f32 v105, v110, v105, v227
	v_min_f32 v104, v104, v226
	v_mfma_f32_16x16x32_f16 v[90:93], v[96:99], v[66:69], v[90:93]
	v_and_or_b32 v232, v84, v247, s77
	v_and_or_b32 v233, v85, v247, s78
	ds_read_b128 v[82:85], v156
	s_waitcnt lgkmcnt(2)
	v_mfma_f32_16x16x32_f16 v[96:99], v[118:121], v[66:69], v[114:117]
	v_med3_f32 v110, v104, v110, v227
	v_med3_f32 v111, v161, v111, v229
	ds_read_b128 v[170:173], v152
	v_mfma_f32_16x16x32_f16 v[78:81], v[118:121], v[34:37], v[78:81]
	v_and_or_b32 v234, v74, v247, s24
	ds_read_b128 v[114:117], v155
	v_and_or_b32 v235, v75, v247, s79
	v_and_or_b32 v236, v76, v247, s80
	s_waitcnt lgkmcnt(2)
	v_mfma_f32_16x16x32_f16 v[100:103], v[82:85], v[30:33], v[100:103]
	ds_read_b128 v[118:121], v154 offset:256
	v_min_f32 v104, v104, v227
	ds_read_b128 v[198:201], v151
	v_mfma_f32_16x16x32_f16 v[82:85], v[82:85], v[62:65], v[90:93]
	v_and_or_b32 v237, v77, v247, s81
	v_and_or_b32 v238, v86, v247, s24
	s_waitcnt lgkmcnt(2)
	v_mfma_f32_16x16x32_f16 v[74:77], v[114:117], v[30:33], v[78:81]
	ds_read_b128 v[174:177], v150
	ds_read_b128 v[202:205], v149
	ds_read_b128 v[178:181], v148
	ds_read_b128 v[78:81], v154
	v_mfma_f32_16x16x32_f16 v[90:93], v[114:117], v[62:65], v[96:99]
	v_and_or_b32 v239, v87, v247, s79
	v_and_or_b32 v240, v88, v247, s80
	v_and_or_b32 v241, v89, v247, s81
	s_waitcnt lgkmcnt(0)
	v_mfma_f32_16x16x32_f16 v[86:89], v[78:81], v[26:29], v[100:103]
	ds_read_b128 v[96:99], v160 offset:256
	ds_read_b128 v[114:117], v159 offset:256
	s_nop 0
	ds_read_b128 v[100:103], v156 offset:256
	v_mfma_f32_16x16x32_f16 v[78:81], v[78:81], v[58:61], v[82:85]
	ds_read_b128 v[206:209], v147
	ds_read_b128 v[182:185], v146
	ds_read_b128 v[186:189], v152 offset:256
	ds_read_b128 v[82:85], v153
	s_waitcnt lgkmcnt(0)
	v_mfma_f32_16x16x32_f16 v[74:77], v[82:85], v[26:29], v[74:77]
	ds_read_b128 v[210:213], v151 offset:256
	ds_read_b128 v[214:217], v149 offset:256
	ds_read_b128 v[190:193], v148 offset:256
	v_mfma_f32_16x16x32_f16 v[82:85], v[82:85], v[58:61], v[90:93]
	ds_read_b128 v[218:221], v147 offset:256
	ds_read_b128 v[194:197], v146 offset:256
	ds_read_b128 v[222:225], v145 offset:256
	ds_read_b128 v[90:93], v158 offset:256
	v_mfma_f32_16x16x32_f16 v[86:89], v[96:99], v[22:25], v[86:89]
	s_addk_i32 s3, 0x300
	v_mfma_f32_16x16x32_f16 v[78:81], v[96:99], v[54:57], v[78:81]
	ds_read_b128 v[96:99], v153 offset:256
	v_mfma_f32_16x16x32_f16 v[74:77], v[114:117], v[22:25], v[74:77]
	v_mfma_f32_16x16x32_f16 v[82:85], v[114:117], v[54:57], v[82:85]
	ds_read_b128 v[114:117], v150 offset:256
	s_waitcnt lgkmcnt(2)
	v_mfma_f32_16x16x32_f16 v[86:89], v[90:93], v[18:21], v[86:89]
	v_mfma_f32_16x16x32_f16 v[78:81], v[90:93], v[50:53], v[78:81]
	ds_read_b128 v[90:93], v145
	v_mfma_f32_16x16x32_f16 v[74:77], v[162:165], v[18:21], v[74:77]
	v_mfma_f32_16x16x32_f16 v[82:85], v[162:165], v[50:53], v[82:85]
	v_mfma_f32_16x16x32_f16 v[86:89], v[100:103], v[14:17], v[86:89]
	v_mfma_f32_16x16x32_f16 v[78:81], v[100:103], v[46:49], v[78:81]
	v_med3_f32 v100, v230, v161, v229
	v_min_f32 v101, v230, v229
	v_med3_f32 v102, v110, v105, v228
	v_med3_f32 v103, v104, v110, v228
	v_min_f32 v104, v104, v228
	s_nop 0
	v_med3_f32 v105, v100, v111, v231
	v_med3_f32 v100, v101, v100, v231
	v_min_f32 v101, v101, v231
	v_med3_f32 v161, v103, v102, v234
	v_med3_f32 v163, v104, v103, v234
	v_min_f32 v104, v104, v234
	s_nop 0
	v_med3_f32 v105, v100, v105, v232
	v_med3_f32 v110, v101, v100, v232
	v_add_u32_e32 v100, 0x182e0, v95
	v_add_u32_e32 v95, 0x18320, v95
	v_mfma_f32_16x16x32_f16 v[74:77], v[166:169], v[14:17], v[74:77]
	v_min_f32 v111, v101, v232
	ds_read_b128 v[100:103], v100
	v_med3_f32 v161, v163, v161, v235
	v_mfma_f32_16x16x32_f16 v[82:85], v[166:169], v[46:49], v[82:85]
	v_med3_f32 v105, v110, v105, v233
	v_med3_f32 v110, v111, v110, v233
	v_min_f32 v111, v111, v233
	v_mfma_f32_16x16x32_f16 v[86:89], v[118:121], v[10:13], v[86:89]
	v_med3_f32 v163, v104, v163, v235
	v_min_f32 v104, v104, v235
	v_mfma_f32_16x16x32_f16 v[78:81], v[118:121], v[42:45], v[78:81]
	v_med3_f32 v161, v163, v161, v236
	v_med3_f32 v163, v104, v163, v236
	s_nop 6
	v_and_or_b32 v162, v86, v247, s4
	v_and_or_b32 v164, v87, v247, s88
	s_waitcnt lgkmcnt(3)
	v_mfma_f32_16x16x32_f16 v[74:77], v[96:99], v[10:13], v[74:77]
	v_mfma_f32_16x16x32_f16 v[82:85], v[96:99], v[42:45], v[82:85]
	ds_read_b128 v[96:99], v95
	v_and_or_b32 v165, v88, v247, s89
	v_and_or_b32 v166, v89, v247, s90
	s_waitcnt lgkmcnt(1)
	v_mfma_f32_16x16x32_f16 v[86:89], v[170:173], v[38:41], v[100:103]
	s_waitcnt vmcnt(4)
	s_waitcnt lgkmcnt(0)
	s_barrier
	v_mfma_f32_16x16x32_f16 v[100:103], v[170:173], v[70:73], v[100:103]
	v_and_or_b32 v95, v78, v247, s4
	v_and_or_b32 v167, v79, v247, s88
	v_and_or_b32 v168, v80, v247, s89
	s_waitcnt lgkmcnt(0)
	v_mfma_f32_16x16x32_f16 v[118:121], v[198:201], v[38:41], v[96:99]
	v_mfma_f32_16x16x32_f16 v[96:99], v[198:201], v[70:73], v[96:99]
	v_and_or_b32 v169, v81, v247, s90
	v_and_or_b32 v170, v74, v247, s23
	v_mfma_f32_16x16x32_f16 v[78:81], v[174:177], v[34:37], v[86:89]
	v_mfma_f32_16x16x32_f16 v[86:89], v[174:177], v[66:69], v[100:103]
	v_min_f32 v103, v104, v236
	v_med3_f32 v104, v163, v161, v237
	s_nop 1
	v_and_or_b32 v101, v75, v247, s91
	v_and_or_b32 v102, v76, v247, s92
	v_and_or_b32 v100, v77, v247, s93
	v_mfma_f32_16x16x32_f16 v[74:77], v[202:205], v[34:37], v[118:121]
	v_med3_f32 v118, v103, v163, v237
	v_min_f32 v103, v103, v237
	v_mfma_f32_16x16x32_f16 v[96:99], v[202:205], v[66:69], v[96:99]
	v_and_or_b32 v119, v82, v247, s23
	v_and_or_b32 v120, v83, v247, s91
	v_med3_f32 v82, v110, v105, v238
	v_med3_f32 v83, v111, v110, v238
	v_mfma_f32_16x16x32_f16 v[78:81], v[178:181], v[30:33], v[78:81]
	v_min_f32 v110, v111, v238
	v_med3_f32 v111, v83, v82, v239
	s_addk_i32 s23, 0xc0
	v_mfma_f32_16x16x32_f16 v[86:89], v[178:181], v[62:65], v[86:89]
	v_and_or_b32 v105, v84, v247, s92
	v_and_or_b32 v121, v85, v247, s93
	v_med3_f32 v161, v110, v83, v239
	v_mfma_f32_16x16x32_f16 v[74:77], v[206:209], v[30:33], v[74:77]
	s_add_u32 s0, s0, 0x18000
	s_addc_u32 s1, s1, 0
	s_add_i32 s33, s33, 6
	v_mfma_f32_16x16x32_f16 v[82:85], v[206:209], v[62:65], v[96:99]
	v_min_f32 v96, v110, v239
	v_med3_f32 v97, v161, v111, v240
	v_med3_f32 v99, v118, v104, v162
	v_mfma_f32_16x16x32_f16 v[78:81], v[182:185], v[26:29], v[78:81]
	v_med3_f32 v98, v96, v161, v240
	v_min_f32 v96, v96, v240
	v_med3_f32 v104, v103, v118, v162
	v_mfma_f32_16x16x32_f16 v[86:89], v[182:185], v[58:61], v[86:89]
	v_med3_f32 v97, v98, v97, v241
	v_med3_f32 v98, v96, v98, v241
	v_min_f32 v96, v96, v241
	v_mfma_f32_16x16x32_f16 v[74:77], v[90:93], v[26:29], v[74:77]
	s_cmpk_eq_i32 s3, 0xf00
	v_mfma_f32_16x16x32_f16 v[82:85], v[90:93], v[58:61], v[82:85]
	v_min_f32 v90, v103, v162
	v_med3_f32 v91, v104, v99, v164
	v_med3_f32 v93, v98, v97, v95
	v_mfma_f32_16x16x32_f16 v[78:81], v[186:189], v[22:25], v[78:81]
	v_med3_f32 v92, v90, v104, v164
	v_min_f32 v90, v90, v164
	v_med3_f32 v97, v96, v98, v95
	v_mfma_f32_16x16x32_f16 v[86:89], v[186:189], v[54:57], v[86:89]
	v_med3_f32 v91, v92, v91, v165
	v_med3_f32 v92, v90, v92, v165
	v_min_f32 v90, v90, v165
	v_mfma_f32_16x16x32_f16 v[74:77], v[210:213], v[22:25], v[74:77]
	v_min_f32 v95, v96, v95
	v_med3_f32 v91, v92, v91, v166
	v_med3_f32 v93, v97, v93, v167
	v_mfma_f32_16x16x32_f16 v[82:85], v[210:213], v[54:57], v[82:85]
	v_med3_f32 v96, v95, v97, v167
	v_med3_f32 v92, v90, v92, v166
	v_min_f32 v90, v90, v166
	v_mfma_f32_16x16x32_f16 v[78:81], v[114:117], v[18:21], v[78:81]
	v_min_f32 v95, v95, v167
	v_med3_f32 v93, v96, v93, v168
	v_med3_f32 v91, v92, v91, v170
	v_mfma_f32_16x16x32_f16 v[86:89], v[114:117], v[50:53], v[86:89]
	v_med3_f32 v96, v95, v96, v168
	v_min_f32 v95, v95, v168
	v_med3_f32 v92, v90, v92, v170
	v_mfma_f32_16x16x32_f16 v[74:77], v[214:217], v[18:21], v[74:77]
	v_med3_f32 v97, v96, v93, v169
	v_med3_f32 v96, v95, v96, v169
	v_min_f32 v90, v90, v170
	v_mfma_f32_16x16x32_f16 v[82:85], v[214:217], v[50:53], v[82:85]
	v_med3_f32 v91, v92, v91, v101
	v_med3_f32 v98, v90, v92, v101
	v_min_f32 v99, v90, v101
	v_min_f32 v95, v95, v169
	v_mfma_f32_16x16x32_f16 v[78:81], v[190:193], v[14:17], v[78:81]
	v_med3_f32 v101, v98, v91, v102
	v_med3_f32 v103, v95, v96, v119
	v_min_f32 v95, v95, v119
	v_mfma_f32_16x16x32_f16 v[90:93], v[190:193], v[46:49], v[86:89]
	v_med3_f32 v86, v99, v98, v102
	v_min_f32 v87, v99, v102
	v_med3_f32 v102, v96, v97, v119
	v_mfma_f32_16x16x32_f16 v[74:77], v[218:221], v[14:17], v[74:77]
	v_med3_f32 v111, v86, v101, v100
	v_med3_f32 v101, v87, v86, v100
	v_min_f32 v110, v87, v100
	v_mfma_f32_16x16x32_f16 v[96:99], v[218:221], v[46:49], v[82:85]
	v_med3_f32 v100, v103, v102, v120
	v_med3_f32 v102, v95, v103, v120
	v_min_f32 v95, v95, v120
	v_mfma_f32_16x16x32_f16 v[86:89], v[194:197], v[10:13], v[78:81]
	v_mfma_f32_16x16x32_f16 v[82:85], v[194:197], v[42:45], v[90:93]
	v_med3_f32 v90, v102, v100, v105
	v_med3_f32 v91, v95, v102, v105
	v_min_f32 v92, v95, v105
	v_mfma_f32_16x16x32_f16 v[78:81], v[222:225], v[10:13], v[74:77]
	v_med3_f32 v100, v92, v91, v121
	v_mfma_f32_16x16x32_f16 v[74:77], v[222:225], v[42:45], v[96:99]
	v_med3_f32 v98, v91, v90, v121
	v_min_f32 v99, v92, v121
	s_cbranch_scc0 .LBB1_7
	s_add_u32 s0, s26, 0x88000
	v_readfirstlane_b32 s3, v112
	v_and_b32_e32 v90, 16, v0
	s_addc_u32 s1, s27, 0
	s_add_i32 s6, s3, 0x10000
	v_mov_b32_e32 v123, 0
	v_cmp_eq_u32_e64 s[4:5], 0, v90
	v_lshl_add_u64 v[90:91], s[0:1], 0, v[122:123]
	s_mov_b32 m0, s6
	s_nop 0
	global_load_lds_dwordx4 v[90:91], off
	s_add_i32 s6, s3, 0x10400
	v_mov_b32_e32 v107, v123
	v_lshl_add_u64 v[90:91], s[0:1], 0, v[106:107]
	s_add_u32 s0, s26, 0x8c000
	s_mov_b32 m0, s6
	s_nop 0
	global_load_lds_dwordx4 v[90:91], off
	s_addc_u32 s1, s27, 0
	s_add_i32 s6, s3, 0x14000
	v_lshl_add_u64 v[90:91], s[0:1], 0, v[122:123]
	s_mov_b32 m0, s6
	s_nop 0
	global_load_lds_dwordx4 v[90:91], off
	s_add_i32 s3, s3, 0x14400
	v_lshl_add_u64 v[90:91], s[0:1], 0, v[106:107]
	s_mov_b32 m0, s3
	s_nop 0
	global_load_lds_dwordx4 v[90:91], off
	ds_read_b128 v[90:93], v144
	ds_read_b128 v[114:117], v144 offset:8192
	v_add_u32_e32 v161, 0x18060, v94
	ds_read_b128 v[94:97], v161 offset:3840
	ds_read_b128 v[118:121], v161 offset:3904
	ds_read_b128 v[162:165], v143
	s_waitcnt lgkmcnt(2)
	v_mfma_f32_16x16x32_f16 v[102:105], v[90:93], v[38:41], v[94:97]
	ds_read_b128 v[166:169], v142
	ds_read_b128 v[174:177], v142 offset:8192
	ds_read_b128 v[178:181], v144 offset:24576
	v_mfma_f32_16x16x32_f16 v[90:93], v[90:93], v[70:73], v[94:97]
	ds_read_b128 v[182:185], v161 offset:4032
	ds_read_b128 v[186:189], v143 offset:16384
	s_add_u32 s0, s26, 0x90000
	s_waitcnt lgkmcnt(6)
	v_mfma_f32_16x16x32_f16 v[94:97], v[114:117], v[38:41], v[118:121]
	s_addc_u32 s1, s27, 0
	v_cmp_gt_u32_e64 s[6:7], 32, v131
	v_mfma_f32_16x16x32_f16 v[114:117], v[114:117], v[70:73], v[118:121]
	s_nop 2
	ds_read_b128 v[118:121], v143 offset:8192
	s_waitcnt lgkmcnt(6)
	v_mfma_f32_16x16x32_f16 v[102:105], v[162:165], v[34:37], v[102:105]
	v_mfma_f32_16x16x32_f16 v[162:165], v[162:165], v[66:69], v[90:93]
	s_waitcnt lgkmcnt(0)
	v_mfma_f32_16x16x32_f16 v[92:95], v[118:121], v[34:37], v[94:97]
	v_mfma_f32_16x16x32_f16 v[170:173], v[118:121], v[66:69], v[114:117]
	v_and_b32_e32 v78, 0xfffffc00, v78
	v_or_b32_e32 v90, 0x3b0, v78
	v_and_b32_e32 v78, 0xfffffc00, v79
	v_or_b32_e32 v91, 0x3b1, v78
	v_mfma_f32_16x16x32_f16 v[102:105], v[166:169], v[30:33], v[102:105]
	v_mfma_f32_16x16x32_f16 v[162:165], v[166:169], v[62:65], v[162:165]
	v_and_b32_e32 v78, 0xfffffc00, v80
	v_or_b32_e32 v118, 0x3b2, v78
	v_and_b32_e32 v78, 0xfffffc00, v81
	v_or_b32_e32 v115, 0x3b3, v78
	v_and_b32_e32 v74, 0xfffffc00, v74
	v_mfma_f32_16x16x32_f16 v[78:81], v[174:177], v[30:33], v[92:95]
	s_nop 2
	ds_read_b128 v[92:95], v141
	v_mfma_f32_16x16x32_f16 v[166:169], v[174:177], v[62:65], v[170:173]
	v_or_b32_e32 v114, 0x3b0, v74
	v_and_b32_e32 v74, 0xfffffc00, v75
	v_or_b32_e32 v116, 0x3b1, v74
	v_and_b32_e32 v74, 0xfffffc00, v76
	v_or_b32_e32 v117, 0x3b2, v74
	v_and_b32_e32 v96, 0xfffffc00, v77
	v_or_b32_e32 v119, 0x3b3, v96
	s_waitcnt lgkmcnt(0)
	v_mfma_f32_16x16x32_f16 v[74:77], v[92:95], v[26:29], v[102:105]
	ds_read_b128 v[170:173], v144 offset:16384
	ds_read_b128 v[174:177], v161 offset:3968
	v_mfma_f32_16x16x32_f16 v[92:95], v[92:95], v[58:61], v[162:165]
	ds_read_b128 v[102:105], v141 offset:8192
	s_nop 1
	ds_read_b128 v[162:165], v144 offset:256
	s_waitcnt lgkmcnt(1)
	v_mfma_f32_16x16x32_f16 v[78:81], v[102:105], v[26:29], v[78:81]
	v_mfma_f32_16x16x32_f16 v[102:105], v[102:105], v[58:61], v[166:169]
	s_waitcnt lgkmcnt(0)
	v_mfma_f32_16x16x32_f16 v[74:77], v[162:165], v[22:25], v[74:77]
	s_nop 0
	ds_read_b128 v[166:169], v141 offset:8448
	v_mfma_f32_16x16x32_f16 v[92:95], v[162:165], v[54:57], v[92:95]
	ds_read_b128 v[162:165], v144 offset:8448
	s_waitcnt lgkmcnt(0)
	v_mfma_f32_16x16x32_f16 v[78:81], v[162:165], v[22:25], v[78:81]
	v_mfma_f32_16x16x32_f16 v[102:105], v[162:165], v[54:57], v[102:105]
	ds_read_b128 v[162:165], v143 offset:256
	s_waitcnt lgkmcnt(0)
	v_mfma_f32_16x16x32_f16 v[74:77], v[162:165], v[18:21], v[74:77]
	v_mfma_f32_16x16x32_f16 v[92:95], v[162:165], v[50:53], v[92:95]
	ds_read_b128 v[162:165], v143 offset:8448
	s_waitcnt lgkmcnt(0)
	v_mfma_f32_16x16x32_f16 v[78:81], v[162:165], v[18:21], v[78:81]
	v_mfma_f32_16x16x32_f16 v[102:105], v[162:165], v[50:53], v[102:105]
	ds_read_b128 v[162:165], v142 offset:256
	s_waitcnt lgkmcnt(0)
	v_mfma_f32_16x16x32_f16 v[74:77], v[162:165], v[14:17], v[74:77]
	v_mfma_f32_16x16x32_f16 v[92:95], v[162:165], v[46:49], v[92:95]
	ds_read_b128 v[162:165], v142 offset:8448
	s_waitcnt lgkmcnt(0)
	v_mfma_f32_16x16x32_f16 v[78:81], v[162:165], v[14:17], v[78:81]
	v_mfma_f32_16x16x32_f16 v[102:105], v[162:165], v[46:49], v[102:105]
	ds_read_b128 v[162:165], v141 offset:256
	s_waitcnt lgkmcnt(0)
	v_mfma_f32_16x16x32_f16 v[74:77], v[162:165], v[10:13], v[74:77]
	v_mfma_f32_16x16x32_f16 v[92:95], v[162:165], v[42:45], v[92:95]
	s_nop 6
	v_and_b32_e32 v74, 0xfffffc00, v74
	v_or_b32_e32 v120, 0x3c0, v74
	v_and_b32_e32 v74, 0xfffffc00, v75
	v_or_b32_e32 v121, 0x3c1, v74
	v_and_b32_e32 v74, 0xfffffc00, v76
	v_mfma_f32_16x16x32_f16 v[78:81], v[166:169], v[10:13], v[78:81]
	v_mfma_f32_16x16x32_f16 v[102:105], v[166:169], v[42:45], v[102:105]
	v_or_b32_e32 v162, 0x3c2, v74
	v_and_b32_e32 v74, 0xfffffc00, v77
	v_or_b32_e32 v163, 0x3c3, v74
	v_and_b32_e32 v74, 0xfffffc00, v92
	v_or_b32_e32 v166, 0x3c0, v74
	v_mfma_f32_16x16x32_f16 v[74:77], v[170:173], v[38:41], v[174:177]
	v_mfma_f32_16x16x32_f16 v[174:177], v[170:173], v[70:73], v[174:177]
	v_and_b32_e32 v92, 0xfffffc00, v93
	v_or_b32_e32 v168, 0x3c1, v92
	v_and_b32_e32 v92, 0xfffffc00, v94
	v_or_b32_e32 v169, 0x3c2, v92
	v_and_b32_e32 v96, 0xfffffc00, v95
	v_mfma_f32_16x16x32_f16 v[92:95], v[178:181], v[38:41], v[182:185]
	v_mfma_f32_16x16x32_f16 v[178:181], v[178:181], v[70:73], v[182:185]
	v_and_b32_e32 v78, 0xfffffc00, v78
	v_or_b32_e32 v171, 0x3d0, v78
	v_and_b32_e32 v78, 0xfffffc00, v79
	ds_read_b128 v[182:185], v143 offset:24576
	v_or_b32_e32 v170, 0x3c3, v96
	v_or_b32_e32 v172, 0x3d1, v78
	v_mfma_f32_16x16x32_f16 v[74:77], v[186:189], v[34:37], v[74:77]
	v_mfma_f32_16x16x32_f16 v[174:177], v[186:189], v[66:69], v[174:177]
	v_and_b32_e32 v78, 0xfffffc00, v80
	v_or_b32_e32 v173, 0x3d2, v78
	v_and_b32_e32 v78, 0xfffffc00, v81
	v_or_b32_e32 v198, 0x3d3, v78
	v_and_b32_e32 v96, 0xfffffc00, v102
	s_waitcnt lgkmcnt(0)
	v_mfma_f32_16x16x32_f16 v[78:81], v[182:185], v[34:37], v[92:95]
	ds_read_b128 v[186:189], v141 offset:24832
	s_nop 1
	ds_read_b128 v[92:95], v142 offset:16384
	v_mfma_f32_16x16x32_f16 v[178:181], v[182:185], v[66:69], v[178:181]
	v_or_b32_e32 v164, 0x3d0, v96
	v_and_b32_e32 v96, 0xfffffc00, v103
	v_or_b32_e32 v161, 0x3d1, v96
	v_and_b32_e32 v96, 0xfffffc00, v104
	v_or_b32_e32 v165, 0x3d2, v96
	s_waitcnt lgkmcnt(0)
	v_mfma_f32_16x16x32_f16 v[74:77], v[92:95], v[30:33], v[74:77]
	ds_read_b128 v[182:185], v141 offset:16640
	v_mfma_f32_16x16x32_f16 v[92:95], v[92:95], v[62:65], v[174:177]
	v_and_b32_e32 v96, 0xfffffc00, v105
	s_nop 1
	ds_read_b128 v[174:177], v142 offset:24576
	s_waitcnt lgkmcnt(0)
	v_mfma_f32_16x16x32_f16 v[78:81], v[174:177], v[30:33], v[78:81]
	v_mfma_f32_16x16x32_f16 v[102:105], v[174:177], v[62:65], v[178:181]
	ds_read_b128 v[174:177], v141 offset:16384
	s_waitcnt lgkmcnt(0)
	v_mfma_f32_16x16x32_f16 v[74:77], v[174:177], v[26:29], v[74:77]
	ds_read_b128 v[178:181], v142 offset:24832
	v_mfma_f32_16x16x32_f16 v[92:95], v[174:177], v[58:61], v[92:95]
	ds_read_b128 v[174:177], v141 offset:24576
	s_waitcnt lgkmcnt(0)
	v_mfma_f32_16x16x32_f16 v[78:81], v[174:177], v[26:29], v[78:81]
	v_mfma_f32_16x16x32_f16 v[102:105], v[174:177], v[58:61], v[102:105]
	ds_read_b128 v[174:177], v144 offset:16640
	s_waitcnt lgkmcnt(0)
	v_mfma_f32_16x16x32_f16 v[74:77], v[174:177], v[22:25], v[74:77]
	v_mfma_f32_16x16x32_f16 v[92:95], v[174:177], v[54:57], v[92:95]
	ds_read_b128 v[174:177], v144 offset:24832
	s_waitcnt lgkmcnt(0)
	v_mfma_f32_16x16x32_f16 v[78:81], v[174:177], v[22:25], v[78:81]
	v_mfma_f32_16x16x32_f16 v[102:105], v[174:177], v[54:57], v[102:105]
	ds_read_b128 v[174:177], v143 offset:16640
	s_waitcnt lgkmcnt(0)
	v_mfma_f32_16x16x32_f16 v[74:77], v[174:177], v[18:21], v[74:77]
	v_mfma_f32_16x16x32_f16 v[92:95], v[174:177], v[50:53], v[92:95]
	ds_read_b128 v[174:177], v143 offset:24832
	s_waitcnt lgkmcnt(0)
	v_mfma_f32_16x16x32_f16 v[78:81], v[174:177], v[18:21], v[78:81]
	v_mfma_f32_16x16x32_f16 v[78:81], v[178:181], v[14:17], v[78:81]
	v_mfma_f32_16x16x32_f16 v[78:81], v[186:189], v[10:13], v[78:81]
	v_mfma_f32_16x16x32_f16 v[102:105], v[174:177], v[50:53], v[102:105]
	ds_read_b128 v[174:177], v142 offset:16640
	s_waitcnt vmcnt(4)
	s_waitcnt lgkmcnt(0)
	s_waitcnt lgkmcnt(0)
	v_mfma_f32_16x16x32_f16 v[74:77], v[174:177], v[14:17], v[74:77]
	s_barrier
	s_nop 2
	v_and_b32_e32 v78, 0xfffffc00, v78
	v_or_b32_e32 v78, 0x3f0, v78
	v_mfma_f32_16x16x32_f16 v[92:95], v[174:177], v[46:49], v[92:95]
	v_and_b32_e32 v79, 0xfffffc00, v79
	v_or_b32_e32 v79, 0x3f1, v79
	v_mfma_f32_16x16x32_f16 v[174:177], v[178:181], v[46:49], v[102:105]
	v_mfma_f32_16x16x32_f16 v[102:105], v[182:185], v[10:13], v[74:77]
	v_or_b32_e32 v167, 0x3d3, v96
	v_readfirstlane_b32 s3, v112
	v_lshl_add_u64 v[96:97], s[0:1], 0, v[122:123]
	s_mov_b32 m0, s3
	s_nop 0
	global_load_lds_dwordx4 v[96:97], off
	s_addk_i32 s3, 0x400
	v_lshl_add_u64 v[96:97], s[0:1], 0, v[106:107]
	s_add_u32 s0, s26, 0x94000
	s_mov_b32 m0, s3
	s_nop 0
	global_load_lds_dwordx4 v[96:97], off
	s_addc_u32 s1, s27, 0
	v_readfirstlane_b32 s3, v113
	v_lshl_add_u64 v[74:75], s[0:1], 0, v[122:123]
	s_mov_b32 m0, s3
	s_nop 0
	global_load_lds_dwordx4 v[74:75], off
	s_addk_i32 s3, 0x400
	v_lshl_add_u64 v[74:75], s[0:1], 0, v[106:107]
	s_mov_b32 m0, s3
	s_nop 0
	global_load_lds_dwordx4 v[74:75], off
	v_mfma_f32_16x16x32_f16 v[74:77], v[186:189], v[42:45], v[174:177]
	ds_read_b128 v[190:193], v143 offset:32768
	ds_read_b128 v[194:197], v144 offset:41216
	s_add_u32 s0, s26, 0x98000
	ds_read_b128 v[174:177], v144 offset:32768
	v_mfma_f32_16x16x32_f16 v[94:97], v[182:185], v[42:45], v[92:95]
	ds_read_b128 v[182:185], v144 offset:40960
	v_and_b32_e32 v86, 0xfffffc00, v86
	v_or_b32_e32 v86, 0x3a0, v86
	s_waitcnt lgkmcnt(1)
	v_mfma_f32_16x16x32_f16 v[178:181], v[174:177], v[38:41], 0
	v_med3_f32 v92, v101, v111, v86
	v_med3_f32 v93, v110, v101, v86
	v_min_f32 v86, v110, v86
	v_mfma_f32_16x16x32_f16 v[174:177], v[174:177], v[70:73], 0
	ds_read_b128 v[110:113], v143 offset:33024
	v_and_b32_e32 v87, 0xfffffc00, v87
	v_or_b32_e32 v87, 0x3a1, v87
	v_mfma_f32_16x16x32_f16 v[178:181], v[190:193], v[34:37], v[178:181]
	v_and_b32_e32 v88, 0xfffffc00, v88
	v_and_b32_e32 v89, 0xfffffc00, v89
	v_and_b32_e32 v82, 0xfffffc00, v82
	v_mfma_f32_16x16x32_f16 v[174:177], v[190:193], v[66:69], v[174:177]
	ds_read_b128 v[190:193], v143 offset:40960
	v_or_b32_e32 v88, 0x3a2, v88
	v_or_b32_e32 v89, 0x3a3, v89
	s_waitcnt lgkmcnt(2)
	v_mfma_f32_16x16x32_f16 v[186:189], v[182:185], v[38:41], 0
	v_or_b32_e32 v82, 0x3a0, v82
	v_and_b32_e32 v83, 0xfffffc00, v83
	v_med3_f32 v98, v100, v98, v82
	v_mfma_f32_16x16x32_f16 v[182:185], v[182:185], v[70:73], 0
	v_or_b32_e32 v83, 0x3a1, v83
	v_med3_f32 v92, v93, v92, v87
	v_med3_f32 v93, v86, v93, v87
	s_waitcnt lgkmcnt(0)
	v_mfma_f32_16x16x32_f16 v[186:189], v[190:193], v[34:37], v[186:189]
	v_min_f32 v86, v86, v87
	v_med3_f32 v87, v93, v92, v88
	v_and_b32_e32 v84, 0xfffffc00, v84
	v_mfma_f32_16x16x32_f16 v[182:185], v[190:193], v[66:69], v[182:185]
	ds_read_b128 v[190:193], v142 offset:32768
	v_med3_f32 v92, v86, v93, v88
	v_min_f32 v86, v86, v88
	s_waitcnt lgkmcnt(0)
	v_mfma_f32_16x16x32_f16 v[178:181], v[190:193], v[30:33], v[178:181]
	v_med3_f32 v93, v92, v87, v89
	v_med3_f32 v92, v86, v92, v89
	v_and_b32_e32 v85, 0xfffffc00, v85
	v_mfma_f32_16x16x32_f16 v[174:177], v[190:193], v[62:65], v[174:177]
	ds_read_b128 v[190:193], v142 offset:40960
	v_or_b32_e32 v84, 0x3a2, v84
	v_or_b32_e32 v85, 0x3a3, v85
	s_waitcnt lgkmcnt(0)
	v_mfma_f32_16x16x32_f16 v[186:189], v[190:193], v[30:33], v[186:189]
	s_addc_u32 s1, s27, 0
	v_and_b32_e32 v102, 0xfffffc00, v102
	v_or_b32_e32 v102, 0x3e0, v102
	v_mfma_f32_16x16x32_f16 v[182:185], v[190:193], v[62:65], v[182:185]
	ds_read_b128 v[190:193], v141 offset:32768
	v_and_b32_e32 v103, 0xfffffc00, v103
	v_or_b32_e32 v103, 0x3e1, v103
	s_waitcnt lgkmcnt(0)
	v_mfma_f32_16x16x32_f16 v[178:181], v[190:193], v[26:29], v[178:181]
	v_and_b32_e32 v94, 0xfffffc00, v94
	v_or_b32_e32 v94, 0x3e0, v94
	v_and_b32_e32 v95, 0xfffffc00, v95
	v_mfma_f32_16x16x32_f16 v[174:177], v[190:193], v[58:61], v[174:177]
	ds_read_b128 v[190:193], v141 offset:40960
	v_or_b32_e32 v95, 0x3e1, v95
	v_and_b32_e32 v74, 0xfffffc00, v74
	s_waitcnt lgkmcnt(0)
	v_mfma_f32_16x16x32_f16 v[186:189], v[190:193], v[26:29], v[186:189]
	v_or_b32_e32 v74, 0x3f0, v74
	v_and_b32_e32 v75, 0xfffffc00, v75
	v_or_b32_e32 v75, 0x3f1, v75
	v_mfma_f32_16x16x32_f16 v[182:185], v[190:193], v[58:61], v[182:185]
	ds_read_b128 v[190:193], v144 offset:33024
	s_waitcnt lgkmcnt(0)
	v_mfma_f32_16x16x32_f16 v[178:181], v[190:193], v[22:25], v[178:181]
	v_mfma_f32_16x16x32_f16 v[174:177], v[190:193], v[54:57], v[174:177]
	ds_read_b128 v[190:193], v143 offset:41216
	v_mfma_f32_16x16x32_f16 v[186:189], v[194:197], v[22:25], v[186:189]
	v_mfma_f32_16x16x32_f16 v[182:185], v[194:197], v[54:57], v[182:185]
	v_min_f32 v194, v86, v89
	ds_read_b128 v[86:89], v142 offset:33024
	v_mfma_f32_16x16x32_f16 v[178:181], v[110:113], v[18:21], v[178:181]
	v_mfma_f32_16x16x32_f16 v[110:113], v[110:113], v[50:53], v[174:177]
	s_waitcnt lgkmcnt(1)
	v_mfma_f32_16x16x32_f16 v[174:177], v[190:193], v[18:21], v[186:189]
	v_med3_f32 v186, v99, v100, v82
	v_min_f32 v82, v99, v82
	s_nop 0
	v_med3_f32 v187, v186, v98, v83
	v_mfma_f32_16x16x32_f16 v[98:101], v[190:193], v[50:53], v[182:185]
	v_med3_f32 v186, v82, v186, v83
	v_min_f32 v82, v82, v83
	s_nop 0
	v_med3_f32 v83, v186, v187, v84
	v_med3_f32 v186, v82, v186, v84
	s_nop 1
	ds_read_b128 v[182:185], v142 offset:41216
	v_min_f32 v82, v82, v84
	v_med3_f32 v190, v186, v83, v85
	s_waitcnt lgkmcnt(0)
	v_mfma_f32_16x16x32_f16 v[174:177], v[182:185], v[14:17], v[174:177]
	v_med3_f32 v191, v82, v186, v85
	ds_read_b128 v[186:189], v141 offset:33024
	v_min_f32 v192, v82, v85
	v_mfma_f32_16x16x32_f16 v[82:85], v[182:185], v[46:49], v[98:101]
	ds_read_b128 v[182:185], v141 offset:41216
	v_mfma_f32_16x16x32_f16 v[178:181], v[86:89], v[14:17], v[178:181]
	v_mfma_f32_16x16x32_f16 v[110:113], v[86:89], v[46:49], v[110:113]
	v_med3_f32 v86, v92, v93, v90
	v_med3_f32 v92, v194, v92, v90
	v_min_f32 v90, v194, v90
	s_waitcnt lgkmcnt(0)
	v_mfma_f32_16x16x32_f16 v[82:85], v[182:185], v[42:45], v[82:85]
	v_med3_f32 v93, v92, v86, v91
	v_med3_f32 v98, v90, v92, v91
	v_min_f32 v99, v90, v91
	v_mfma_f32_16x16x32_f16 v[86:89], v[186:189], v[10:13], v[178:181]
	v_med3_f32 v178, v98, v93, v118
	v_med3_f32 v179, v99, v98, v118
	v_min_f32 v118, v99, v118
	v_mfma_f32_16x16x32_f16 v[90:93], v[186:189], v[42:45], v[110:113]
	v_med3_f32 v193, v179, v178, v115
	v_med3_f32 v194, v118, v179, v115
	v_min_f32 v118, v118, v115
	v_mfma_f32_16x16x32_f16 v[98:101], v[182:185], v[10:13], v[174:177]
	v_med3_f32 v115, v191, v190, v114
	s_nop 2
	ds_read_b128 v[110:113], v143 offset:49152
	v_med3_f32 v182, v192, v191, v114
	v_min_f32 v114, v192, v114
	s_waitcnt lgkmcnt(0)
	v_mfma_f32_16x16x32_f16 v[178:181], v[110:113], v[34:37], 0
	ds_read_b128 v[174:177], v143 offset:57344
	v_med3_f32 v115, v182, v115, v116
	v_med3_f32 v190, v114, v182, v116
	ds_read_b128 v[182:185], v142 offset:49152
	v_min_f32 v114, v114, v116
	v_med3_f32 v115, v190, v115, v117
	v_mfma_f32_16x16x32_f16 v[110:113], v[110:113], v[66:69], 0
	v_med3_f32 v190, v114, v190, v117
	v_min_f32 v191, v114, v117
	v_fma_mix_f32 v86, v86, v38, 0 op_sel_hi:[0,1,0]
	s_waitcnt lgkmcnt(1)
	v_mfma_f32_16x16x32_f16 v[186:189], v[174:177], v[34:37], 0
	v_med3_f32 v192, v190, v115, v119
	v_med3_f32 v190, v191, v190, v119
	v_min_f32 v191, v191, v119
	v_mfma_f32_16x16x32_f16 v[114:117], v[174:177], v[66:69], 0
	ds_read_b128 v[174:177], v142 offset:57344
	v_med3_f32 v119, v194, v193, v120
	v_med3_f32 v193, v118, v194, v120
	v_min_f32 v118, v118, v120
	s_waitcnt lgkmcnt(1)
	v_mfma_f32_16x16x32_f16 v[178:181], v[182:185], v[30:33], v[178:181]
	v_med3_f32 v119, v193, v119, v121
	v_med3_f32 v120, v118, v193, v121
	v_min_f32 v118, v118, v121
	v_mfma_f32_16x16x32_f16 v[110:113], v[182:185], v[62:65], v[110:113]
	v_med3_f32 v119, v120, v119, v162
	ds_read_b128 v[182:185], v141 offset:49152
	v_med3_f32 v193, v118, v120, v162
	v_min_f32 v162, v118, v162
	s_waitcnt lgkmcnt(1)
	v_mfma_f32_16x16x32_f16 v[186:189], v[174:177], v[30:33], v[186:189]
	v_med3_f32 v194, v193, v119, v163
	ds_read_b128 v[118:121], v141 offset:57344
	v_med3_f32 v193, v162, v193, v163
	v_mfma_f32_16x16x32_f16 v[114:117], v[174:177], v[62:65], v[114:117]
	v_min_f32 v162, v162, v163
	v_med3_f32 v163, v190, v192, v166
	v_med3_f32 v190, v191, v190, v166
	s_waitcnt lgkmcnt(1)
	v_mfma_f32_16x16x32_f16 v[174:177], v[182:185], v[26:29], v[178:181]
	v_min_f32 v166, v191, v166
	v_med3_f32 v163, v190, v163, v168
	v_fma_mix_f32 v38, v87, v38, v86 op_sel:[0,1,0] op_sel_hi:[0,1,0]
	v_mfma_f32_16x16x32_f16 v[110:113], v[182:185], v[58:61], v[110:113]
	v_fma_mix_f32 v90, v90, v70, 0 op_sel_hi:[0,1,0]
	ds_read_b128 v[178:181], v144 offset:49408
	v_fma_mix_f32 v38, v88, v39, v38 op_sel_hi:[0,1,0]
	s_waitcnt lgkmcnt(1)
	v_mfma_f32_16x16x32_f16 v[182:185], v[118:121], v[26:29], v[186:189]
	v_med3_f32 v186, v166, v190, v168
	v_min_f32 v166, v166, v168
	v_fma_mix_f32 v70, v91, v70, v90 op_sel:[0,1,0] op_sel_hi:[0,1,0]
	v_mfma_f32_16x16x32_f16 v[114:117], v[118:121], v[58:61], v[114:117]
	ds_read_b128 v[118:121], v144 offset:57600
	v_med3_f32 v163, v186, v163, v169
	v_med3_f32 v168, v166, v186, v169
	s_waitcnt lgkmcnt(1)
	v_mfma_f32_16x16x32_f16 v[174:177], v[178:181], v[22:25], v[174:177]
	v_min_f32 v166, v166, v169
	v_med3_f32 v192, v168, v163, v170
	v_med3_f32 v163, v193, v194, v171
	v_mfma_f32_16x16x32_f16 v[110:113], v[178:181], v[54:57], v[110:113]
	ds_read_b128 v[178:181], v143 offset:49408
	v_med3_f32 v195, v166, v168, v170
	v_med3_f32 v168, v162, v193, v171
	s_waitcnt lgkmcnt(1)
	v_mfma_f32_16x16x32_f16 v[182:185], v[118:121], v[22:25], v[182:185]
	v_min_f32 v162, v162, v171
	v_med3_f32 v163, v168, v163, v172
	v_min_f32 v166, v166, v170
	v_mfma_f32_16x16x32_f16 v[114:117], v[118:121], v[54:57], v[114:117]
	ds_read_b128 v[118:121], v143 offset:57600
	v_med3_f32 v186, v162, v168, v172
	v_min_f32 v162, v162, v172
	s_waitcnt lgkmcnt(1)
	v_mfma_f32_16x16x32_f16 v[168:171], v[178:181], v[18:21], v[174:177]
	v_med3_f32 v172, v162, v186, v173
	v_med3_f32 v163, v186, v163, v173
	v_min_f32 v162, v162, v173
	v_mfma_f32_16x16x32_f16 v[110:113], v[178:181], v[50:53], v[110:113]
	v_med3_f32 v193, v172, v163, v198
	v_med3_f32 v194, v162, v172, v198
	s_nop 1
	ds_read_b128 v[172:175], v142 offset:49408
	s_waitcnt lgkmcnt(1)
	v_mfma_f32_16x16x32_f16 v[176:179], v[118:121], v[18:21], v[182:185]
	v_min_f32 v196, v162, v198
	ds_read_b128 v[188:191], v141 offset:57600
	v_lshl_add_u64 v[162:163], s[0:1], 0, v[122:123]
	v_readfirstlane_b32 s3, v108
	ds_read_b128 v[184:187], v142 offset:57600
	ds_read_b128 v[180:183], v141 offset:49408
	s_waitcnt vmcnt(4)
	s_waitcnt lgkmcnt(0)
	s_barrier
	s_mov_b32 m0, s3
	s_nop 0
	global_load_lds_dwordx4 v[162:163], off
	s_addk_i32 s3, 0x400
	v_lshl_add_u64 v[162:163], s[0:1], 0, v[106:107]
	s_add_u32 s0, s26, 0x9c000
	s_mov_b32 m0, s3
	s_nop 0
	global_load_lds_dwordx4 v[162:163], off
	s_addc_u32 s1, s27, 0
	v_lshl_add_u64 v[106:107], s[0:1], 0, v[106:107]
	v_readfirstlane_b32 s3, v109
	v_lshl_add_u64 v[108:109], s[0:1], 0, v[122:123]
	s_mov_b32 m0, s3
	s_nop 0
	global_load_lds_dwordx4 v[108:109], off
	s_addk_i32 s3, 0x400
	s_mov_b32 m0, s3
	s_nop 0
	global_load_lds_dwordx4 v[106:107], off
	v_mfma_f32_16x16x32_f16 v[114:117], v[118:121], v[50:53], v[114:117]
	v_med3_f32 v122, v195, v192, v164
	v_med3_f32 v162, v166, v195, v164
	v_min_f32 v163, v166, v164
	s_waitcnt lgkmcnt(3)
	v_mfma_f32_16x16x32_f16 v[118:121], v[172:175], v[14:17], v[168:171]
	v_med3_f32 v122, v162, v122, v161
	v_med3_f32 v162, v163, v162, v161
	v_min_f32 v161, v163, v161
	s_waitcnt lgkmcnt(1)
	v_mfma_f32_16x16x32_f16 v[168:171], v[184:187], v[14:17], v[176:179]
	v_med3_f32 v122, v162, v122, v165
	v_med3_f32 v166, v161, v162, v165
	v_min_f32 v161, v161, v165
	v_mfma_f32_16x16x32_f16 v[106:109], v[188:191], v[10:13], v[168:171]
	ds_read_b128 v[162:165], v154
	s_nop 0
	ds_read_b128 v[176:179], v156
	v_med3_f32 v122, v166, v122, v167
	v_mfma_f32_16x16x32_f16 v[110:113], v[172:175], v[46:49], v[110:113]
	s_nop 2
	ds_read_b128 v[168:171], v155
	v_fma_mix_f32 v38, v89, v39, v38 op_sel:[0,1,0] op_sel_hi:[0,1,0]
	v_fma_mix_f32 v70, v92, v71, v70 op_sel_hi:[0,1,0]
	v_mfma_f32_16x16x32_f16 v[172:175], v[184:187], v[46:49], v[114:117]
	ds_read_b128 v[184:187], v153
	v_fma_mix_f32 v39, v93, v71, v70 op_sel:[0,1,0] op_sel_hi:[0,1,0]
	v_fma_mix_f32 v38, v98, v40, v38 op_sel_hi:[0,1,0]
	s_waitcnt lgkmcnt(4)
	v_mfma_f32_16x16x32_f16 v[114:117], v[180:183], v[10:13], v[118:121]
	v_fma_mix_f32 v39, v82, v72, v39 op_sel_hi:[0,1,0]
	v_fma_mix_f32 v38, v99, v40, v38 op_sel:[0,1,0] op_sel_hi:[0,1,0]
	v_fma_mix_f32 v39, v83, v72, v39 op_sel:[0,1,0] op_sel_hi:[0,1,0]
	v_mfma_f32_16x16x32_f16 v[118:121], v[180:183], v[42:45], v[110:113]
	v_fma_mix_f32 v38, v100, v41, v38 op_sel_hi:[0,1,0]
	v_fma_mix_f32 v70, v84, v73, v39 op_sel_hi:[0,1,0]
	v_fma_mix_f32 v71, v101, v41, v38 op_sel:[0,1,0] op_sel_hi:[0,1,0]
	v_mfma_f32_16x16x32_f16 v[110:113], v[188:191], v[42:45], v[172:175]
	v_med3_f32 v188, v161, v166, v167
	v_min_f32 v189, v161, v167
	v_med3_f32 v161, v194, v193, v102
	s_waitcnt lgkmcnt(2)
	v_mfma_f32_16x16x32_f16 v[172:175], v[176:179], v[30:33], 0
	v_med3_f32 v190, v196, v194, v102
	v_min_f32 v102, v196, v102
	v_med3_f32 v122, v188, v122, v94
	v_mfma_f32_16x16x32_f16 v[176:179], v[176:179], v[62:65], 0
	v_med3_f32 v161, v190, v161, v103
	v_fma_mix_f32 v70, v85, v73, v70 op_sel:[0,1,0] op_sel_hi:[0,1,0]
	v_fma_mix_f32 v82, v114, v34, v71 op_sel_hi:[0,1,0]
	s_waitcnt lgkmcnt(1)
	v_mfma_f32_16x16x32_f16 v[180:183], v[168:171], v[30:33], 0
	v_fma_mix_f32 v83, v118, v66, v70 op_sel_hi:[0,1,0]
	v_fma_mix_f32 v34, v115, v34, v82 op_sel:[0,1,0] op_sel_hi:[0,1,0]
	v_fma_mix_f32 v66, v119, v66, v83 op_sel:[0,1,0] op_sel_hi:[0,1,0]
	v_mfma_f32_16x16x32_f16 v[166:169], v[168:171], v[62:65], 0
	v_fma_mix_f32 v34, v116, v35, v34 op_sel_hi:[0,1,0]
	v_fma_mix_f32 v66, v120, v67, v66 op_sel_hi:[0,1,0]
	v_fma_mix_f32 v34, v117, v35, v34 op_sel:[0,1,0] op_sel_hi:[0,1,0]
	v_mfma_f32_16x16x32_f16 v[170:173], v[162:165], v[26:29], v[172:175]
	v_fma_mix_f32 v35, v121, v67, v66 op_sel:[0,1,0] op_sel_hi:[0,1,0]
	v_fma_mix_f32 v34, v106, v36, v34 op_sel_hi:[0,1,0]
	v_fma_mix_f32 v35, v110, v68, v35 op_sel_hi:[0,1,0]
	v_mfma_f32_16x16x32_f16 v[162:165], v[162:165], v[58:61], v[176:179]
	v_fma_mix_f32 v34, v107, v36, v34 op_sel:[0,1,0] op_sel_hi:[0,1,0]
	v_fma_mix_f32 v35, v111, v68, v35 op_sel:[0,1,0] op_sel_hi:[0,1,0]
	v_fma_mix_f32 v34, v108, v37, v34 op_sel_hi:[0,1,0]
	ds_read_b128 v[174:177], v160 offset:256
	v_med3_f32 v160, v102, v190, v103
	v_min_f32 v102, v102, v103
	v_and_b32_e32 v103, 0xfffffc00, v104
	s_waitcnt lgkmcnt(1)
	v_mfma_f32_16x16x32_f16 v[178:181], v[184:187], v[26:29], v[180:183]
	v_or_b32_e32 v103, 0x3e2, v103
	v_med3_f32 v161, v160, v161, v103
	v_fma_mix_f32 v35, v112, v69, v35 op_sel_hi:[0,1,0]
	v_mfma_f32_16x16x32_f16 v[166:169], v[184:187], v[58:61], v[166:169]
	ds_read_b128 v[182:185], v159 offset:256
	v_and_b32_e32 v159, 0xfffffc00, v105
	v_med3_f32 v186, v102, v160, v103
	s_waitcnt lgkmcnt(1)
	v_mfma_f32_16x16x32_f16 v[170:173], v[174:177], v[22:25], v[170:173]
	v_min_f32 v187, v102, v103
	v_fma_mix_f32 v34, v109, v37, v34 op_sel:[0,1,0] op_sel_hi:[0,1,0]
	v_fma_mix_f32 v66, v113, v69, v35 op_sel:[0,1,0] op_sel_hi:[0,1,0]
	v_mfma_f32_16x16x32_f16 v[102:105], v[174:177], v[54:57], v[162:165]
	v_or_b32_e32 v174, 0x3e3, v159
	v_med3_f32 v190, v186, v161, v174
	ds_read_b128 v[158:161], v158 offset:256
	s_waitcnt lgkmcnt(1)
	v_mfma_f32_16x16x32_f16 v[162:165], v[182:185], v[22:25], v[178:181]
	v_med3_f32 v178, v187, v186, v174
	v_min_f32 v179, v187, v174
	ds_read_b128 v[174:177], v157 offset:256
	s_waitcnt lgkmcnt(1)
	v_mfma_f32_16x16x32_f16 v[170:173], v[158:161], v[18:21], v[170:173]
	v_med3_f32 v180, v189, v188, v94
	v_min_f32 v94, v189, v94
	v_mfma_f32_16x16x32_f16 v[102:105], v[158:161], v[50:53], v[102:105]
	ds_read_b128 v[156:159], v156 offset:256
	v_med3_f32 v122, v180, v122, v95
	v_med3_f32 v180, v94, v180, v95
	v_mfma_f32_16x16x32_f16 v[166:169], v[182:185], v[54:57], v[166:169]
	v_min_f32 v94, v94, v95
	v_and_b32_e32 v95, 0xfffffc00, v96
	v_or_b32_e32 v95, 0x3e2, v95
	s_waitcnt lgkmcnt(1)
	v_mfma_f32_16x16x32_f16 v[160:163], v[174:177], v[18:21], v[162:165]
	v_med3_f32 v122, v180, v122, v95
	v_mfma_f32_16x16x32_f16 v[164:167], v[174:177], v[50:53], v[166:169]
	ds_read_b128 v[174:177], v155 offset:256
	v_and_b32_e32 v155, 0xfffffc00, v97
	s_waitcnt lgkmcnt(1)
	v_mfma_f32_16x16x32_f16 v[168:171], v[156:159], v[14:17], v[170:173]
	v_med3_f32 v172, v94, v180, v95
	v_min_f32 v173, v94, v95
	v_mfma_f32_16x16x32_f16 v[94:97], v[156:159], v[46:49], v[102:105]
	v_or_b32_e32 v158, 0x3e3, v155
	v_med3_f32 v122, v172, v122, v158
	v_med3_f32 v182, v173, v172, v158
	v_min_f32 v183, v173, v158
	v_med3_f32 v172, v178, v190, v78
	s_nop 1
	ds_read_b128 v[102:105], v154 offset:256
	s_waitcnt lgkmcnt(1)
	v_mfma_f32_16x16x32_f16 v[154:157], v[174:177], v[14:17], v[160:163]
	v_med3_f32 v122, v182, v122, v74
	v_med3_f32 v182, v183, v182, v74
	v_min_f32 v74, v183, v74
	v_mfma_f32_16x16x32_f16 v[158:161], v[174:177], v[46:49], v[164:167]
	v_and_b32_e32 v175, 0xfffffc00, v81
	v_med3_f32 v122, v182, v122, v75
	v_med3_f32 v182, v74, v182, v75
	s_waitcnt lgkmcnt(0)
	v_mfma_f32_16x16x32_f16 v[166:169], v[102:105], v[10:13], v[168:171]
	v_min_f32 v74, v74, v75
	ds_read_b128 v[162:165], v153 offset:256
	v_med3_f32 v153, v179, v178, v78
	v_mfma_f32_16x16x32_f16 v[94:97], v[102:105], v[42:45], v[94:97]
	ds_read_b128 v[102:105], v146
	v_min_f32 v78, v179, v78
	v_med3_f32 v170, v153, v172, v79
	s_waitcnt lgkmcnt(1)
	v_mfma_f32_16x16x32_f16 v[154:157], v[162:165], v[10:13], v[154:157]
	v_med3_f32 v153, v78, v153, v79
	v_min_f32 v78, v78, v79
	v_and_b32_e32 v79, 0xfffffc00, v80
	v_or_b32_e32 v79, 0x3f2, v79
	v_mfma_f32_16x16x32_f16 v[158:161], v[162:165], v[42:45], v[158:161]
	v_med3_f32 v174, v153, v170, v79
	ds_read_b128 v[162:165], v145
	v_med3_f32 v153, v78, v153, v79
	s_waitcnt lgkmcnt(1)
	v_mfma_f32_16x16x32_f16 v[170:173], v[102:105], v[26:29], 0
	v_min_f32 v178, v78, v79
	v_or_b32_e32 v179, 0x3f3, v175
	v_med3_f32 v184, v153, v174, v179
	v_mfma_f32_16x16x32_f16 v[78:81], v[102:105], v[58:61], 0
	ds_read_b128 v[102:105], v152 offset:256
	v_med3_f32 v185, v178, v153, v179
	v_min_f32 v186, v178, v179
	ds_read_b128 v[178:181], v151 offset:256
	s_waitcnt lgkmcnt(2)
	v_mfma_f32_16x16x32_f16 v[174:177], v[162:165], v[26:29], 0
	v_and_b32_e32 v75, 0xfffffc00, v76
	v_or_b32_e32 v75, 0x3f2, v75
	v_med3_f32 v122, v182, v122, v75
	s_waitcnt lgkmcnt(1)
	v_mfma_f32_16x16x32_f16 v[170:173], v[102:105], v[22:25], v[170:173]
	v_fma_mix_f32 v67, v166, v30, v34 op_sel_hi:[0,1,0]
	v_fma_mix_f32 v30, v167, v30, v67 op_sel:[0,1,0] op_sel_hi:[0,1,0]
	v_fma_mix_f32 v30, v168, v31, v30 op_sel_hi:[0,1,0]
	v_mfma_f32_16x16x32_f16 v[78:81], v[102:105], v[54:57], v[78:81]
	ds_read_b128 v[102:105], v150 offset:256
	v_fma_mix_f32 v30, v169, v31, v30 op_sel:[0,1,0] op_sel_hi:[0,1,0]
	v_fma_mix_f32 v30, v154, v32, v30 op_sel_hi:[0,1,0]
	s_waitcnt lgkmcnt(1)
	v_mfma_f32_16x16x32_f16 v[150:153], v[178:181], v[22:25], v[174:177]
	v_fma_mix_f32 v30, v155, v32, v30 op_sel:[0,1,0] op_sel_hi:[0,1,0]
	v_fma_mix_f32 v30, v156, v33, v30 op_sel_hi:[0,1,0]
	s_nop 0
	ds_read_b128 v[174:177], v149 offset:256
	v_mfma_f32_16x16x32_f16 v[162:165], v[162:165], v[58:61], 0
	v_med3_f32 v149, v74, v182, v75
	v_mfma_f32_16x16x32_f16 v[162:165], v[178:181], v[54:57], v[162:165]
	v_min_f32 v178, v74, v75
	v_and_b32_e32 v179, 0xfffffc00, v77
	v_or_b32_e32 v179, 0x3f3, v179
	s_waitcnt lgkmcnt(1)
	v_mfma_f32_16x16x32_f16 v[74:77], v[102:105], v[50:53], v[78:81]
	v_med3_f32 v122, v149, v122, v179
	v_mfma_f32_16x16x32_f16 v[170:173], v[102:105], v[18:21], v[170:173]
	s_nop 1
	ds_read_b128 v[78:81], v148 offset:256
	s_waitcnt lgkmcnt(1)
	v_mfma_f32_16x16x32_f16 v[102:105], v[174:177], v[18:21], v[150:153]
	v_med3_f32 v152, v178, v149, v179
	v_min_f32 v153, v178, v179
	v_mfma_f32_16x16x32_f16 v[148:151], v[174:177], v[50:53], v[162:165]
	s_nop 2
	ds_read_b128 v[162:165], v147 offset:256
	s_waitcnt lgkmcnt(1)
	v_mfma_f32_16x16x32_f16 v[170:173], v[78:81], v[14:17], v[170:173]
	v_mfma_f32_16x16x32_f16 v[74:77], v[78:81], v[46:49], v[74:77]
	ds_read_b128 v[78:81], v146 offset:256
	s_waitcnt lgkmcnt(1)
	v_mfma_f32_16x16x32_f16 v[86:89], v[162:165], v[14:17], v[102:105]
	s_nop 2
	ds_read_b128 v[102:105], v145 offset:256
	s_waitcnt vmcnt(4)
	v_mfma_f32_16x16x32_f16 v[90:93], v[162:165], v[46:49], v[148:151]
	s_waitcnt lgkmcnt(0)
	s_barrier
	ds_read_b128 v[82:85], v144 offset:8448
	s_waitcnt lgkmcnt(2)
	v_mfma_f32_16x16x32_f16 v[38:41], v[78:81], v[42:45], v[74:77]
	s_nop 2
	ds_read_b128 v[74:77], v144 offset:256
	s_waitcnt lgkmcnt(2)
	v_mfma_f32_16x16x32_f16 v[70:73], v[102:105], v[42:45], v[90:93]
	s_nop 2
	ds_read_b128 v[90:93], v143 offset:256
	v_mfma_f32_16x16x32_f16 v[146:149], v[78:81], v[10:13], v[170:173]
	v_mfma_f32_16x16x32_f16 v[78:81], v[102:105], v[10:13], v[86:89]
	ds_read_b128 v[102:105], v143 offset:8448
	s_waitcnt lgkmcnt(2)
	v_mfma_f32_16x16x32_f16 v[86:89], v[74:77], v[22:25], 0
	v_mfma_f32_16x16x32_f16 v[74:77], v[74:77], v[54:57], 0
	s_waitcnt lgkmcnt(1)
	v_mfma_f32_16x16x32_f16 v[86:89], v[90:93], v[18:21], v[86:89]
	v_mfma_f32_16x16x32_f16 v[34:37], v[90:93], v[50:53], v[74:77]
	v_fma_mix_f32 v90, v94, v62, v66 op_sel_hi:[0,1,0]
	ds_read_b128 v[66:69], v142 offset:256
	v_fma_mix_f32 v62, v95, v62, v90 op_sel:[0,1,0] op_sel_hi:[0,1,0]
	ds_read_b128 v[90:93], v142 offset:8448
	v_mfma_f32_16x16x32_f16 v[98:101], v[82:85], v[22:25], 0
	v_fma_mix_f32 v62, v96, v63, v62 op_sel_hi:[0,1,0]
	v_fma_mix_f32 v31, v97, v63, v62 op_sel:[0,1,0] op_sel_hi:[0,1,0]
	v_fma_mix_f32 v31, v158, v64, v31 op_sel_hi:[0,1,0]
	v_mfma_f32_16x16x32_f16 v[82:85], v[82:85], v[54:57], 0
	v_fma_mix_f32 v31, v159, v64, v31 op_sel:[0,1,0] op_sel_hi:[0,1,0]
	v_fma_mix_f32 v31, v160, v65, v31 op_sel_hi:[0,1,0]
	v_fma_mix_f32 v62, v157, v33, v30 op_sel:[0,1,0] op_sel_hi:[0,1,0]
	s_waitcnt lgkmcnt(1)
	v_mfma_f32_16x16x32_f16 v[86:89], v[66:69], v[14:17], v[86:89]
	v_fma_mix_f32 v63, v161, v65, v31 op_sel:[0,1,0] op_sel_hi:[0,1,0]
	v_fma_mix_f32 v38, v38, v58, v63 op_sel_hi:[0,1,0]
	v_fma_mix_f32 v38, v39, v58, v38 op_sel:[0,1,0] op_sel_hi:[0,1,0]
	v_mfma_f32_16x16x32_f16 v[34:37], v[66:69], v[46:49], v[34:37]
	ds_read_b128 v[66:69], v141 offset:256
	v_fma_mix_f32 v38, v40, v59, v38 op_sel_hi:[0,1,0]
	v_mfma_f32_16x16x32_f16 v[74:77], v[102:105], v[18:21], v[98:101]
	v_mfma_f32_16x16x32_f16 v[82:85], v[102:105], v[50:53], v[82:85]
	s_waitcnt lgkmcnt(1)
	v_mfma_f32_16x16x32_f16 v[74:77], v[90:93], v[14:17], v[74:77]
	v_mfma_f32_16x16x32_f16 v[30:33], v[90:93], v[46:49], v[82:85]
	v_fma_mix_f32 v90, v146, v26, v62 op_sel_hi:[0,1,0]
	v_fma_mix_f32 v26, v147, v26, v90 op_sel:[0,1,0] op_sel_hi:[0,1,0]
	v_fma_mix_f32 v26, v148, v27, v26 op_sel_hi:[0,1,0]
	v_fma_mix_f32 v26, v149, v27, v26 op_sel:[0,1,0] op_sel_hi:[0,1,0]
	ds_read_b128 v[62:65], v141 offset:8448
	s_waitcnt lgkmcnt(1)
	v_mfma_f32_16x16x32_f16 v[82:85], v[66:69], v[10:13], v[86:89]
	v_fma_mix_f32 v27, v41, v59, v38 op_sel:[0,1,0] op_sel_hi:[0,1,0]
	v_fma_mix_f32 v26, v78, v28, v26 op_sel_hi:[0,1,0]
	v_fma_mix_f32 v27, v70, v60, v27 op_sel_hi:[0,1,0]
	v_mfma_f32_16x16x32_f16 v[34:37], v[66:69], v[42:45], v[34:37]
	ds_read_b128 v[66:69], v143 offset:16640
	v_fma_mix_f32 v26, v79, v28, v26 op_sel:[0,1,0] op_sel_hi:[0,1,0]
	v_fma_mix_f32 v27, v71, v60, v27 op_sel:[0,1,0] op_sel_hi:[0,1,0]
	v_fma_mix_f32 v26, v80, v29, v26 op_sel_hi:[0,1,0]
	v_fma_mix_f32 v58, v72, v61, v27 op_sel_hi:[0,1,0]
	v_fma_mix_f32 v59, v81, v29, v26 op_sel:[0,1,0] op_sel_hi:[0,1,0]
	v_fma_mix_f32 v70, v73, v61, v58 op_sel:[0,1,0] op_sel_hi:[0,1,0]
	v_fma_mix_f32 v71, v82, v22, v59 op_sel_hi:[0,1,0]
	ds_read_b128 v[58:61], v142 offset:16640
	v_fma_mix_f32 v34, v34, v54, v70 op_sel_hi:[0,1,0]
	v_fma_mix_f32 v22, v83, v22, v71 op_sel:[0,1,0] op_sel_hi:[0,1,0]
	v_fma_mix_f32 v34, v35, v54, v34 op_sel:[0,1,0] op_sel_hi:[0,1,0]
	v_fma_mix_f32 v22, v84, v23, v22 op_sel_hi:[0,1,0]
	v_fma_mix_f32 v34, v36, v55, v34 op_sel_hi:[0,1,0]
	ds_read_b128 v[38:41], v143 offset:24832
	v_fma_mix_f32 v22, v85, v23, v22 op_sel:[0,1,0] op_sel_hi:[0,1,0]
	v_fma_mix_f32 v23, v37, v55, v34 op_sel:[0,1,0] op_sel_hi:[0,1,0]
	ds_read_b128 v[34:37], v141 offset:16640
	s_waitcnt lgkmcnt(4)
	v_mfma_f32_16x16x32_f16 v[74:77], v[62:65], v[10:13], v[74:77]
	ds_read_b128 v[70:73], v142 offset:24832
	v_mfma_f32_16x16x32_f16 v[30:33], v[62:65], v[42:45], v[30:33]
	s_waitcnt lgkmcnt(4)
	v_mfma_f32_16x16x32_f16 v[62:65], v[66:69], v[18:21], 0
	s_nop 3
	v_fma_mix_f32 v22, v74, v24, v22 op_sel_hi:[0,1,0]
	s_nop 0
	v_fma_mix_f32 v23, v30, v56, v23 op_sel_hi:[0,1,0]
	v_fma_mix_f32 v22, v75, v24, v22 op_sel:[0,1,0] op_sel_hi:[0,1,0]
	v_mfma_f32_16x16x32_f16 v[26:29], v[66:69], v[50:53], 0
	v_fma_mix_f32 v23, v31, v56, v23 op_sel:[0,1,0] op_sel_hi:[0,1,0]
	v_fma_mix_f32 v22, v76, v25, v22 op_sel_hi:[0,1,0]
	v_fma_mix_f32 v23, v32, v57, v23 op_sel_hi:[0,1,0]
	s_waitcnt lgkmcnt(3)
	v_mfma_f32_16x16x32_f16 v[62:65], v[58:61], v[14:17], v[62:65]
	v_fma_mix_f32 v30, v77, v25, v22 op_sel:[0,1,0] op_sel_hi:[0,1,0]
	v_fma_mix_f32 v31, v33, v57, v23 op_sel:[0,1,0] op_sel_hi:[0,1,0]
	ds_read_b128 v[22:25], v141 offset:24832
	v_mfma_f32_16x16x32_f16 v[26:29], v[58:61], v[46:49], v[26:29]
	s_waitcnt vmcnt(0)
	s_waitcnt lgkmcnt(0)
	s_barrier
	s_waitcnt lgkmcnt(3)
	v_mfma_f32_16x16x32_f16 v[66:69], v[38:41], v[18:21], 0
	v_mfma_f32_16x16x32_f16 v[38:41], v[38:41], v[50:53], 0
	s_waitcnt lgkmcnt(2)
	v_mfma_f32_16x16x32_f16 v[62:65], v[34:37], v[10:13], v[62:65]
	v_mfma_f32_16x16x32_f16 v[26:29], v[34:37], v[42:45], v[26:29]
	ds_read_b128 v[34:37], v142 offset:33024
	s_nop 5
	v_fma_mix_f32 v54, v62, v18, v30 op_sel_hi:[0,1,0]
	v_fma_mix_f32 v18, v63, v18, v54 op_sel:[0,1,0] op_sel_hi:[0,1,0]
	s_waitcnt lgkmcnt(2)
	v_mfma_f32_16x16x32_f16 v[58:61], v[70:73], v[14:17], v[66:69]
	v_fma_mix_f32 v18, v64, v19, v18 op_sel_hi:[0,1,0]
	v_fma_mix_f32 v26, v26, v50, v31 op_sel_hi:[0,1,0]
	v_fma_mix_f32 v26, v27, v50, v26 op_sel:[0,1,0] op_sel_hi:[0,1,0]
	v_mfma_f32_16x16x32_f16 v[30:33], v[70:73], v[46:49], v[38:41]
	v_fma_mix_f32 v26, v28, v51, v26 op_sel_hi:[0,1,0]
	v_fma_mix_f32 v18, v65, v19, v18 op_sel:[0,1,0] op_sel_hi:[0,1,0]
	v_fma_mix_f32 v19, v29, v51, v26 op_sel:[0,1,0] op_sel_hi:[0,1,0]
	s_waitcnt lgkmcnt(1)
	v_mfma_f32_16x16x32_f16 v[38:41], v[22:25], v[10:13], v[58:61]
	ds_read_b128 v[26:29], v141 offset:33024
	v_mfma_f32_16x16x32_f16 v[22:25], v[22:25], v[42:45], v[30:33]
	s_nop 2
	ds_read_b128 v[30:33], v142 offset:41216
	s_waitcnt lgkmcnt(2)
	v_mfma_f32_16x16x32_f16 v[54:57], v[34:37], v[14:17], 0
	s_nop 1
	v_fma_mix_f32 v19, v22, v52, v19 op_sel_hi:[0,1,0]
	v_fma_mix_f32 v19, v23, v52, v19 op_sel:[0,1,0] op_sel_hi:[0,1,0]
	v_fma_mix_f32 v18, v38, v20, v18 op_sel_hi:[0,1,0]
	v_mfma_f32_16x16x32_f16 v[34:37], v[34:37], v[46:49], 0
	v_fma_mix_f32 v22, v24, v53, v19 op_sel_hi:[0,1,0]
	v_fma_mix_f32 v18, v39, v20, v18 op_sel:[0,1,0] op_sel_hi:[0,1,0]
	v_fma_mix_f32 v39, v25, v53, v22 op_sel:[0,1,0] op_sel_hi:[0,1,0]
	ds_read_b128 v[22:25], v141 offset:41216
	v_fma_mix_f32 v18, v40, v21, v18 op_sel_hi:[0,1,0]
	v_fma_mix_f32 v38, v41, v21, v18 op_sel:[0,1,0] op_sel_hi:[0,1,0]
	s_waitcnt lgkmcnt(2)
	v_mfma_f32_16x16x32_f16 v[18:21], v[26:29], v[10:13], v[54:57]
	v_mfma_f32_16x16x32_f16 v[26:29], v[26:29], v[42:45], v[34:37]
	s_waitcnt lgkmcnt(1)
	v_mfma_f32_16x16x32_f16 v[58:61], v[30:33], v[14:17], 0
	s_nop 4
	v_fma_mix_f32 v18, v18, v14, v38 op_sel_hi:[0,1,0]
	v_fma_mix_f32 v26, v26, v46, v39 op_sel_hi:[0,1,0]
	v_fma_mix_f32 v14, v19, v14, v18 op_sel:[0,1,0] op_sel_hi:[0,1,0]
	v_mfma_f32_16x16x32_f16 v[30:33], v[30:33], v[46:49], 0
	v_fma_mix_f32 v18, v27, v46, v26 op_sel:[0,1,0] op_sel_hi:[0,1,0]
	v_fma_mix_f32 v14, v20, v15, v14 op_sel_hi:[0,1,0]
	v_fma_mix_f32 v26, v28, v47, v18 op_sel_hi:[0,1,0]
	v_fma_mix_f32 v14, v21, v15, v14 op_sel:[0,1,0] op_sel_hi:[0,1,0]
	s_waitcnt lgkmcnt(0)
	v_mfma_f32_16x16x32_f16 v[18:21], v[22:25], v[10:13], v[58:61]
	v_fma_mix_f32 v15, v29, v47, v26 op_sel:[0,1,0] op_sel_hi:[0,1,0]
	ds_read_b128 v[26:29], v141 offset:49408
	v_mfma_f32_16x16x32_f16 v[22:25], v[22:25], v[42:45], v[30:33]
	s_nop 4
	v_fma_mix_f32 v14, v18, v16, v14 op_sel_hi:[0,1,0]
	s_nop 1
	v_fma_mix_f32 v15, v22, v48, v15 op_sel_hi:[0,1,0]
	v_fma_mix_f32 v14, v19, v16, v14 op_sel:[0,1,0] op_sel_hi:[0,1,0]
	v_fma_mix_f32 v15, v23, v48, v15 op_sel:[0,1,0] op_sel_hi:[0,1,0]
	v_fma_mix_f32 v14, v20, v17, v14 op_sel_hi:[0,1,0]
	v_fma_mix_f32 v18, v24, v49, v15 op_sel_hi:[0,1,0]
	v_fma_mix_f32 v22, v21, v17, v14 op_sel:[0,1,0] op_sel_hi:[0,1,0]
	v_fma_mix_f32 v30, v25, v49, v18 op_sel:[0,1,0] op_sel_hi:[0,1,0]
	ds_read_b128 v[18:21], v141 offset:57600
	s_waitcnt lgkmcnt(1)
	v_mfma_f32_16x16x32_f16 v[14:17], v[26:29], v[10:13], 0
	s_nop 7
	v_fma_mix_f32 v14, v14, v10, v22 op_sel_hi:[0,1,0]
	v_mfma_f32_16x16x32_f16 v[22:25], v[26:29], v[42:45], 0
	v_fma_mix_f32 v14, v15, v10, v14 op_sel:[0,1,0] op_sel_hi:[0,1,0]
	v_fma_mix_f32 v14, v16, v11, v14 op_sel_hi:[0,1,0]
	s_waitcnt lgkmcnt(0)
	v_mfma_f32_16x16x32_f16 v[26:29], v[18:21], v[10:13], 0
	v_fma_mix_f32 v10, v17, v11, v14 op_sel:[0,1,0] op_sel_hi:[0,1,0]
	s_nop 2
	v_fma_mix_f32 v22, v22, v42, v30 op_sel_hi:[0,1,0]
	v_fma_mix_f32 v15, v23, v42, v22 op_sel:[0,1,0] op_sel_hi:[0,1,0]
	v_fma_mix_f32 v15, v24, v43, v15 op_sel_hi:[0,1,0]
	v_fma_mix_f32 v11, v25, v43, v15 op_sel:[0,1,0] op_sel_hi:[0,1,0]
	v_fma_mix_f32 v10, v26, v12, v10 op_sel_hi:[0,1,0]
	v_mfma_f32_16x16x32_f16 v[14:17], v[18:21], v[42:45], 0
	v_fma_mix_f32 v10, v27, v12, v10 op_sel:[0,1,0] op_sel_hi:[0,1,0]
	v_fma_mix_f32 v10, v28, v13, v10 op_sel_hi:[0,1,0]
	v_lshlrev_b32_e32 v12, 2, v125
	v_fma_mix_f32 v10, v29, v13, v10 op_sel:[0,1,0] op_sel_hi:[0,1,0]
	v_or_b32_e32 v13, v12, v186
	v_mov_b32_e32 v18, v13
	v_mov_b32_e32 v19, v13
	s_nop 0
	v_fma_mix_f32 v11, v14, v44, v11 op_sel_hi:[0,1,0]
	v_or_b32_e32 v14, v12, v185
	v_permlane16_swap_b32_e32 v18, v19
	v_cndmask_b32_e64 v18, v18, v19, s[4:5]
	v_mov_b32_e32 v19, v14
	v_mov_b32_e32 v20, v14
	v_fma_mix_f32 v11, v15, v44, v11 op_sel:[0,1,0] op_sel_hi:[0,1,0]
	v_or_b32_e32 v15, v12, v184
	v_permlane16_swap_b32_e32 v19, v20
	v_cndmask_b32_e64 v19, v19, v20, s[4:5]
	v_mov_b32_e32 v20, v15
	v_mov_b32_e32 v21, v15
	v_fma_mix_f32 v11, v16, v45, v11 op_sel_hi:[0,1,0]
	v_or_b32_e32 v16, v12, v153
	v_permlane16_swap_b32_e32 v20, v21
	v_cndmask_b32_e64 v20, v20, v21, s[4:5]
	v_mov_b32_e32 v21, v16
	v_mov_b32_e32 v22, v16
	v_fma_mix_f32 v11, v17, v45, v11 op_sel:[0,1,0] op_sel_hi:[0,1,0]
	v_or_b32_e32 v17, v12, v152
	v_permlane16_swap_b32_e32 v21, v22
	v_cndmask_b32_e64 v21, v21, v22, s[4:5]
	v_mov_b32_e32 v22, v17
	v_mov_b32_e32 v23, v17
	v_med3_f32 v15, v14, v15, v18
	v_med3_f32 v14, v13, v14, v18
	v_or_b32_e32 v12, v12, v122
	s_nop 0
	v_permlane16_swap_b32_e32 v22, v23
	v_min_f32 v13, v13, v18
	v_med3_f32 v15, v14, v15, v19
	v_cndmask_b32_e64 v22, v22, v23, s[4:5]
	v_med3_f32 v14, v13, v14, v19
	v_mov_b32_e32 v23, v12
	v_mov_b32_e32 v24, v12
	v_min_f32 v13, v13, v19
	v_med3_f32 v18, v14, v15, v20
	v_med3_f32 v12, v17, v12, v21
	s_nop 1
	v_permlane16_swap_b32_e32 v23, v24
	v_med3_f32 v19, v13, v14, v20
	v_med3_f32 v14, v16, v17, v21
	v_min_f32 v15, v16, v21
	v_cndmask_b32_e64 v23, v23, v24, s[4:5]
	v_med3_f32 v12, v14, v12, v22
	v_med3_f32 v14, v15, v14, v22
	v_min_f32 v15, v15, v22
	v_min_f32 v13, v13, v20
	v_mov_b32_e32 v20, v19
	v_med3_f32 v12, v14, v12, v23
	v_med3_f32 v16, v15, v14, v23
	v_mov_b32_e32 v14, v10
	s_nop 1
	v_permlane16_swap_b32_e32 v10, v14
	v_add_f32_e32 v14, v10, v14
	v_mov_b32_e32 v10, v11
	s_nop 1
	v_permlane16_swap_b32_e32 v11, v10
	v_min_f32 v17, v15, v23
	v_add_f32_e32 v15, v11, v10
	v_mov_b32_e32 v10, v13
	v_mov_b32_e32 v11, v13
	s_nop 1
	v_permlane32_swap_b32_e32 v10, v11
	v_cndmask_b32_e64 v10, v10, v11, s[6:7]
	v_mov_b32_e32 v11, v19
	s_nop 1
	v_permlane32_swap_b32_e32 v11, v20
	v_cndmask_b32_e64 v11, v11, v20, s[6:7]
	v_mov_b32_e32 v20, v18
	v_mov_b32_e32 v21, v18
	s_nop 1
	v_permlane32_swap_b32_e32 v20, v21
	v_cndmask_b32_e64 v20, v20, v21, s[6:7]
	v_mov_b32_e32 v21, v17
	v_mov_b32_e32 v22, v17
	s_nop 1
	v_permlane32_swap_b32_e32 v21, v22
	v_cndmask_b32_e64 v21, v21, v22, s[6:7]
	v_mov_b32_e32 v22, v16
	v_mov_b32_e32 v23, v16
	v_med3_f32 v18, v19, v18, v10
	s_nop 1
	v_permlane32_swap_b32_e32 v22, v23
	v_med3_f32 v19, v13, v19, v10
	v_min_f32 v10, v13, v10
	v_cndmask_b32_e64 v22, v22, v23, s[6:7]
	v_med3_f32 v13, v19, v18, v11
	v_med3_f32 v18, v10, v19, v11
	v_min_f32 v11, v10, v11
	v_mov_b32_e32 v23, v12
	v_mov_b32_e32 v24, v12
	v_med3_f32 v10, v18, v13, v20
	v_med3_f32 v13, v11, v18, v20
	v_min_f32 v19, v11, v20
	v_med3_f32 v11, v16, v12, v21
	v_med3_f32 v12, v17, v16, v21
	s_nop 1
	v_permlane32_swap_b32_e32 v23, v24
	v_min_f32 v16, v17, v21
	v_med3_f32 v11, v12, v11, v22
	v_cndmask_b32_e64 v23, v23, v24, s[6:7]
	v_med3_f32 v12, v16, v12, v22
	v_min_f32 v17, v16, v22
	v_mov_b32_e32 v18, v15
	v_med3_f32 v11, v12, v11, v23
	v_med3_f32 v16, v17, v12, v23
	v_min_f32 v12, v17, v23
	v_mov_b32_e32 v17, v14
	s_nop 1
	v_permlane32_swap_b32_e32 v14, v17
	v_permlane32_swap_b32_e32 v15, v18
	v_cndmask_b32_e64 v12, v12, v19, s[4:5]
	s_and_saveexec_b64 s[0:1], s[6:7]
	s_cbranch_execz .LBB1_10
	s_load_dword s3, s[12:13], 0x0
	v_add_f32_e32 v19, v137, v138
	v_add_f32_e32 v20, v139, v140
	v_add_f32_e32 v14, v14, v17
	v_add_f32_e32 v15, v15, v18
	v_cndmask_b32_e64 v19, v20, v19, s[4:5]
	v_cndmask_b32_e64 v14, v15, v14, s[4:5]
	v_fmac_f32_e32 v14, 2.0, v19
	s_waitcnt lgkmcnt(0)
	v_add_f32_e32 v14, s3, v14
	v_add_f32_e32 v14, v132, v14
	v_add_f32_e32 v123, v12, v14

	.amdhsa_kernel _Z6k_mainPKfS0_S0_PKDF16_S0_S0_S0_S0_S0_S0_PfP15HIP_vector_typeIiLj4EEPiS3_
		.amdhsa_group_segment_fixed_size 105056
		.amdhsa_private_segment_fixed_size 0
		.amdhsa_kernarg_size 112
		.amdhsa_user_sgpr_count 2
		.amdhsa_user_sgpr_dispatch_ptr 0
		.amdhsa_user_sgpr_queue_ptr 0
		.amdhsa_user_sgpr_kernarg_segment_ptr 1
		.amdhsa_user_sgpr_dispatch_id 0
		.amdhsa_user_sgpr_kernarg_preload_length 0
		.amdhsa_user_sgpr_kernarg_preload_offset 0
		.amdhsa_user_sgpr_private_segment_size 0
		.amdhsa_uses_dynamic_stack 0
		.amdhsa_enable_private_segment 0
		.amdhsa_system_sgpr_workgroup_id_x 1
		.amdhsa_system_sgpr_workgroup_id_y 0
		.amdhsa_system_sgpr_workgroup_id_z 0
		.amdhsa_system_sgpr_workgroup_info 0
		.amdhsa_system_vgpr_workitem_id 0
		.amdhsa_next_free_vgpr 248
		.amdhsa_next_free_sgpr 97
		.amdhsa_accum_offset 248
		.amdhsa_reserve_vcc 1
		.amdhsa_float_round_mode_32 0
		.amdhsa_float_round_mode_16_64 0
		.amdhsa_float_denorm_mode_32 3
		.amdhsa_float_denorm_mode_16_64 3
		.amdhsa_dx10_clamp 1
		.amdhsa_ieee_mode 1
		.amdhsa_fp16_overflow 0
		.amdhsa_tg_split 0
		.amdhsa_exception_fp_ieee_invalid_op 0
		.amdhsa_exception_fp_denorm_src 0
		.amdhsa_exception_fp_ieee_div_zero 0
		.amdhsa_exception_fp_ieee_overflow 0
		.amdhsa_exception_fp_ieee_underflow 0
		.amdhsa_exception_fp_ieee_inexact 0
		.amdhsa_exception_int_div_zero 0
	.end_amdhsa_kernel
